# static s_setprio 1 for waves 0-3 in all GEMM phases, all per-segment priority flips deleted
# speedup vs baseline: 1.0054x; 1.0038x over previous
; #define PG8_WAIT_V(n) asm volatile("s_waitcnt vmcnt(" #n ")" ::: "memory")
; #define PG8_BAR __builtin_amdgcn_s_barrier()
; template <class Epi, class Sched, bool ALIGN_EPI = false, bool SP2 = false>
; __device__ __forceinline__ void gemm_phase(PG8_LAS unsigned char* lds, const Gemm g, const Sched& S, const Epi& E) {
;     int tid_l = threadIdx.x; asm volatile("" : "+v"(tid_l));
;     const int tid = tid_l, wid = __builtin_amdgcn_readfirstlane(tid >> 6), lane = tid & 63, wr = wid >> 2, wc = wid & 3, fr = lane & 15, fq = lane >> 4;
;     const int K = g.K, nt = K / BK;
;     unsigned voffA, voffB;
;     { int R, C; stage_rc(tid * 16, R, C); const int Rb = Epi::PERM ? ((R & ~31) + perm32(R & 31)) : R;
;         voffA = (unsigned)(R * g.lda + C) * 2u; voffB = (unsigned)(Rb * g.ldb + C) * 2u; }
;     const size_t voffA_step = (size_t)64 * g.lda * 2, voffB_step = (size_t)64 * g.ldb * 2;
;     const size_t kstep = (size_t)(BK * 2);
;     const size_t hstepA = (size_t)HALF * g.lda * 2, hstepB = (size_t)HALF * g.ldb * 2;
;     const size_t tstepA = 2 * hstepA, tstepB = 2 * hstepB;
;     const unsigned ldsw = (unsigned)wid * 1024u;
;     const int aoff = lds_byte(wr * 64 + fr, fq * 8), boff = lds_byte(wc * 32 + fr, fq * 8);
;     ...
;     Unit cur, nxt; int ui = 0;
;     if (!S.next(0, cur)) return;
;     f32x4 acc[2][2][4][2];
;     if constexpr (!SP2) {
; #pragma unroll
;     for (int a = 0; a < 2; ++a)
; #pragma unroll
;         for (int b = 0; b < 2; ++b)
; #pragma unroll
;             for (int m = 0; m < 4; ++m)
; #pragma unroll
;                 for (int n = 0; n < 2; ++n) acc[a][b][m][n] = (f32x4){0.f, 0.f, 0.f, 0.f};
;     }
;     bf16x8 At[4][2], B0[2][2], B1[2][2];
;     const char* cA = (const char*)S.opA(g, cur) + (size_t)cur.pm * tstepA; const char* cB = (const char*)S.opB(g, cur) + (size_t)cur.pn * tstepB;
;     S.a_ready(cur);
;     if constexpr (SP2) {
;         PG8_STAGE(PG8_SB(0, 0), cB, voffB); PG8_STAGE(PG8_SB(0, 1), cB + hstepB, voffB); PG8_STAGE(PG8_SA(0, 0), cA, voffA); PG8_STAGE(PG8_SA(0, 1), cA + hstepA, voffA);
;         if (wr == 1) PG8_BAR;
;         PG8_WAIT_V(2); PG8_BAR;
;         PG8_STAGE(PG8_SB(1, 0), cB + kstep, voffB); PG8_STAGE(PG8_SA(1, 0), cA + kstep, voffA); PG8_STAGE(PG8_SB(1, 1), cB + hstepB + kstep, voffB);
;         if (Epi::NST > 0) PG8_WAIT_V(0); else PG8_WAIT_V(6);
;         PG8_BAR;
;     } else {
.LBB0_119:
	v_readlane_b32 s2, v255, 47
	v_readlane_b32 s3, v255, 48
	s_mul_i32 s14, s2, 0x300000
	v_readlane_b32 s2, v254, 0
	v_mov_b32_e32 v3, v212
	v_readlane_b32 s3, v254, 1
	s_andn2_b64 vcc, exec, s[2:3]
	v_readfirstlane_b32 s2, v3
	s_cbranch_vccnz .LBB0_157
	v_bfe_i32 v5, v3, 27, 1
	v_lshlrev_b32_e32 v4, 4, v3
	v_lshrrev_b32_e32 v5, 22, v5
	v_add_u32_e32 v5, v4, v5
	v_and_b32_e32 v5, 0xfffffc00, v5
	v_sub_u32_e32 v4, v4, v5
	v_lshrrev_b32_e32 v5, 4, v4
	v_ashrrev_i32_e32 v6, 31, v3
	v_bitop3_b32 v4, v5, v4, 32 bitop3:0x6c
	v_lshrrev_b32_e32 v6, 26, v6
	v_ashrrev_i32_e32 v5, 31, v4
	v_add_u32_e32 v6, v3, v6
	v_lshrrev_b32_e32 v5, 26, v5
	v_ashrrev_i32_e32 v9, 6, v6
	v_add_u32_e32 v5, v4, v5
	v_lshlrev_b32_e32 v6, 3, v9
	v_ashrrev_i32_e32 v8, 6, v5
	v_and_b32_e32 v6, -16, v6
	v_add_u32_e32 v6, v8, v6
	v_and_b32_e32 v7, 3, v8
	s_mov_b32 s0, 0xfffe0
	v_lshrrev_b32_e32 v10, 2, v6
	v_lshlrev_b32_e32 v11, 1, v6
	v_and_b32_e32 v5, 0xc0, v5
	v_readlane_b32 s6, v255, 21
	v_and_or_b32 v7, v6, s0, v7
	v_and_b32_e32 v10, 4, v10
	v_and_b32_e32 v11, 24, v11
	v_sub_u32_e32 v4, v4, v5
	v_mov_b32_e32 v5, 1
	v_readlane_b32 s7, v255, 22
	s_add_u32 s34, s6, s4
	v_or3_b32 v7, v7, v10, v11
	v_lshlrev_b32_e32 v10, 5, v9
	v_ashrrev_i16_sdwa v4, v5, sext(v4) dst_sel:DWORD dst_unused:UNUSED_PAD src0_sel:DWORD src1_sel:BYTE_0
	s_addc_u32 s35, s7, s5
	s_ashr_i32 s4, s2, 6
	v_and_b32_e32 v10, 32, v10
	v_bfe_i32 v11, v4, 0, 16
	s_ashr_i32 s3, s2, 8
	s_cmp_eq_u32 s3, 0
	s_cbranch_scc0 .Lsp_gu
	s_setprio 1
.Lsp_gu:
	s_lshl_b32 s36, s4, 10
	v_add_u32_e32 v4, v10, v11
	v_readlane_b32 s6, v254, 9
	v_lshlrev_b32_e32 v5, 1, v4
	s_movk_i32 s0, 0x840
	v_readlane_b32 s7, v254, 10
	s_add_u32 s28, s34, s6
	v_lshl_add_u32 v132, v7, 12, v5
	v_mul_lo_u32 v5, v6, s0
	s_addc_u32 s29, s35, s7
	v_mov_b32_e32 v133, v2
	s_add_i32 s37, s36, 0
	v_add_lshl_u32 v134, v4, v5, 1
	v_lshl_add_u64 v[4:5], s[28:29], 0, v[132:133]
	s_add_i32 m0, s37, 0x10000
	v_lshl_add_u64 v[6:7], v[4:5], 0, s[90:91]
	global_load_lds_dwordx4 v132, s[28:29]
	s_add_i32 m0, s37, 0x12000
	s_mov_b64 s[6:7], 0x80000
	global_load_lds_dwordx4 v[6:7], off
	v_lshl_add_u64 v[6:7], v[4:5], 0, s[6:7]
	s_add_i32 m0, s37, 0x14000
	s_mov_b64 s[6:7], 0xc0000
	global_load_lds_dwordx4 v[6:7], off
	v_lshl_add_u64 v[6:7], v[4:5], 0, s[6:7]
	s_add_i32 m0, s37, 0x16000
	v_readlane_b32 s6, v254, 14
	global_load_lds_dwordx4 v[6:7], off
	v_mov_b32_e32 v135, v2
	v_readlane_b32 s7, v254, 15
	s_mov_b32 m0, s37
	s_add_i32 s38, s37, 0x2000
	v_lshl_add_u64 v[6:7], s[6:7], 0, v[134:135]
	s_waitcnt lgkmcnt(0)
	v_lshl_add_u64 v[12:13], v[6:7], 0, s[96:97]
	s_add_i32 s39, s37, 0x4000
	global_load_lds_dwordx4 v134, s[6:7]
	v_readlane_b32 s6, v254, 16
	s_mov_b32 m0, s38
	v_readlane_b32 s7, v254, 17
	global_load_lds_dwordx4 v[12:13], off
	s_nop 0
	v_lshl_add_u64 v[12:13], s[6:7], 0, v[134:135]
	s_mov_b32 m0, s39
	s_add_i32 s40, s37, 0x6000
	global_load_lds_dwordx4 v134, s[6:7]
	v_lshl_add_u64 v[12:13], v[12:13], 0, s[96:97]
	s_mov_b32 m0, s40
	s_cmp_eq_u32 s3, 1
	global_load_lds_dwordx4 v[12:13], off
	s_cselect_b64 s[18:19], -1, 0
	s_cmp_lg_u32 s3, 1
	s_mov_b64 s[10:11], 0x80080
	s_mov_b64 s[20:21], 0xc0080
	s_cbranch_scc1 .LBB0_122
	s_barrier

;     __device__ bool next(int i, Unit& u) const { const int rounds = nwg / G; if (i >= rounds) return false; return StaticOrder::next(rounds - 1 - i, u); }
;     __device__ bool next(int i, Unit& u) const { const int rounds = nwg / G; if (i >= 2 * rounds) return false; const bool ok = StaticOrder::next(i >= rounds ? i - rounds : i, u); u.z = (i >= rounds) ? 1 : 0; return ok; }
; template <class Epi, class Sched, bool ALIGN_EPI = false, bool SP2 = false>
; __device__ __forceinline__ void gemm_phase(PG8_LAS unsigned char* lds, const Gemm g, const Sched& S, const Epi& E) {
;     ...
;         const bool has_next = S.next(ui + 1, nxt);
;         const char* nA = has_next ? (const char*)S.opA(g, nxt) + (size_t)nxt.pm * tstepA : cA; const char* nB = has_next ? (const char*)S.opB(g, nxt) + (size_t)nxt.pn * tstepB : cB;
.LBB0_129:
	s_ashr_i32 s23, s22, 31
	s_lshl_b64 s[4:5], s[22:23], 20
	s_add_u32 s26, s34, s4
	s_addc_u32 s27, s35, s5
	s_add_i32 s45, 0, 0x10000
	s_add_i32 s47, 0, 0x14000
	v_add_u32_e32 v140, s45, v160
	v_add_u32_e32 v141, s47, v160
	ds_read_b128 v[4:7], v140
	ds_read_b128 v[8:11], v140 offset:1024
	ds_read_b128 v[12:15], v140 offset:2048
	ds_read_b128 v[16:19], v140 offset:3072
	ds_read_b128 v[20:23], v141
	ds_read_b128 v[24:27], v141 offset:1024
	ds_read_b128 v[28:31], v141 offset:2048
	ds_read_b128 v[32:35], v141 offset:3072
	s_and_b64 s[4:5], s[10:11], exec
	s_cselect_b32 s4, s27, s29
	s_cselect_b32 s5, s26, s28
	v_lshl_add_u64 v[184:185], s[30:31], 0, v[134:135]
	s_mov_b64 s[10:11], 0x84080
	s_add_i32 s23, s37, 0xc000
	s_waitcnt vmcnt(0)
	v_lshl_add_u64 v[68:69], v[184:185], 0, s[10:11]
	s_mov_b32 m0, s23
	s_mov_b64 s[10:11], 0xc6080
	s_add_i32 s33, s37, 0xe000
	ds_read_b128 v[36:39], v163
	ds_read_b128 v[40:43], v163 offset:1024
	ds_read_b128 v[44:47], v163 offset:2048
	ds_read_b128 v[48:51], v163 offset:3072
	ds_read_b128 v[52:55], v163 offset:4096
	ds_read_b128 v[56:59], v163 offset:5120
	ds_read_b128 v[60:63], v163 offset:6144
	ds_read_b128 v[64:67], v163 offset:7168
	global_load_lds_dwordx4 v[68:69], off
	v_lshl_add_u64 v[68:69], v[184:185], 0, s[10:11]
	s_mov_b32 m0, s33
	s_nop 0
	global_load_lds_dwordx4 v[68:69], off
	s_waitcnt vmcnt(16)
	s_waitcnt lgkmcnt(0)
	s_barrier
	s_waitcnt lgkmcnt(0)
	v_mfma_f32_16x16x32_bf16 v[88:91], v[12:15], v[52:55], 0
	v_mfma_f32_16x16x32_bf16 v[92:95], v[16:19], v[56:59], v[88:91]
	v_mfma_f32_16x16x32_bf16 v[88:91], v[4:7], v[60:63], 0
	v_mfma_f32_16x16x32_bf16 v[68:71], v[4:7], v[36:39], 0
	v_mfma_f32_16x16x32_bf16 v[72:75], v[12:15], v[36:39], 0
	v_mfma_f32_16x16x32_bf16 v[76:79], v[4:7], v[44:47], 0
	v_mfma_f32_16x16x32_bf16 v[80:83], v[12:15], v[44:47], 0
	v_mfma_f32_16x16x32_bf16 v[84:87], v[4:7], v[52:55], 0
	v_mfma_f32_16x16x32_bf16 v[96:99], v[8:11], v[64:67], v[88:91]
	v_mfma_f32_16x16x32_bf16 v[88:91], v[12:15], v[60:63], 0
	v_mfma_f32_16x16x32_bf16 v[68:71], v[8:11], v[40:43], v[68:71]
	v_mfma_f32_16x16x32_bf16 v[72:75], v[16:19], v[40:43], v[72:75]
	v_mfma_f32_16x16x32_bf16 v[76:79], v[8:11], v[48:51], v[76:79]
	v_mfma_f32_16x16x32_bf16 v[80:83], v[16:19], v[48:51], v[80:83]
	v_mfma_f32_16x16x32_bf16 v[84:87], v[8:11], v[56:59], v[84:87]
	v_mfma_f32_16x16x32_bf16 v[108:111], v[16:19], v[64:67], v[88:91]
	v_mfma_f32_16x16x32_bf16 v[88:91], v[20:23], v[36:39], 0
	v_mfma_f32_16x16x32_bf16 v[36:39], v[28:31], v[36:39], 0
	v_mfma_f32_16x16x32_bf16 v[112:115], v[24:27], v[40:43], v[88:91]
	v_mfma_f32_16x16x32_bf16 v[36:39], v[32:35], v[40:43], v[36:39]
	v_mfma_f32_16x16x32_bf16 v[40:43], v[20:23], v[44:47], 0
	v_mfma_f32_16x16x32_bf16 v[44:47], v[28:31], v[44:47], 0
	v_mfma_f32_16x16x32_bf16 v[40:43], v[24:27], v[48:51], v[40:43]
	v_mfma_f32_16x16x32_bf16 v[44:47], v[32:35], v[48:51], v[44:47]
	v_mfma_f32_16x16x32_bf16 v[48:51], v[20:23], v[52:55], 0
	v_mfma_f32_16x16x32_bf16 v[52:55], v[28:31], v[52:55], 0
	v_mfma_f32_16x16x32_bf16 v[48:51], v[24:27], v[56:59], v[48:51]
	v_mfma_f32_16x16x32_bf16 v[52:55], v[32:35], v[56:59], v[52:55]
	v_mfma_f32_16x16x32_bf16 v[56:59], v[20:23], v[60:63], 0
	v_mfma_f32_16x16x32_bf16 v[60:63], v[28:31], v[60:63], 0
	v_mfma_f32_16x16x32_bf16 v[56:59], v[24:27], v[64:67], v[56:59]
	v_mfma_f32_16x16x32_bf16 v[60:63], v[32:35], v[64:67], v[60:63]
	s_barrier
	v_lshl_add_u64 v[186:187], s[28:29], 0, v[132:133]
	s_mov_b64 s[10:11], 0x100
	s_add_i32 s45, s45, s36
	v_lshl_add_u64 v[142:143], v[186:187], 0, s[10:11]
	s_mov_b32 m0, s45
	s_mov_b64 s[48:49], 0x40100
	s_add_i32 s46, s45, 0x2000
	ds_read_b128 v[64:67], v163 offset:16384
	ds_read_b128 v[88:91], v163 offset:17408
	ds_read_b128 v[100:103], v163 offset:18432
	ds_read_b128 v[104:107], v163 offset:19456
	ds_read_b128 v[116:119], v163 offset:20480
	ds_read_b128 v[120:123], v163 offset:21504
	ds_read_b128 v[124:127], v163 offset:22528
	ds_read_b128 v[128:131], v163 offset:23552
	global_load_lds_dwordx4 v[142:143], off
	v_lshl_add_u64 v[142:143], v[186:187], 0, s[48:49]
	s_mov_b32 m0, s46
	s_mov_b64 s[48:49], 0x80100
	s_add_i32 s47, s47, s36
	global_load_lds_dwordx4 v[142:143], off
	v_lshl_add_u64 v[142:143], v[186:187], 0, s[48:49]
	s_mov_b32 m0, s47
	s_mov_b64 s[48:49], 0xc0100
	global_load_lds_dwordx4 v[142:143], off
	v_lshl_add_u64 v[142:143], v[186:187], 0, s[48:49]
	s_add_i32 s48, s47, 0x2000
	s_mov_b32 m0, s48
	s_nop 0
	global_load_lds_dwordx4 v[142:143], off
	v_lshl_add_u64 v[142:143], v[184:185], 0, s[10:11]
	s_mov_b32 m0, s37
	s_mov_b64 s[10:11], 0x42100
	global_load_lds_dwordx4 v[142:143], off
	v_lshl_add_u64 v[142:143], v[184:185], 0, s[10:11]
	s_mov_b32 m0, s38
	s_nop 0
	global_load_lds_dwordx4 v[142:143], off
	s_waitcnt vmcnt(16)
	s_waitcnt lgkmcnt(0)
	s_barrier
	s_waitcnt lgkmcnt(0)
	v_mfma_f32_16x16x32_bf16 v[142:145], v[4:7], v[64:67], 0
	v_mfma_f32_16x16x32_bf16 v[152:155], v[4:7], v[100:103], 0
	v_mfma_f32_16x16x32_bf16 v[164:167], v[4:7], v[116:119], 0
	v_mfma_f32_16x16x32_bf16 v[4:7], v[4:7], v[124:127], 0
	v_mfma_f32_16x16x32_bf16 v[144:147], v[8:11], v[88:91], v[142:145]
	v_mfma_f32_16x16x32_bf16 v[152:155], v[8:11], v[104:107], v[152:155]
	v_mfma_f32_16x16x32_bf16 v[164:167], v[8:11], v[120:123], v[164:167]
	v_mfma_f32_16x16x32_bf16 v[4:7], v[8:11], v[128:131], v[4:7]
	v_mfma_f32_16x16x32_bf16 v[8:11], v[12:15], v[124:127], 0
	v_mfma_f32_16x16x32_bf16 v[148:151], v[12:15], v[64:67], 0
	v_mfma_f32_16x16x32_bf16 v[156:159], v[12:15], v[100:103], 0
	v_mfma_f32_16x16x32_bf16 v[168:171], v[12:15], v[116:119], 0
	v_mfma_f32_16x16x32_bf16 v[12:15], v[16:19], v[128:131], v[8:11]
	v_mfma_f32_16x16x32_bf16 v[148:151], v[16:19], v[88:91], v[148:151]
	v_mfma_f32_16x16x32_bf16 v[156:159], v[16:19], v[104:107], v[156:159]
	v_mfma_f32_16x16x32_bf16 v[168:171], v[16:19], v[120:123], v[168:171]
	v_mfma_f32_16x16x32_bf16 v[8:11], v[20:23], v[64:67], 0
	v_mfma_f32_16x16x32_bf16 v[16:19], v[24:27], v[88:91], v[8:11]
	v_mfma_f32_16x16x32_bf16 v[8:11], v[28:31], v[64:67], 0
	v_mfma_f32_16x16x32_bf16 v[172:175], v[32:35], v[88:91], v[8:11]
	v_mfma_f32_16x16x32_bf16 v[8:11], v[20:23], v[100:103], 0
	v_mfma_f32_16x16x32_bf16 v[176:179], v[24:27], v[104:107], v[8:11]
	v_mfma_f32_16x16x32_bf16 v[8:11], v[28:31], v[100:103], 0
	v_mfma_f32_16x16x32_bf16 v[194:197], v[32:35], v[104:107], v[8:11]
	v_mfma_f32_16x16x32_bf16 v[8:11], v[20:23], v[116:119], 0
	v_mfma_f32_16x16x32_bf16 v[198:201], v[24:27], v[120:123], v[8:11]
	v_mfma_f32_16x16x32_bf16 v[8:11], v[28:31], v[116:119], 0
	v_mfma_f32_16x16x32_bf16 v[202:205], v[32:35], v[120:123], v[8:11]
	v_mfma_f32_16x16x32_bf16 v[8:11], v[20:23], v[124:127], 0
	v_mfma_f32_16x16x32_bf16 v[206:209], v[24:27], v[128:131], v[8:11]
	v_mfma_f32_16x16x32_bf16 v[8:11], v[28:31], v[124:127], 0
	v_mfma_f32_16x16x32_bf16 v[220:223], v[32:35], v[128:131], v[8:11]
	s_barrier
	s_add_i32 s49, 0, 0x18000
	s_add_i32 s51, 0, 0x1c000
	v_add_u32_e32 v142, s49, v160
	v_add_u32_e32 v143, s51, v160
	s_nop 0
	ds_read_b128 v[8:11], v142
	ds_read_b128 v[28:31], v142 offset:1024
	ds_read_b128 v[32:35], v142 offset:2048
	ds_read_b128 v[64:67], v142 offset:3072
	ds_read_b128 v[224:227], v143
	ds_read_b128 v[228:231], v143 offset:1024
	ds_read_b128 v[232:235], v143 offset:2048
	ds_read_b128 v[236:239], v143 offset:3072
	s_mov_b64 s[10:11], 0x84100
	s_mov_b32 m0, s39
	v_lshl_add_u64 v[88:89], v[184:185], 0, s[10:11]
	s_mov_b64 s[10:11], 0xc6100
	ds_read_b128 v[20:23], v163 offset:32768
	ds_read_b128 v[24:27], v163 offset:33792
	ds_read_b128 v[240:243], v163 offset:34816
	ds_read_b128 v[244:247], v163 offset:35840
	ds_read_b128 v[248:251], v163 offset:36864
	ds_read_b128 v[216:219], v163 offset:37888
	ds_read_b128 v[190:193], v163 offset:38912
	ds_read_b128 v[180:183], v163 offset:39936
	global_load_lds_dwordx4 v[88:89], off
	v_lshl_add_u64 v[88:89], v[184:185], 0, s[10:11]
	s_mov_b32 m0, s40
	s_nop 0
	global_load_lds_dwordx4 v[88:89], off
	s_waitcnt vmcnt(8)
	s_waitcnt lgkmcnt(0)
	s_barrier
	s_waitcnt lgkmcnt(0)
	v_mfma_f32_16x16x32_bf16 v[68:71], v[8:11], v[20:23], v[68:71]
	v_mfma_f32_16x16x32_bf16 v[120:123], v[28:31], v[24:27], v[68:71]
	v_mfma_f32_16x16x32_bf16 v[68:71], v[32:35], v[20:23], v[72:75]
	v_mfma_f32_16x16x32_bf16 v[116:119], v[64:67], v[24:27], v[68:71]
	v_mfma_f32_16x16x32_bf16 v[68:71], v[8:11], v[240:243], v[76:79]
	v_mfma_f32_16x16x32_bf16 v[104:107], v[28:31], v[244:247], v[68:71]
	v_mfma_f32_16x16x32_bf16 v[68:71], v[32:35], v[240:243], v[80:83]
	v_mfma_f32_16x16x32_bf16 v[100:103], v[64:67], v[244:247], v[68:71]
	v_mfma_f32_16x16x32_bf16 v[68:71], v[8:11], v[248:251], v[84:87]
	v_mfma_f32_16x16x32_bf16 v[88:91], v[28:31], v[216:219], v[68:71]
	v_mfma_f32_16x16x32_bf16 v[68:71], v[32:35], v[248:251], v[92:95]
	v_mfma_f32_16x16x32_bf16 v[84:87], v[64:67], v[216:219], v[68:71]
	v_mfma_f32_16x16x32_bf16 v[68:71], v[8:11], v[190:193], v[96:99]
	v_mfma_f32_16x16x32_bf16 v[72:75], v[28:31], v[180:183], v[68:71]
	v_mfma_f32_16x16x32_bf16 v[68:71], v[32:35], v[190:193], v[108:111]
	v_mfma_f32_16x16x32_bf16 v[68:71], v[64:67], v[180:183], v[68:71]
	v_mfma_f32_16x16x32_bf16 v[76:79], v[224:227], v[20:23], v[112:115]
	v_mfma_f32_16x16x32_bf16 v[20:23], v[232:235], v[20:23], v[36:39]
	v_mfma_f32_16x16x32_bf16 v[124:127], v[236:239], v[24:27], v[20:23]
	v_mfma_f32_16x16x32_bf16 v[20:23], v[224:227], v[240:243], v[40:43]
	v_mfma_f32_16x16x32_bf16 v[112:115], v[228:231], v[244:247], v[20:23]
	v_mfma_f32_16x16x32_bf16 v[20:23], v[232:235], v[240:243], v[44:47]
	v_mfma_f32_16x16x32_bf16 v[108:111], v[236:239], v[244:247], v[20:23]
	v_mfma_f32_16x16x32_bf16 v[20:23], v[224:227], v[248:251], v[48:51]
	v_mfma_f32_16x16x32_bf16 v[96:99], v[228:231], v[216:219], v[20:23]
	v_mfma_f32_16x16x32_bf16 v[20:23], v[232:235], v[248:251], v[52:55]
	v_mfma_f32_16x16x32_bf16 v[92:95], v[236:239], v[216:219], v[20:23]
	v_mfma_f32_16x16x32_bf16 v[20:23], v[224:227], v[190:193], v[56:59]
	v_mfma_f32_16x16x32_bf16 v[80:83], v[228:231], v[180:183], v[20:23]
	v_mfma_f32_16x16x32_bf16 v[20:23], v[232:235], v[190:193], v[60:63]
	v_mfma_f32_16x16x32_bf16 v[128:131], v[228:231], v[24:27], v[76:79]
	v_mfma_f32_16x16x32_bf16 v[76:79], v[236:239], v[180:183], v[20:23]
	s_barrier
; #define PG8_MMA(ai, bj, At, Bt) do { __builtin_amdgcn_s_setprio(1); _Pragma("unroll") for (int m = 0; m < 4; ++m) _Pragma("unroll") for (int n = 0; n < 2; ++n) _Pragma("unroll") for (int k = 0; k < 2; ++k) \
;         acc[ai][bj][m][n] = __builtin_amdgcn_mfma_f32_16x16x32_bf16(Bt[n][k], At[m][k], acc[ai][bj][m][n], 0, 0, 0); __builtin_amdgcn_s_setprio(0); } while (0)
; #define PG8_WAIT_V(n) asm volatile("s_waitcnt vmcnt(" #n ")" ::: "memory")
; #define PG8_TRIP_HEAD(T) const int t = (T); const bool last = (t == nt - 2); \
;             const char* a1 = cA + (size_t)(t + 1) * kstep; \
;             const char* a2 = last ? nA : cA + (size_t)(t + 2) * kstep; const char* b2 = last ? nB : cB + (size_t)(t + 2) * kstep; \
;             const char* a3 = a2 + kstep; const char* b3 = b2 + kstep; \
;             if (last && has_next) S.a_ready(nxt);
; template <class Epi, class Sched, bool ALIGN_EPI = false, bool SP2 = false>
; __device__ __forceinline__ void gemm_phase(PG8_LAS unsigned char* lds, const Gemm g, const Sched& S, const Epi& E) {
;     ...
;         if constexpr (SP2) {
;             { PG8_TRIP_HEAD(0) PG8_TRIP_SP2(asm volatile("s_waitcnt vmcnt(%0)" :: "n"(8 + Epi::NST) : "memory"), PG8_MMAZ) }
;             for (int tt = 2; tt < nt; tt += 2) { PG8_TRIP_HEAD(tt) PG8_TRIP_SP2(PG8_WAIT_V(8), PG8_MMA) }
	s_mov_b64 s[10:11], 0x180
	s_add_i32 s49, s49, s36
	s_nop 1
	v_lshl_add_u64 v[20:21], v[186:187], 0, s[10:11]
	s_mov_b32 m0, s49
	s_mov_b64 s[52:53], 0x40180
	s_add_i32 s50, s49, 0x2000
	ds_read_b128 v[44:47], v163 offset:49152
	ds_read_b128 v[48:51], v163 offset:50176
	ds_read_b128 v[180:183], v163 offset:51200
	ds_read_b128 v[190:193], v163 offset:52224
	ds_read_b128 v[216:219], v163 offset:53248
	ds_read_b128 v[240:243], v163 offset:54272
	ds_read_b128 v[244:247], v163 offset:55296
	ds_read_b128 v[248:251], v163 offset:56320
	global_load_lds_dwordx4 v[20:21], off
	v_lshl_add_u64 v[20:21], v[186:187], 0, s[52:53]
	s_mov_b32 m0, s50
	s_mov_b64 s[52:53], 0x80180
	s_add_i32 s51, s51, s36
	global_load_lds_dwordx4 v[20:21], off
	v_lshl_add_u64 v[20:21], v[186:187], 0, s[52:53]
	s_mov_b32 m0, s51
	s_mov_b64 s[52:53], 0xc0180
	global_load_lds_dwordx4 v[20:21], off
	v_lshl_add_u64 v[20:21], v[186:187], 0, s[52:53]
	s_add_i32 s52, s51, 0x2000
	s_mov_b32 m0, s52
	s_nop 0
	global_load_lds_dwordx4 v[20:21], off
	v_lshl_add_u64 v[20:21], v[184:185], 0, s[10:11]
	s_mov_b32 m0, s0
	s_mov_b64 s[10:11], 0x42180
	global_load_lds_dwordx4 v[20:21], off
	v_lshl_add_u64 v[20:21], v[184:185], 0, s[10:11]
	s_mov_b32 m0, s41
	s_nop 0
	global_load_lds_dwordx4 v[20:21], off
	s_waitcnt vmcnt(8)
	s_waitcnt lgkmcnt(0)
	s_barrier
	s_waitcnt lgkmcnt(0)
	v_mfma_f32_16x16x32_bf16 v[20:23], v[8:11], v[44:47], v[144:147]
	v_mfma_f32_16x16x32_bf16 v[56:59], v[28:31], v[48:51], v[20:23]
	v_mfma_f32_16x16x32_bf16 v[20:23], v[32:35], v[44:47], v[148:151]
	v_mfma_f32_16x16x32_bf16 v[52:55], v[64:67], v[48:51], v[20:23]
	v_mfma_f32_16x16x32_bf16 v[20:23], v[8:11], v[180:183], v[152:155]
	v_mfma_f32_16x16x32_bf16 v[40:43], v[28:31], v[190:193], v[20:23]
	v_mfma_f32_16x16x32_bf16 v[20:23], v[32:35], v[180:183], v[156:159]
	v_mfma_f32_16x16x32_bf16 v[36:39], v[64:67], v[190:193], v[20:23]
	v_mfma_f32_16x16x32_bf16 v[20:23], v[8:11], v[216:219], v[164:167]
	v_mfma_f32_16x16x32_bf16 v[4:7], v[8:11], v[244:247], v[4:7]
	v_mfma_f32_16x16x32_bf16 v[24:27], v[28:31], v[240:243], v[20:23]
	v_mfma_f32_16x16x32_bf16 v[20:23], v[32:35], v[216:219], v[168:171]
	v_mfma_f32_16x16x32_bf16 v[8:11], v[28:31], v[248:251], v[4:7]
	v_mfma_f32_16x16x32_bf16 v[4:7], v[32:35], v[244:247], v[12:15]
	v_mfma_f32_16x16x32_bf16 v[20:23], v[64:67], v[240:243], v[20:23]
	v_mfma_f32_16x16x32_bf16 v[4:7], v[64:67], v[248:251], v[4:7]
	v_mfma_f32_16x16x32_bf16 v[12:15], v[224:227], v[44:47], v[16:19]
	v_mfma_f32_16x16x32_bf16 v[64:67], v[228:231], v[48:51], v[12:15]
	v_mfma_f32_16x16x32_bf16 v[12:15], v[232:235], v[44:47], v[172:175]
	v_mfma_f32_16x16x32_bf16 v[60:63], v[236:239], v[48:51], v[12:15]
	v_mfma_f32_16x16x32_bf16 v[12:15], v[224:227], v[180:183], v[176:179]
	v_mfma_f32_16x16x32_bf16 v[48:51], v[228:231], v[190:193], v[12:15]
	v_mfma_f32_16x16x32_bf16 v[12:15], v[232:235], v[180:183], v[194:197]
	v_mfma_f32_16x16x32_bf16 v[44:47], v[236:239], v[190:193], v[12:15]
	v_mfma_f32_16x16x32_bf16 v[12:15], v[224:227], v[216:219], v[198:201]
	v_mfma_f32_16x16x32_bf16 v[32:35], v[228:231], v[240:243], v[12:15]
	v_mfma_f32_16x16x32_bf16 v[12:15], v[232:235], v[216:219], v[202:205]
	v_mfma_f32_16x16x32_bf16 v[28:31], v[236:239], v[240:243], v[12:15]
	v_mfma_f32_16x16x32_bf16 v[12:15], v[224:227], v[244:247], v[206:209]
	v_mfma_f32_16x16x32_bf16 v[16:19], v[228:231], v[248:251], v[12:15]
	v_mfma_f32_16x16x32_bf16 v[12:15], v[232:235], v[244:247], v[220:223]
	v_mfma_f32_16x16x32_bf16 v[12:15], v[236:239], v[248:251], v[12:15]
	s_barrier
	s_add_u32 s10, s30, 0x84180
	s_addc_u32 s11, s31, 0
	s_add_u32 s28, s28, 0x200
	s_addc_u32 s29, s29, 0
	s_mov_b32 s30, 0
	s_mov_b64 s[60:61], 0x80000
	s_mov_b64 s[62:63], 0x80080
	s_mov_b64 s[64:65], 0xc0000
	s_mov_b64 s[66:67], 0xc0080
	s_mov_b64 s[68:69], 0xc6000
.LBB0_130:
	ds_read_b128 v[144:147], v140
	ds_read_b128 v[148:151], v140 offset:1024
	ds_read_b128 v[152:155], v140 offset:2048
	ds_read_b128 v[156:159], v140 offset:3072
	ds_read_b128 v[164:167], v141
	ds_read_b128 v[168:171], v141 offset:1024
	ds_read_b128 v[172:175], v141 offset:2048
	ds_read_b128 v[176:179], v141 offset:3072
	s_add_u32 s31, s10, 0xfff7c080
	s_addc_u32 s53, s11, -1
	s_cmp_eq_u32 s30, 28
	s_cselect_b32 s55, s25, s53
	s_cselect_b32 s54, s24, s31
	s_cselect_b32 s57, s4, s29
	s_cselect_b32 s56, s5, s28
	s_mov_b32 m0, s23
	v_lshl_add_u64 v[184:185], s[10:11], 0, v[138:139]
	ds_read_b128 v[180:183], v163
	ds_read_b128 v[190:193], v163 offset:1024
	ds_read_b128 v[194:197], v163 offset:2048
	ds_read_b128 v[198:201], v163 offset:3072
	ds_read_b128 v[202:205], v163 offset:4096
	ds_read_b128 v[206:209], v163 offset:5120
	ds_read_b128 v[216:219], v163 offset:6144
	ds_read_b128 v[220:223], v163 offset:7168
	global_load_lds_dwordx4 v[184:185], off
	v_lshl_add_u64 v[184:185], v[184:185], 0, s[96:97]
	s_mov_b32 m0, s33
	s_nop 0
	global_load_lds_dwordx4 v[184:185], off
	s_waitcnt vmcnt(8)
	s_waitcnt lgkmcnt(0)
	s_barrier
	s_waitcnt lgkmcnt(0)
	v_mfma_f32_16x16x32_bf16 v[120:123], v[144:147], v[180:183], v[120:123]
	v_mfma_f32_16x16x32_bf16 v[116:119], v[152:155], v[180:183], v[116:119]
	v_mfma_f32_16x16x32_bf16 v[104:107], v[144:147], v[194:197], v[104:107]
	v_mfma_f32_16x16x32_bf16 v[100:103], v[152:155], v[194:197], v[100:103]
	v_mfma_f32_16x16x32_bf16 v[88:91], v[144:147], v[202:205], v[88:91]
	v_mfma_f32_16x16x32_bf16 v[84:87], v[152:155], v[202:205], v[84:87]
	v_mfma_f32_16x16x32_bf16 v[72:75], v[144:147], v[216:219], v[72:75]
	v_mfma_f32_16x16x32_bf16 v[68:71], v[152:155], v[216:219], v[68:71]
	v_mfma_f32_16x16x32_bf16 v[120:123], v[148:151], v[190:193], v[120:123]
	v_mfma_f32_16x16x32_bf16 v[116:119], v[156:159], v[190:193], v[116:119]
	v_mfma_f32_16x16x32_bf16 v[104:107], v[148:151], v[198:201], v[104:107]
	v_mfma_f32_16x16x32_bf16 v[100:103], v[156:159], v[198:201], v[100:103]
	v_mfma_f32_16x16x32_bf16 v[88:91], v[148:151], v[206:209], v[88:91]
	v_mfma_f32_16x16x32_bf16 v[84:87], v[156:159], v[206:209], v[84:87]
	v_mfma_f32_16x16x32_bf16 v[72:75], v[148:151], v[220:223], v[72:75]
	v_mfma_f32_16x16x32_bf16 v[68:71], v[156:159], v[220:223], v[68:71]
	v_mfma_f32_16x16x32_bf16 v[128:131], v[164:167], v[180:183], v[128:131]
	v_mfma_f32_16x16x32_bf16 v[124:127], v[172:175], v[180:183], v[124:127]
	v_mfma_f32_16x16x32_bf16 v[112:115], v[164:167], v[194:197], v[112:115]
	v_mfma_f32_16x16x32_bf16 v[108:111], v[172:175], v[194:197], v[108:111]
	v_mfma_f32_16x16x32_bf16 v[96:99], v[164:167], v[202:205], v[96:99]
	v_mfma_f32_16x16x32_bf16 v[92:95], v[172:175], v[202:205], v[92:95]
	v_mfma_f32_16x16x32_bf16 v[80:83], v[164:167], v[216:219], v[80:83]
	v_mfma_f32_16x16x32_bf16 v[76:79], v[172:175], v[216:219], v[76:79]
	v_mfma_f32_16x16x32_bf16 v[128:131], v[168:171], v[190:193], v[128:131]
	v_mfma_f32_16x16x32_bf16 v[124:127], v[176:179], v[190:193], v[124:127]
	v_mfma_f32_16x16x32_bf16 v[112:115], v[168:171], v[198:201], v[112:115]
	v_mfma_f32_16x16x32_bf16 v[108:111], v[176:179], v[198:201], v[108:111]
	v_mfma_f32_16x16x32_bf16 v[96:99], v[168:171], v[206:209], v[96:99]
	v_mfma_f32_16x16x32_bf16 v[92:95], v[176:179], v[206:209], v[92:95]
	v_mfma_f32_16x16x32_bf16 v[80:83], v[168:171], v[220:223], v[80:83]
	v_mfma_f32_16x16x32_bf16 v[76:79], v[176:179], v[220:223], v[76:79]
	s_barrier
	s_mov_b32 m0, s45
	v_lshl_add_u64 v[184:185], s[56:57], 0, v[132:133]
	ds_read_b128 v[180:183], v163 offset:16384
	ds_read_b128 v[190:193], v163 offset:17408
	ds_read_b128 v[194:197], v163 offset:18432
	ds_read_b128 v[198:201], v163 offset:19456
	ds_read_b128 v[202:205], v163 offset:20480
	ds_read_b128 v[206:209], v163 offset:21504
	ds_read_b128 v[216:219], v163 offset:22528
	ds_read_b128 v[220:223], v163 offset:23552
	global_load_lds_dwordx4 v[184:185], off
	v_lshl_add_u64 v[186:187], v[184:185], 0, s[90:91]
	s_mov_b32 m0, s46
	s_nop 0
	global_load_lds_dwordx4 v[186:187], off
	v_lshl_add_u64 v[186:187], v[184:185], 0, s[60:61]
	s_mov_b32 m0, s47
	s_nop 0
	global_load_lds_dwordx4 v[186:187], off
	v_lshl_add_u64 v[186:187], v[184:185], 0, s[64:65]
	s_mov_b32 m0, s48
	s_nop 0
	global_load_lds_dwordx4 v[186:187], off
	v_lshl_add_u64 v[186:187], s[54:55], 0, v[134:135]
	s_mov_b32 m0, s37
	v_lshl_add_u64 v[188:189], v[186:187], 0, s[96:97]
	global_load_lds_dwordx4 v[186:187], off
	s_mov_b32 m0, s38
	s_nop 0
	global_load_lds_dwordx4 v[188:189], off
	s_waitcnt vmcnt(8)
	s_waitcnt lgkmcnt(0)
	s_barrier
	s_waitcnt lgkmcnt(0)
	v_mfma_f32_16x16x32_bf16 v[56:59], v[144:147], v[180:183], v[56:59]
	v_mfma_f32_16x16x32_bf16 v[52:55], v[152:155], v[180:183], v[52:55]
	v_mfma_f32_16x16x32_bf16 v[40:43], v[144:147], v[194:197], v[40:43]
	v_mfma_f32_16x16x32_bf16 v[36:39], v[152:155], v[194:197], v[36:39]
	v_mfma_f32_16x16x32_bf16 v[24:27], v[144:147], v[202:205], v[24:27]
	v_mfma_f32_16x16x32_bf16 v[20:23], v[152:155], v[202:205], v[20:23]
	v_mfma_f32_16x16x32_bf16 v[8:11], v[144:147], v[216:219], v[8:11]
	v_mfma_f32_16x16x32_bf16 v[4:7], v[152:155], v[216:219], v[4:7]
	v_mfma_f32_16x16x32_bf16 v[56:59], v[148:151], v[190:193], v[56:59]
	v_mfma_f32_16x16x32_bf16 v[52:55], v[156:159], v[190:193], v[52:55]
	v_mfma_f32_16x16x32_bf16 v[40:43], v[148:151], v[198:201], v[40:43]
	v_mfma_f32_16x16x32_bf16 v[36:39], v[156:159], v[198:201], v[36:39]
	v_mfma_f32_16x16x32_bf16 v[24:27], v[148:151], v[206:209], v[24:27]
	v_mfma_f32_16x16x32_bf16 v[20:23], v[156:159], v[206:209], v[20:23]
	v_mfma_f32_16x16x32_bf16 v[8:11], v[148:151], v[220:223], v[8:11]
	v_mfma_f32_16x16x32_bf16 v[4:7], v[156:159], v[220:223], v[4:7]
	v_mfma_f32_16x16x32_bf16 v[64:67], v[164:167], v[180:183], v[64:67]
	v_mfma_f32_16x16x32_bf16 v[60:63], v[172:175], v[180:183], v[60:63]
	v_mfma_f32_16x16x32_bf16 v[48:51], v[164:167], v[194:197], v[48:51]
	v_mfma_f32_16x16x32_bf16 v[44:47], v[172:175], v[194:197], v[44:47]
	v_mfma_f32_16x16x32_bf16 v[32:35], v[164:167], v[202:205], v[32:35]
	v_mfma_f32_16x16x32_bf16 v[28:31], v[172:175], v[202:205], v[28:31]
	v_mfma_f32_16x16x32_bf16 v[16:19], v[164:167], v[216:219], v[16:19]
	v_mfma_f32_16x16x32_bf16 v[12:15], v[172:175], v[216:219], v[12:15]
	v_mfma_f32_16x16x32_bf16 v[64:67], v[168:171], v[190:193], v[64:67]
	v_mfma_f32_16x16x32_bf16 v[60:63], v[176:179], v[190:193], v[60:63]
	v_mfma_f32_16x16x32_bf16 v[48:51], v[168:171], v[198:201], v[48:51]
	v_mfma_f32_16x16x32_bf16 v[44:47], v[176:179], v[198:201], v[44:47]
	v_mfma_f32_16x16x32_bf16 v[32:35], v[168:171], v[206:209], v[32:35]
	v_mfma_f32_16x16x32_bf16 v[28:31], v[176:179], v[206:209], v[28:31]
	v_mfma_f32_16x16x32_bf16 v[16:19], v[168:171], v[220:223], v[16:19]
	v_mfma_f32_16x16x32_bf16 v[12:15], v[176:179], v[220:223], v[12:15]
	s_barrier
; #define PG8_MMA(ai, bj, At, Bt) do { __builtin_amdgcn_s_setprio(1); _Pragma("unroll") for (int m = 0; m < 4; ++m) _Pragma("unroll") for (int n = 0; n < 2; ++n) _Pragma("unroll") for (int k = 0; k < 2; ++k) \
;         acc[ai][bj][m][n] = __builtin_amdgcn_mfma_f32_16x16x32_bf16(Bt[n][k], At[m][k], acc[ai][bj][m][n], 0, 0, 0); __builtin_amdgcn_s_setprio(0); } while (0)
; #define PG8_WAIT_V(n) asm volatile("s_waitcnt vmcnt(" #n ")" ::: "memory")
; #define PG8_TRIP_HEAD(T) const int t = (T); const bool last = (t == nt - 2); \
;             const char* a1 = cA + (size_t)(t + 1) * kstep; \
;             const char* a2 = last ? nA : cA + (size_t)(t + 2) * kstep; const char* b2 = last ? nB : cB + (size_t)(t + 2) * kstep; \
;             const char* a3 = a2 + kstep; const char* b3 = b2 + kstep; \
;             if (last && has_next) S.a_ready(nxt);
; template <class Epi, class Sched, bool ALIGN_EPI = false, bool SP2 = false>
; __device__ __forceinline__ void gemm_phase(PG8_LAS unsigned char* lds, const Gemm g, const Sched& S, const Epi& E) {
;     ...
;         if constexpr (SP2) {
;             { PG8_TRIP_HEAD(0) PG8_TRIP_SP2(asm volatile("s_waitcnt vmcnt(%0)" :: "n"(8 + Epi::NST) : "memory"), PG8_MMAZ) }
;             for (int tt = 2; tt < nt; tt += 2) { PG8_TRIP_HEAD(tt) PG8_TRIP_SP2(PG8_WAIT_V(8), PG8_MMA) }
	ds_read_b128 v[144:147], v142
	ds_read_b128 v[148:151], v142 offset:1024
	ds_read_b128 v[152:155], v142 offset:2048
	ds_read_b128 v[156:159], v142 offset:3072
	ds_read_b128 v[164:167], v143
	ds_read_b128 v[168:171], v143 offset:1024
	ds_read_b128 v[172:175], v143 offset:2048
	ds_read_b128 v[176:179], v143 offset:3072
	s_mov_b32 m0, s39
	v_lshl_add_u64 v[188:189], v[186:187], 0, s[82:83]
	ds_read_b128 v[180:183], v163 offset:32768
	ds_read_b128 v[190:193], v163 offset:33792
	ds_read_b128 v[194:197], v163 offset:34816
	ds_read_b128 v[198:201], v163 offset:35840
	ds_read_b128 v[202:205], v163 offset:36864
	ds_read_b128 v[206:209], v163 offset:37888
	ds_read_b128 v[216:219], v163 offset:38912
	ds_read_b128 v[220:223], v163 offset:39936
	global_load_lds_dwordx4 v[188:189], off
	v_lshl_add_u64 v[188:189], v[186:187], 0, s[68:69]
	s_mov_b32 m0, s40
	s_nop 0
	global_load_lds_dwordx4 v[188:189], off
	s_waitcnt vmcnt(8)
	s_waitcnt lgkmcnt(0)
	s_barrier
	s_waitcnt lgkmcnt(0)
	v_mfma_f32_16x16x32_bf16 v[120:123], v[144:147], v[180:183], v[120:123]
	v_mfma_f32_16x16x32_bf16 v[116:119], v[152:155], v[180:183], v[116:119]
	v_mfma_f32_16x16x32_bf16 v[104:107], v[144:147], v[194:197], v[104:107]
	v_mfma_f32_16x16x32_bf16 v[100:103], v[152:155], v[194:197], v[100:103]
	v_mfma_f32_16x16x32_bf16 v[88:91], v[144:147], v[202:205], v[88:91]
	v_mfma_f32_16x16x32_bf16 v[84:87], v[152:155], v[202:205], v[84:87]
	v_mfma_f32_16x16x32_bf16 v[72:75], v[144:147], v[216:219], v[72:75]
	v_mfma_f32_16x16x32_bf16 v[68:71], v[152:155], v[216:219], v[68:71]
	v_mfma_f32_16x16x32_bf16 v[120:123], v[148:151], v[190:193], v[120:123]
	v_mfma_f32_16x16x32_bf16 v[116:119], v[156:159], v[190:193], v[116:119]
	v_mfma_f32_16x16x32_bf16 v[104:107], v[148:151], v[198:201], v[104:107]
	v_mfma_f32_16x16x32_bf16 v[100:103], v[156:159], v[198:201], v[100:103]
	v_mfma_f32_16x16x32_bf16 v[88:91], v[148:151], v[206:209], v[88:91]
	v_mfma_f32_16x16x32_bf16 v[84:87], v[156:159], v[206:209], v[84:87]
	v_mfma_f32_16x16x32_bf16 v[72:75], v[148:151], v[220:223], v[72:75]
	v_mfma_f32_16x16x32_bf16 v[68:71], v[156:159], v[220:223], v[68:71]
	v_mfma_f32_16x16x32_bf16 v[128:131], v[164:167], v[180:183], v[128:131]
	v_mfma_f32_16x16x32_bf16 v[124:127], v[172:175], v[180:183], v[124:127]
	v_mfma_f32_16x16x32_bf16 v[112:115], v[164:167], v[194:197], v[112:115]
	v_mfma_f32_16x16x32_bf16 v[108:111], v[172:175], v[194:197], v[108:111]
	v_mfma_f32_16x16x32_bf16 v[96:99], v[164:167], v[202:205], v[96:99]
	v_mfma_f32_16x16x32_bf16 v[92:95], v[172:175], v[202:205], v[92:95]
	v_mfma_f32_16x16x32_bf16 v[80:83], v[164:167], v[216:219], v[80:83]
	v_mfma_f32_16x16x32_bf16 v[76:79], v[172:175], v[216:219], v[76:79]
	v_mfma_f32_16x16x32_bf16 v[128:131], v[168:171], v[190:193], v[128:131]
	v_mfma_f32_16x16x32_bf16 v[124:127], v[176:179], v[190:193], v[124:127]
	v_mfma_f32_16x16x32_bf16 v[112:115], v[168:171], v[198:201], v[112:115]
	v_mfma_f32_16x16x32_bf16 v[108:111], v[176:179], v[198:201], v[108:111]
	v_mfma_f32_16x16x32_bf16 v[96:99], v[168:171], v[206:209], v[96:99]
	v_mfma_f32_16x16x32_bf16 v[92:95], v[176:179], v[206:209], v[92:95]
	v_mfma_f32_16x16x32_bf16 v[80:83], v[168:171], v[220:223], v[80:83]
	v_mfma_f32_16x16x32_bf16 v[76:79], v[176:179], v[220:223], v[76:79]
	s_barrier
	s_mov_b32 m0, s49
	v_lshl_add_u64 v[188:189], v[184:185], 0, s[78:79]
	ds_read_b128 v[180:183], v163 offset:49152
	ds_read_b128 v[190:193], v163 offset:50176
	ds_read_b128 v[194:197], v163 offset:51200
	ds_read_b128 v[198:201], v163 offset:52224
	ds_read_b128 v[202:205], v163 offset:53248
	ds_read_b128 v[206:209], v163 offset:54272
	ds_read_b128 v[216:219], v163 offset:55296
	ds_read_b128 v[220:223], v163 offset:56320
	global_load_lds_dwordx4 v[188:189], off
	v_lshl_add_u64 v[188:189], v[184:185], 0, s[84:85]
	s_mov_b32 m0, s50
	s_nop 0
	global_load_lds_dwordx4 v[188:189], off
	v_lshl_add_u64 v[188:189], v[184:185], 0, s[62:63]
	s_mov_b32 m0, s51
	v_lshl_add_u64 v[184:185], v[184:185], 0, s[66:67]
	global_load_lds_dwordx4 v[188:189], off
	s_mov_b32 m0, s52
	s_nop 0
	global_load_lds_dwordx4 v[184:185], off
	v_lshl_add_u64 v[184:185], v[186:187], 0, s[78:79]
	s_mov_b32 m0, s0
	s_nop 0
	global_load_lds_dwordx4 v[184:185], off
	v_lshl_add_u64 v[184:185], v[186:187], 0, s[92:93]
	s_mov_b32 m0, s41
	s_nop 0
	global_load_lds_dwordx4 v[184:185], off
	s_waitcnt vmcnt(8)
	s_waitcnt lgkmcnt(0)
	s_barrier
	s_waitcnt lgkmcnt(0)
	v_mfma_f32_16x16x32_bf16 v[56:59], v[144:147], v[180:183], v[56:59]
	v_mfma_f32_16x16x32_bf16 v[52:55], v[152:155], v[180:183], v[52:55]
	v_mfma_f32_16x16x32_bf16 v[40:43], v[144:147], v[194:197], v[40:43]
	v_mfma_f32_16x16x32_bf16 v[36:39], v[152:155], v[194:197], v[36:39]
	v_mfma_f32_16x16x32_bf16 v[24:27], v[144:147], v[202:205], v[24:27]
	v_mfma_f32_16x16x32_bf16 v[20:23], v[152:155], v[202:205], v[20:23]
	v_mfma_f32_16x16x32_bf16 v[8:11], v[144:147], v[216:219], v[8:11]
	v_mfma_f32_16x16x32_bf16 v[4:7], v[152:155], v[216:219], v[4:7]
	v_mfma_f32_16x16x32_bf16 v[56:59], v[148:151], v[190:193], v[56:59]
	v_mfma_f32_16x16x32_bf16 v[52:55], v[156:159], v[190:193], v[52:55]
	v_mfma_f32_16x16x32_bf16 v[40:43], v[148:151], v[198:201], v[40:43]
	v_mfma_f32_16x16x32_bf16 v[36:39], v[156:159], v[198:201], v[36:39]
	v_mfma_f32_16x16x32_bf16 v[24:27], v[148:151], v[206:209], v[24:27]
	v_mfma_f32_16x16x32_bf16 v[20:23], v[156:159], v[206:209], v[20:23]
	v_mfma_f32_16x16x32_bf16 v[8:11], v[148:151], v[220:223], v[8:11]
	v_mfma_f32_16x16x32_bf16 v[4:7], v[156:159], v[220:223], v[4:7]
	v_mfma_f32_16x16x32_bf16 v[64:67], v[164:167], v[180:183], v[64:67]
	v_mfma_f32_16x16x32_bf16 v[60:63], v[172:175], v[180:183], v[60:63]
	v_mfma_f32_16x16x32_bf16 v[48:51], v[164:167], v[194:197], v[48:51]
	v_mfma_f32_16x16x32_bf16 v[44:47], v[172:175], v[194:197], v[44:47]
	v_mfma_f32_16x16x32_bf16 v[32:35], v[164:167], v[202:205], v[32:35]
	v_mfma_f32_16x16x32_bf16 v[28:31], v[172:175], v[202:205], v[28:31]
	v_mfma_f32_16x16x32_bf16 v[16:19], v[164:167], v[216:219], v[16:19]
	v_mfma_f32_16x16x32_bf16 v[12:15], v[172:175], v[216:219], v[12:15]
	v_mfma_f32_16x16x32_bf16 v[64:67], v[168:171], v[190:193], v[64:67]
	v_mfma_f32_16x16x32_bf16 v[60:63], v[176:179], v[190:193], v[60:63]
	v_mfma_f32_16x16x32_bf16 v[48:51], v[168:171], v[198:201], v[48:51]
	v_mfma_f32_16x16x32_bf16 v[44:47], v[176:179], v[198:201], v[44:47]
	v_mfma_f32_16x16x32_bf16 v[32:35], v[168:171], v[206:209], v[32:35]
	v_mfma_f32_16x16x32_bf16 v[28:31], v[176:179], v[206:209], v[28:31]
	v_mfma_f32_16x16x32_bf16 v[16:19], v[168:171], v[220:223], v[16:19]
	v_mfma_f32_16x16x32_bf16 v[12:15], v[176:179], v[220:223], v[12:15]
	s_barrier
	s_add_i32 s30, s30, 2
	s_add_u32 s10, s10, 0x100
	s_addc_u32 s11, s11, 0
	s_add_u32 s28, s28, 0x100
	s_addc_u32 s29, s29, 0
	s_cmp_gt_u32 s30, 29
	s_cbranch_scc0 .LBB0_130
	s_and_b64 vcc, exec, s[20:21]
	s_cbranch_vccz .LBB0_133
	s_barrier

; #define PG8_WAIT_V(n) asm volatile("s_waitcnt vmcnt(" #n ")" ::: "memory")
; #define PG8_BAR __builtin_amdgcn_s_barrier()
; __device__ __forceinline__ unsigned xb_xcc_id() { return (unsigned)__builtin_amdgcn_s_getreg((3 << 11) | 20) & 0xFu; }
; template <class Epi, class Sched, bool ALIGN_EPI = false, bool SP2 = false>
; __device__ __forceinline__ void gemm_phase(PG8_LAS unsigned char* lds, const Gemm g, const Sched& S, const Epi& E) {
;     ...
;     PG8_WAIT_V(0);
;     if constexpr (!ALIGN_EPI) { if (wr == 0) PG8_BAR; }
;     PG8_BAR;
; __device__ __forceinline__ void xcd_barrier(const XcdBarrier& b) {
;     asm volatile("s_waitcnt vmcnt(0)" ::: "memory");
;     __syncthreads();
;     if (threadIdx.x == 0) {
;         unsigned* bar = b.bar; const unsigned bx_ = xb_xcc_id();
;         __builtin_amdgcn_s_waitcnt(0);
;         unsigned nloc = b.st[0], nx = b.st[1];
;         if (nloc == 0u) { xcd_barrier_complete(bar, bx_, nloc, nx); b.st[0] = nloc; b.st[1] = nx; }
.LBB0_157:
	s_setprio 0
	s_waitcnt vmcnt(0)
	s_waitcnt vmcnt(0) lgkmcnt(0)
	s_barrier
	s_mov_b64 s[6:7], exec
	v_readlane_b32 s2, v252, 15
	v_readlane_b32 s3, v252, 16
	s_and_b64 s[2:3], s[6:7], s[2:3]
	s_mov_b64 exec, s[2:3]
	s_cbranch_execz .LBB0_209
	v_readlane_b32 s2, v255, 32
	s_getreg_b32 s0, hwreg(HW_REG_XCC_ID, 0, 4)
	s_waitcnt vmcnt(0) expcnt(0) lgkmcnt(0)
	v_mov_b32_e32 v3, s2
	ds_read_b32 v5, v3
	v_readlane_b32 s2, v255, 33
	s_and_b32 s0, s0, 15
	s_waitcnt lgkmcnt(0)
	v_cmp_ne_u32_e32 vcc, 0, v5
	v_mov_b32_e32 v3, s2
	ds_read_b32 v4, v3
	s_cbranch_vccnz .LBB0_173
	v_readlane_b32 s4, v252, 8
	v_readlane_b32 s5, v252, 9
	s_load_dwordx2 s[2:3], s[4:5], 0x4
	v_readlane_b32 s4, v252, 10
	v_readlane_b32 s5, v252, 11
	s_waitcnt lgkmcnt(0)
	s_mul_i32 s2, s2, s4
	s_mul_i32 s2, s2, s3
	s_mov_b32 s3, 1
	s_branch .LBB0_161

; #define PG8_WAIT_V(n) asm volatile("s_waitcnt vmcnt(" #n ")" ::: "memory")
; #define PG8_BAR __builtin_amdgcn_s_barrier()
; template <class Epi, class Sched, bool ALIGN_EPI = false, bool SP2 = false>
; __device__ __forceinline__ void gemm_phase(PG8_LAS unsigned char* lds, const Gemm g, const Sched& S, const Epi& E) {
;     int tid_l = threadIdx.x; asm volatile("" : "+v"(tid_l));
;     const int tid = tid_l, wid = __builtin_amdgcn_readfirstlane(tid >> 6), lane = tid & 63, wr = wid >> 2, wc = wid & 3, fr = lane & 15, fq = lane >> 4;
;     const int K = g.K, nt = K / BK;
;     unsigned voffA, voffB;
;     { int R, C; stage_rc(tid * 16, R, C); const int Rb = Epi::PERM ? ((R & ~31) + perm32(R & 31)) : R;
;         voffA = (unsigned)(R * g.lda + C) * 2u; voffB = (unsigned)(Rb * g.ldb + C) * 2u; }
;     const size_t voffA_step = (size_t)64 * g.lda * 2, voffB_step = (size_t)64 * g.ldb * 2;
;     const size_t kstep = (size_t)(BK * 2);
;     const size_t hstepA = (size_t)HALF * g.lda * 2, hstepB = (size_t)HALF * g.ldb * 2;
;     const size_t tstepA = 2 * hstepA, tstepB = 2 * hstepB;
;     const unsigned ldsw = (unsigned)wid * 1024u;
;     const int aoff = lds_byte(wr * 64 + fr, fq * 8), boff = lds_byte(wc * 32 + fr, fq * 8);
;     ...
;     Unit cur, nxt; int ui = 0;
;     if (!S.next(0, cur)) return;
;     f32x4 acc[2][2][4][2];
;     if constexpr (!SP2) {
; #pragma unroll
;     for (int a = 0; a < 2; ++a)
; #pragma unroll
;         for (int b = 0; b < 2; ++b)
; #pragma unroll
;             for (int m = 0; m < 4; ++m)
; #pragma unroll
;                 for (int n = 0; n < 2; ++n) acc[a][b][m][n] = (f32x4){0.f, 0.f, 0.f, 0.f};
;     }
;     bf16x8 At[4][2], B0[2][2], B1[2][2];
;     const char* cA = (const char*)S.opA(g, cur) + (size_t)cur.pm * tstepA; const char* cB = (const char*)S.opB(g, cur) + (size_t)cur.pn * tstepB;
;     S.a_ready(cur);
;     if constexpr (SP2) {
;         PG8_STAGE(PG8_SB(0, 0), cB, voffB); PG8_STAGE(PG8_SB(0, 1), cB + hstepB, voffB); PG8_STAGE(PG8_SA(0, 0), cA, voffA); PG8_STAGE(PG8_SA(0, 1), cA + hstepA, voffA);
;         if (wr == 1) PG8_BAR;
;         PG8_WAIT_V(2); PG8_BAR;
;         PG8_STAGE(PG8_SB(1, 0), cB + kstep, voffB); PG8_STAGE(PG8_SA(1, 0), cA + kstep, voffA); PG8_STAGE(PG8_SB(1, 1), cB + hstepB + kstep, voffB);
;         if (Epi::NST > 0) PG8_WAIT_V(0); else PG8_WAIT_V(6);
;         PG8_BAR;
;     } else {
.LBB0_216:
	v_ashrrev_i32_e32 v4, 31, v12
	v_lshrrev_b32_e32 v4, 26, v4
	v_add_u32_e32 v4, v12, v4
	v_ashrrev_i32_e32 v8, 6, v4
	v_bfe_i32 v4, v12, 27, 1
	v_lshlrev_b32_e32 v3, 4, v12
	v_lshrrev_b32_e32 v4, 22, v4
	v_add_u32_e32 v4, v3, v4
	v_and_b32_e32 v4, 0xfffffc00, v4
	v_sub_u32_e32 v3, v3, v4
	v_lshrrev_b32_e32 v4, 4, v3
	v_bitop3_b32 v3, v4, v3, 32 bitop3:0x6c
	v_ashrrev_i32_e32 v5, 31, v3
	v_lshrrev_b32_e32 v5, 26, v5
	v_lshlrev_b32_e32 v4, 3, v8
	v_add_u32_e32 v5, v3, v5
	v_and_b32_e32 v4, -16, v4
	v_ashrrev_i32_e32 v10, 6, v5
	v_and_b32_e32 v5, 0xc0, v5
	v_readlane_b32 s4, v255, 21
	v_add_u32_e32 v4, v10, v4
	v_lshlrev_b32_e32 v6, 5, v8
	v_sub_u32_e32 v3, v3, v5
	v_mov_b32_e32 v5, 1
	v_readlane_b32 s5, v255, 22
	s_add_u32 s28, s4, s16
	v_and_b32_e32 v9, 32, v6
	v_ashrrev_i16_sdwa v3, v5, sext(v3) dst_sel:DWORD dst_unused:UNUSED_PAD src0_sel:DWORD src1_sel:BYTE_0
	v_lshlrev_b32_e32 v5, 1, v4
	v_lshrrev_b32_e32 v6, 2, v4
	v_and_b32_e32 v7, 3, v10
	s_mov_b32 s0, 0x7fffe0
	s_addc_u32 s29, s5, s17
	s_ashr_i32 s5, s6, 6
	v_bfe_i32 v11, v3, 0, 16
	v_and_b32_e32 v5, 24, v5
	v_and_b32_e32 v6, 4, v6
	v_and_or_b32 v7, v4, s0, v7
	s_movk_i32 s0, 0x1600
	s_ashr_i32 s4, s6, 8
	s_cmp_eq_u32 s4, 0
	s_cbranch_scc0 .Lsp_down
	s_setprio 1
.Lsp_down:
	v_add_u32_e32 v3, v9, v11
	v_or3_b32 v5, v7, v6, v5
	v_mul_lo_u32 v4, v4, s0
	s_lshl_b32 s30, s5, 10
	s_mul_i32 s9, s2, 0x2c0000
	v_add_lshl_u32 v160, v3, v4, 1
	v_mul_u32_u24_e32 v4, 0x1600, v5
	s_mul_hi_i32 s8, s2, 0x2c0000
	s_add_u32 s24, s28, s9
	v_add_lshl_u32 v162, v4, v3, 1
	s_addc_u32 s25, s29, s8
	v_mov_b32_e32 v163, v2
	s_add_i32 s31, s30, 0
	v_lshl_add_u64 v[4:5], s[24:25], 0, v[162:163]
	s_add_i32 m0, s31, 0x10000
	v_lshl_add_u64 v[6:7], v[4:5], 0, s[86:87]
	global_load_lds_dwordx4 v162, s[24:25]
	s_add_i32 m0, s31, 0x12000
	s_mov_b64 s[8:9], 0x160000
	global_load_lds_dwordx4 v[6:7], off
	v_lshl_add_u64 v[6:7], v[4:5], 0, s[8:9]
	s_add_i32 m0, s31, 0x14000
	s_mul_i32 s7, s3, 0x2c0000
	global_load_lds_dwordx4 v[6:7], off
	s_add_i32 m0, s31, 0x16000
	s_mul_hi_i32 s0, s3, 0x2c0000
	s_mov_b64 s[10:11], 0x210000
	s_add_u32 s26, s94, s7
	v_lshl_add_u64 v[6:7], v[4:5], 0, s[10:11]
	s_addc_u32 s27, s95, s0
	v_mov_b32_e32 v161, v2
	global_load_lds_dwordx4 v[6:7], off
	v_lshl_add_u64 v[6:7], s[26:27], 0, v[160:161]
	s_mov_b32 m0, s31
	s_add_i32 s34, s31, 0x2000
	global_load_lds_dwordx4 v160, s[26:27]
	v_lshl_add_u64 v[14:15], v[6:7], 0, s[86:87]
	s_mov_b32 m0, s34
	s_add_i32 s35, s31, 0x4000
	global_load_lds_dwordx4 v[14:15], off
	v_lshl_add_u64 v[14:15], v[6:7], 0, s[8:9]
	s_mov_b32 m0, s35
	s_add_i32 s36, s31, 0x6000
	global_load_lds_dwordx4 v[14:15], off
	v_lshl_add_u64 v[14:15], v[6:7], 0, s[10:11]
	s_mov_b32 m0, s36
	s_cmp_eq_u32 s4, 1
	global_load_lds_dwordx4 v[14:15], off
	s_cselect_b64 s[10:11], -1, 0
	s_cmp_lg_u32 s4, 1
	s_cbranch_scc1 .LBB0_218
	s_barrier

;     __device__ bool next(int i, Unit& u) const { const int rounds = nwg / G; if (i >= rounds) return false; return StaticOrder::next(rounds - 1 - i, u); }
;     __device__ bool next(int i, Unit& u) const { const int rounds = nwg / G; if (i >= 2 * rounds) return false; const bool ok = StaticOrder::next(i >= rounds ? i - rounds : i, u); u.z = (i >= rounds) ? 1 : 0; return ok; }
; template <class Epi, class Sched, bool ALIGN_EPI = false, bool SP2 = false>
; __device__ __forceinline__ void gemm_phase(PG8_LAS unsigned char* lds, const Gemm g, const Sched& S, const Epi& E) {
;     ...
;         const bool has_next = S.next(ui + 1, nxt);
;         const char* nA = has_next ? (const char*)S.opA(g, nxt) + (size_t)nxt.pm * tstepA : cA; const char* nB = has_next ? (const char*)S.opB(g, nxt) + (size_t)nxt.pn * tstepB : cB;
.LBB0_232:
	s_add_i32 s5, 0, 0x10000
	s_add_i32 s42, 0, 0x14000
	v_add_u32_e32 v116, s5, v176
	v_add_u32_e32 v117, s42, v176
	ds_read_b128 v[4:7], v116
	ds_read_b128 v[8:11], v116 offset:1024
	ds_read_b128 v[12:15], v116 offset:2048
	ds_read_b128 v[16:19], v116 offset:3072
	ds_read_b128 v[20:23], v117
	ds_read_b128 v[24:27], v117 offset:1024
	ds_read_b128 v[28:31], v117 offset:2048
	ds_read_b128 v[32:35], v117 offset:3072
	v_lshl_add_u64 v[188:189], s[26:27], 0, v[160:161]
	s_mov_b64 s[62:63], 0x160080
	s_add_i32 s0, s31, 0xc000
	v_lshl_add_u64 v[68:69], v[188:189], 0, s[62:63]
	s_mov_b32 m0, s0
	s_mov_b64 s[64:65], 0x210080
	s_add_i32 s4, s31, 0xe000
	ds_read_b128 v[36:39], v178
	ds_read_b128 v[40:43], v178 offset:1024
	ds_read_b128 v[44:47], v178 offset:2048
	ds_read_b128 v[48:51], v178 offset:3072
	ds_read_b128 v[52:55], v178 offset:4096
	ds_read_b128 v[56:59], v178 offset:5120
	ds_read_b128 v[60:63], v178 offset:6144
	ds_read_b128 v[64:67], v178 offset:7168
	global_load_lds_dwordx4 v[68:69], off
	v_lshl_add_u64 v[68:69], v[188:189], 0, s[64:65]
	s_mov_b32 m0, s4
	s_nop 0
	global_load_lds_dwordx4 v[68:69], off
	s_waitcnt vmcnt(16)
	s_waitcnt lgkmcnt(0)
	s_barrier
	s_waitcnt lgkmcnt(0)
	v_mfma_f32_16x16x32_bf16 v[92:95], v[4:7], v[60:63], 0
	v_mfma_f32_16x16x32_bf16 v[68:71], v[4:7], v[36:39], 0
	v_mfma_f32_16x16x32_bf16 v[72:75], v[12:15], v[36:39], 0
	v_mfma_f32_16x16x32_bf16 v[76:79], v[4:7], v[44:47], 0
	v_mfma_f32_16x16x32_bf16 v[80:83], v[12:15], v[44:47], 0
	v_mfma_f32_16x16x32_bf16 v[84:87], v[4:7], v[52:55], 0
	v_mfma_f32_16x16x32_bf16 v[88:91], v[12:15], v[52:55], 0
	v_mfma_f32_16x16x32_bf16 v[100:103], v[8:11], v[64:67], v[92:95]
	v_mfma_f32_16x16x32_bf16 v[92:95], v[12:15], v[60:63], 0
	v_mfma_f32_16x16x32_bf16 v[68:71], v[8:11], v[40:43], v[68:71]
	v_mfma_f32_16x16x32_bf16 v[72:75], v[16:19], v[40:43], v[72:75]
	v_mfma_f32_16x16x32_bf16 v[76:79], v[8:11], v[48:51], v[76:79]
	v_mfma_f32_16x16x32_bf16 v[80:83], v[16:19], v[48:51], v[80:83]
	v_mfma_f32_16x16x32_bf16 v[84:87], v[8:11], v[56:59], v[84:87]
	v_mfma_f32_16x16x32_bf16 v[88:91], v[16:19], v[56:59], v[88:91]
	v_mfma_f32_16x16x32_bf16 v[104:107], v[16:19], v[64:67], v[92:95]
	v_mfma_f32_16x16x32_bf16 v[92:95], v[20:23], v[36:39], 0
	v_mfma_f32_16x16x32_bf16 v[36:39], v[28:31], v[36:39], 0
	v_mfma_f32_16x16x32_bf16 v[120:123], v[24:27], v[40:43], v[92:95]
	v_mfma_f32_16x16x32_bf16 v[36:39], v[32:35], v[40:43], v[36:39]
	v_mfma_f32_16x16x32_bf16 v[40:43], v[20:23], v[44:47], 0
	v_mfma_f32_16x16x32_bf16 v[44:47], v[28:31], v[44:47], 0
	v_mfma_f32_16x16x32_bf16 v[40:43], v[24:27], v[48:51], v[40:43]
	v_mfma_f32_16x16x32_bf16 v[44:47], v[32:35], v[48:51], v[44:47]
	v_mfma_f32_16x16x32_bf16 v[48:51], v[20:23], v[52:55], 0
	v_mfma_f32_16x16x32_bf16 v[52:55], v[28:31], v[52:55], 0
	v_mfma_f32_16x16x32_bf16 v[48:51], v[24:27], v[56:59], v[48:51]
	v_mfma_f32_16x16x32_bf16 v[52:55], v[32:35], v[56:59], v[52:55]
	v_mfma_f32_16x16x32_bf16 v[56:59], v[20:23], v[60:63], 0
	v_mfma_f32_16x16x32_bf16 v[60:63], v[28:31], v[60:63], 0
	v_mfma_f32_16x16x32_bf16 v[56:59], v[24:27], v[64:67], v[56:59]
	v_mfma_f32_16x16x32_bf16 v[60:63], v[32:35], v[64:67], v[60:63]
	s_barrier
	v_lshl_add_u64 v[214:215], s[24:25], 0, v[162:163]
	s_mov_b64 s[44:45], 0x100
	s_add_i32 s5, s5, s30
	v_lshl_add_u64 v[118:119], v[214:215], 0, s[44:45]
	s_mov_b32 m0, s5
	s_mov_b64 s[46:47], 0xb0100
	s_add_i32 s33, s5, 0x2000
	ds_read_b128 v[64:67], v178 offset:16384
	ds_read_b128 v[92:95], v178 offset:17408
	ds_read_b128 v[96:99], v178 offset:18432
	ds_read_b128 v[108:111], v178 offset:19456
	ds_read_b128 v[112:115], v178 offset:20480
	ds_read_b128 v[124:127], v178 offset:21504
	ds_read_b128 v[128:131], v178 offset:22528
	ds_read_b128 v[132:135], v178 offset:23552
	global_load_lds_dwordx4 v[118:119], off
	v_lshl_add_u64 v[118:119], v[214:215], 0, s[46:47]
	s_mov_b32 m0, s33
	s_mov_b64 s[50:51], 0x160100
	s_add_i32 s42, s42, s30
	global_load_lds_dwordx4 v[118:119], off
	v_lshl_add_u64 v[118:119], v[214:215], 0, s[50:51]
	s_mov_b32 m0, s42
	s_mov_b64 s[52:53], 0x210100
	s_add_i32 s43, s42, 0x2000
	global_load_lds_dwordx4 v[118:119], off
	v_lshl_add_u64 v[118:119], v[214:215], 0, s[52:53]
	s_mov_b32 m0, s43
	s_nop 0
	global_load_lds_dwordx4 v[118:119], off
	v_lshl_add_u64 v[118:119], v[188:189], 0, s[44:45]
	s_mov_b32 m0, s31
	s_nop 0
	global_load_lds_dwordx4 v[118:119], off
	v_lshl_add_u64 v[118:119], v[188:189], 0, s[46:47]
	s_mov_b32 m0, s34
	s_nop 0
	global_load_lds_dwordx4 v[118:119], off
	s_waitcnt vmcnt(16)
	s_waitcnt lgkmcnt(0)
	s_barrier
	s_waitcnt lgkmcnt(0)
	v_mfma_f32_16x16x32_bf16 v[136:139], v[4:7], v[64:67], 0
	v_mfma_f32_16x16x32_bf16 v[144:147], v[8:11], v[92:95], v[136:139]
	v_mfma_f32_16x16x32_bf16 v[136:139], v[12:15], v[64:67], 0
	v_mfma_f32_16x16x32_bf16 v[148:151], v[16:19], v[92:95], v[136:139]
	v_mfma_f32_16x16x32_bf16 v[136:139], v[4:7], v[96:99], 0
	v_mfma_f32_16x16x32_bf16 v[152:155], v[8:11], v[108:111], v[136:139]
	v_mfma_f32_16x16x32_bf16 v[136:139], v[12:15], v[96:99], 0
	v_mfma_f32_16x16x32_bf16 v[156:159], v[16:19], v[108:111], v[136:139]
	v_mfma_f32_16x16x32_bf16 v[136:139], v[4:7], v[112:115], 0
	v_mfma_f32_16x16x32_bf16 v[4:7], v[4:7], v[128:131], 0
	v_mfma_f32_16x16x32_bf16 v[166:169], v[8:11], v[124:127], v[136:139]
	v_mfma_f32_16x16x32_bf16 v[4:7], v[8:11], v[132:135], v[4:7]
	v_mfma_f32_16x16x32_bf16 v[8:11], v[12:15], v[128:131], 0
	v_mfma_f32_16x16x32_bf16 v[136:139], v[12:15], v[112:115], 0
	v_mfma_f32_16x16x32_bf16 v[8:11], v[16:19], v[132:135], v[8:11]
	v_mfma_f32_16x16x32_bf16 v[170:173], v[16:19], v[124:127], v[136:139]
	v_mfma_f32_16x16x32_bf16 v[12:15], v[20:23], v[64:67], 0
	v_mfma_f32_16x16x32_bf16 v[180:183], v[24:27], v[92:95], v[12:15]
	v_mfma_f32_16x16x32_bf16 v[12:15], v[28:31], v[64:67], 0
	v_mfma_f32_16x16x32_bf16 v[190:193], v[32:35], v[92:95], v[12:15]
	v_mfma_f32_16x16x32_bf16 v[12:15], v[20:23], v[96:99], 0
	v_mfma_f32_16x16x32_bf16 v[194:197], v[24:27], v[108:111], v[12:15]
	v_mfma_f32_16x16x32_bf16 v[12:15], v[28:31], v[96:99], 0
	v_mfma_f32_16x16x32_bf16 v[198:201], v[32:35], v[108:111], v[12:15]
	v_mfma_f32_16x16x32_bf16 v[12:15], v[20:23], v[112:115], 0
	v_mfma_f32_16x16x32_bf16 v[202:205], v[24:27], v[124:127], v[12:15]
	v_mfma_f32_16x16x32_bf16 v[12:15], v[28:31], v[112:115], 0
	v_mfma_f32_16x16x32_bf16 v[206:209], v[32:35], v[124:127], v[12:15]
	v_mfma_f32_16x16x32_bf16 v[12:15], v[20:23], v[128:131], 0
	v_mfma_f32_16x16x32_bf16 v[216:219], v[24:27], v[132:135], v[12:15]
	v_mfma_f32_16x16x32_bf16 v[12:15], v[28:31], v[128:131], 0
	v_mfma_f32_16x16x32_bf16 v[132:135], v[32:35], v[132:135], v[12:15]
	s_barrier
; #define PG8_MMA(ai, bj, At, Bt) do { __builtin_amdgcn_s_setprio(1); _Pragma("unroll") for (int m = 0; m < 4; ++m) _Pragma("unroll") for (int n = 0; n < 2; ++n) _Pragma("unroll") for (int k = 0; k < 2; ++k) \
;         acc[ai][bj][m][n] = __builtin_amdgcn_mfma_f32_16x16x32_bf16(Bt[n][k], At[m][k], acc[ai][bj][m][n], 0, 0, 0); __builtin_amdgcn_s_setprio(0); } while (0)
; #define PG8_WAIT_V(n) asm volatile("s_waitcnt vmcnt(" #n ")" ::: "memory")
; #define PG8_TRIP_HEAD(T) const int t = (T); const bool last = (t == nt - 2); \
;             const char* a1 = cA + (size_t)(t + 1) * kstep; \
;             const char* a2 = last ? nA : cA + (size_t)(t + 2) * kstep; const char* b2 = last ? nB : cB + (size_t)(t + 2) * kstep; \
;             const char* a3 = a2 + kstep; const char* b3 = b2 + kstep; \
;             if (last && has_next) S.a_ready(nxt);
; template <class Epi, class Sched, bool ALIGN_EPI = false, bool SP2 = false>
; __device__ __forceinline__ void gemm_phase(PG8_LAS unsigned char* lds, const Gemm g, const Sched& S, const Epi& E) {
;     ...
;         if constexpr (SP2) {
;             { PG8_TRIP_HEAD(0) PG8_TRIP_SP2(asm volatile("s_waitcnt vmcnt(%0)" :: "n"(8 + Epi::NST) : "memory"), PG8_MMAZ) }
;             for (int tt = 2; tt < nt; tt += 2) { PG8_TRIP_HEAD(tt) PG8_TRIP_SP2(PG8_WAIT_V(8), PG8_MMA) }
	s_add_i32 s44, 0, 0x18000
	s_add_i32 s48, 0, 0x1c000
	v_add_u32_e32 v118, s44, v176
	v_add_u32_e32 v119, s48, v176
	s_nop 0
	ds_read_b128 v[12:15], v118
	ds_read_b128 v[16:19], v118 offset:1024
	ds_read_b128 v[20:23], v118 offset:2048
	ds_read_b128 v[24:27], v118 offset:3072
	ds_read_b128 v[220:223], v119
	ds_read_b128 v[224:227], v119 offset:1024
	ds_read_b128 v[228:231], v119 offset:2048
	ds_read_b128 v[232:235], v119 offset:3072
	s_mov_b32 m0, s35
	v_lshl_add_u64 v[92:93], v[188:189], 0, s[50:51]
	ds_read_b128 v[28:31], v178 offset:32768
	ds_read_b128 v[32:35], v178 offset:33792
	ds_read_b128 v[64:67], v178 offset:34816
	ds_read_b128 v[236:239], v178 offset:35840
	ds_read_b128 v[240:243], v178 offset:36864
	ds_read_b128 v[244:247], v178 offset:37888
	ds_read_b128 v[248:251], v178 offset:38912
	ds_read_b128 v[184:187], v178 offset:39936
	global_load_lds_dwordx4 v[92:93], off
	v_lshl_add_u64 v[92:93], v[188:189], 0, s[52:53]
	s_mov_b32 m0, s36
	s_nop 0
	global_load_lds_dwordx4 v[92:93], off
	s_waitcnt vmcnt(8)
	s_waitcnt lgkmcnt(0)
	s_barrier
	s_waitcnt lgkmcnt(0)
	v_mfma_f32_16x16x32_bf16 v[68:71], v[12:15], v[28:31], v[68:71]
	v_mfma_f32_16x16x32_bf16 v[140:143], v[16:19], v[32:35], v[68:71]
	v_mfma_f32_16x16x32_bf16 v[68:71], v[20:23], v[28:31], v[72:75]
	v_mfma_f32_16x16x32_bf16 v[136:139], v[24:27], v[32:35], v[68:71]
	v_mfma_f32_16x16x32_bf16 v[68:71], v[12:15], v[64:67], v[76:79]
	v_mfma_f32_16x16x32_bf16 v[112:115], v[16:19], v[236:239], v[68:71]
	v_mfma_f32_16x16x32_bf16 v[68:71], v[20:23], v[64:67], v[80:83]
	v_mfma_f32_16x16x32_bf16 v[108:111], v[24:27], v[236:239], v[68:71]
	v_mfma_f32_16x16x32_bf16 v[68:71], v[12:15], v[240:243], v[84:87]
	v_mfma_f32_16x16x32_bf16 v[96:99], v[16:19], v[244:247], v[68:71]
	v_mfma_f32_16x16x32_bf16 v[68:71], v[20:23], v[240:243], v[88:91]
	v_mfma_f32_16x16x32_bf16 v[92:95], v[24:27], v[244:247], v[68:71]
	v_mfma_f32_16x16x32_bf16 v[68:71], v[12:15], v[248:251], v[100:103]
	v_mfma_f32_16x16x32_bf16 v[80:83], v[16:19], v[184:187], v[68:71]
	v_mfma_f32_16x16x32_bf16 v[68:71], v[20:23], v[248:251], v[104:107]
	v_mfma_f32_16x16x32_bf16 v[76:79], v[24:27], v[184:187], v[68:71]
	v_mfma_f32_16x16x32_bf16 v[68:71], v[220:223], v[28:31], v[120:123]
	v_mfma_f32_16x16x32_bf16 v[28:31], v[228:231], v[28:31], v[36:39]
	v_mfma_f32_16x16x32_bf16 v[124:127], v[232:235], v[32:35], v[28:31]
	v_mfma_f32_16x16x32_bf16 v[28:31], v[220:223], v[64:67], v[40:43]
	v_mfma_f32_16x16x32_bf16 v[104:107], v[224:227], v[236:239], v[28:31]
	v_mfma_f32_16x16x32_bf16 v[28:31], v[228:231], v[64:67], v[44:47]
	v_mfma_f32_16x16x32_bf16 v[100:103], v[232:235], v[236:239], v[28:31]
	v_mfma_f32_16x16x32_bf16 v[28:31], v[220:223], v[240:243], v[48:51]
	v_mfma_f32_16x16x32_bf16 v[88:91], v[224:227], v[244:247], v[28:31]
	v_mfma_f32_16x16x32_bf16 v[28:31], v[228:231], v[240:243], v[52:55]
	v_mfma_f32_16x16x32_bf16 v[84:87], v[232:235], v[244:247], v[28:31]
	v_mfma_f32_16x16x32_bf16 v[28:31], v[220:223], v[248:251], v[56:59]
	v_mfma_f32_16x16x32_bf16 v[72:75], v[224:227], v[184:187], v[28:31]
	v_mfma_f32_16x16x32_bf16 v[28:31], v[228:231], v[248:251], v[60:63]
	v_mfma_f32_16x16x32_bf16 v[128:131], v[224:227], v[32:35], v[68:71]
	v_mfma_f32_16x16x32_bf16 v[68:71], v[232:235], v[184:187], v[28:31]
	s_barrier
	s_mov_b64 s[50:51], 0x180
	s_add_i32 s44, s44, s30
	s_nop 1
	v_lshl_add_u64 v[28:29], v[214:215], 0, s[50:51]
	s_mov_b32 m0, s44
	s_mov_b64 s[52:53], 0xb0180
	s_add_i32 s45, s44, 0x2000
	ds_read_b128 v[36:39], v178 offset:49152
	ds_read_b128 v[40:43], v178 offset:50176
	ds_read_b128 v[120:123], v178 offset:51200
	ds_read_b128 v[184:187], v178 offset:52224
	ds_read_b128 v[236:239], v178 offset:53248
	ds_read_b128 v[240:243], v178 offset:54272
	ds_read_b128 v[244:247], v178 offset:55296
	ds_read_b128 v[248:251], v178 offset:56320
	global_load_lds_dwordx4 v[28:29], off
	v_lshl_add_u64 v[28:29], v[214:215], 0, s[52:53]
	s_mov_b32 m0, s45
	s_mov_b64 s[46:47], 0x160180
	global_load_lds_dwordx4 v[28:29], off
	v_lshl_add_u64 v[28:29], v[214:215], 0, s[46:47]
	s_add_i32 s46, s48, s30
	s_mov_b32 m0, s46
	s_mov_b64 s[48:49], 0x210180
	s_add_i32 s47, s46, 0x2000
	global_load_lds_dwordx4 v[28:29], off
	v_lshl_add_u64 v[28:29], v[214:215], 0, s[48:49]
	s_mov_b32 m0, s47
	s_nop 0
	global_load_lds_dwordx4 v[28:29], off
	v_lshl_add_u64 v[28:29], v[188:189], 0, s[50:51]
	s_mov_b32 m0, s37
	s_nop 0
	global_load_lds_dwordx4 v[28:29], off
	v_lshl_add_u64 v[28:29], v[188:189], 0, s[52:53]
	s_mov_b32 m0, s38
	s_nop 0
	global_load_lds_dwordx4 v[28:29], off
	s_waitcnt vmcnt(8)
	s_waitcnt lgkmcnt(0)
	s_barrier
	s_waitcnt lgkmcnt(0)
	v_mfma_f32_16x16x32_bf16 v[28:31], v[12:15], v[36:39], v[144:147]
	v_mfma_f32_16x16x32_bf16 v[56:59], v[16:19], v[40:43], v[28:31]
	v_mfma_f32_16x16x32_bf16 v[28:31], v[20:23], v[36:39], v[148:151]
	v_mfma_f32_16x16x32_bf16 v[52:55], v[24:27], v[40:43], v[28:31]
	v_mfma_f32_16x16x32_bf16 v[28:31], v[12:15], v[120:123], v[152:155]
	v_mfma_f32_16x16x32_bf16 v[48:51], v[16:19], v[184:187], v[28:31]
	v_mfma_f32_16x16x32_bf16 v[28:31], v[20:23], v[120:123], v[156:159]
	v_mfma_f32_16x16x32_bf16 v[44:47], v[24:27], v[184:187], v[28:31]
	v_mfma_f32_16x16x32_bf16 v[28:31], v[12:15], v[236:239], v[166:169]
	v_mfma_f32_16x16x32_bf16 v[4:7], v[12:15], v[244:247], v[4:7]
	v_mfma_f32_16x16x32_bf16 v[32:35], v[16:19], v[240:243], v[28:31]
	v_mfma_f32_16x16x32_bf16 v[28:31], v[20:23], v[236:239], v[170:173]
	v_mfma_f32_16x16x32_bf16 v[16:19], v[16:19], v[248:251], v[4:7]
	v_mfma_f32_16x16x32_bf16 v[4:7], v[20:23], v[244:247], v[8:11]
	v_mfma_f32_16x16x32_bf16 v[28:31], v[24:27], v[240:243], v[28:31]
	v_mfma_f32_16x16x32_bf16 v[12:15], v[24:27], v[248:251], v[4:7]
	v_mfma_f32_16x16x32_bf16 v[4:7], v[220:223], v[36:39], v[180:183]
	v_mfma_f32_16x16x32_bf16 v[64:67], v[224:227], v[40:43], v[4:7]
	v_mfma_f32_16x16x32_bf16 v[4:7], v[228:231], v[36:39], v[190:193]
	v_mfma_f32_16x16x32_bf16 v[60:63], v[232:235], v[40:43], v[4:7]
	v_mfma_f32_16x16x32_bf16 v[4:7], v[220:223], v[120:123], v[194:197]
	v_mfma_f32_16x16x32_bf16 v[40:43], v[224:227], v[184:187], v[4:7]
	v_mfma_f32_16x16x32_bf16 v[4:7], v[228:231], v[120:123], v[198:201]
	v_mfma_f32_16x16x32_bf16 v[36:39], v[232:235], v[184:187], v[4:7]
	v_mfma_f32_16x16x32_bf16 v[4:7], v[220:223], v[236:239], v[202:205]
	v_mfma_f32_16x16x32_bf16 v[24:27], v[224:227], v[240:243], v[4:7]
	v_mfma_f32_16x16x32_bf16 v[4:7], v[228:231], v[236:239], v[206:209]
	v_mfma_f32_16x16x32_bf16 v[20:23], v[232:235], v[240:243], v[4:7]
	v_mfma_f32_16x16x32_bf16 v[4:7], v[220:223], v[244:247], v[216:219]
	v_mfma_f32_16x16x32_bf16 v[8:11], v[224:227], v[248:251], v[4:7]
	v_mfma_f32_16x16x32_bf16 v[4:7], v[228:231], v[244:247], v[132:135]
	v_mfma_f32_16x16x32_bf16 v[4:7], v[232:235], v[248:251], v[4:7]
	s_barrier
	s_add_u32 s26, s26, 0x160180
	s_addc_u32 s27, s27, 0
	s_add_u32 s24, s24, 0x200
	s_addc_u32 s25, s25, 0
	s_mov_b32 s48, 0
	s_mov_b64 s[54:55], 0x160000
	s_mov_b64 s[56:57], 0x210000
	s_mov_b64 s[60:61], 0xb0080
.LBB0_233:
	ds_read_b128 v[120:123], v116
	ds_read_b128 v[132:135], v116 offset:1024
	ds_read_b128 v[144:147], v116 offset:2048
	ds_read_b128 v[148:151], v116 offset:3072
	ds_read_b128 v[152:155], v117
	ds_read_b128 v[156:159], v117 offset:1024
	ds_read_b128 v[166:169], v117 offset:2048
	ds_read_b128 v[170:173], v117 offset:3072
	s_add_u32 s49, s26, 0xffea0080
	s_addc_u32 s50, s27, -1
	s_cmpk_eq_i32 s48, 0x54
	s_cselect_b32 s51, s21, s50
	s_cselect_b32 s50, s20, s49
	s_cselect_b32 s53, s23, s25
	s_cselect_b32 s52, s22, s24
	s_mov_b32 m0, s0
	v_lshl_add_u64 v[188:189], s[26:27], 0, v[164:165]
	ds_read_b128 v[180:183], v178
	ds_read_b128 v[184:187], v178 offset:1024
	ds_read_b128 v[190:193], v178 offset:2048
	ds_read_b128 v[194:197], v178 offset:3072
	ds_read_b128 v[198:201], v178 offset:4096
	ds_read_b128 v[202:205], v178 offset:5120
	ds_read_b128 v[206:209], v178 offset:6144
	ds_read_b128 v[216:219], v178 offset:7168
	global_load_lds_dwordx4 v[188:189], off
	v_lshl_add_u64 v[188:189], v[188:189], 0, s[86:87]
	s_mov_b32 m0, s4
	s_nop 0
	global_load_lds_dwordx4 v[188:189], off
	s_waitcnt vmcnt(8)
	s_waitcnt lgkmcnt(0)
	s_barrier
	s_waitcnt lgkmcnt(0)
	v_mfma_f32_16x16x32_bf16 v[140:143], v[120:123], v[180:183], v[140:143]
	v_mfma_f32_16x16x32_bf16 v[136:139], v[144:147], v[180:183], v[136:139]
	v_mfma_f32_16x16x32_bf16 v[112:115], v[120:123], v[190:193], v[112:115]
	v_mfma_f32_16x16x32_bf16 v[108:111], v[144:147], v[190:193], v[108:111]
	v_mfma_f32_16x16x32_bf16 v[96:99], v[120:123], v[198:201], v[96:99]
	v_mfma_f32_16x16x32_bf16 v[92:95], v[144:147], v[198:201], v[92:95]
	v_mfma_f32_16x16x32_bf16 v[80:83], v[120:123], v[206:209], v[80:83]
	v_mfma_f32_16x16x32_bf16 v[76:79], v[144:147], v[206:209], v[76:79]
	v_mfma_f32_16x16x32_bf16 v[140:143], v[132:135], v[184:187], v[140:143]
	v_mfma_f32_16x16x32_bf16 v[136:139], v[148:151], v[184:187], v[136:139]
	v_mfma_f32_16x16x32_bf16 v[112:115], v[132:135], v[194:197], v[112:115]
	v_mfma_f32_16x16x32_bf16 v[108:111], v[148:151], v[194:197], v[108:111]
	v_mfma_f32_16x16x32_bf16 v[96:99], v[132:135], v[202:205], v[96:99]
	v_mfma_f32_16x16x32_bf16 v[92:95], v[148:151], v[202:205], v[92:95]
	v_mfma_f32_16x16x32_bf16 v[80:83], v[132:135], v[216:219], v[80:83]
	v_mfma_f32_16x16x32_bf16 v[76:79], v[148:151], v[216:219], v[76:79]
	v_mfma_f32_16x16x32_bf16 v[128:131], v[152:155], v[180:183], v[128:131]
	v_mfma_f32_16x16x32_bf16 v[124:127], v[166:169], v[180:183], v[124:127]
	v_mfma_f32_16x16x32_bf16 v[104:107], v[152:155], v[190:193], v[104:107]
	v_mfma_f32_16x16x32_bf16 v[100:103], v[166:169], v[190:193], v[100:103]
	v_mfma_f32_16x16x32_bf16 v[88:91], v[152:155], v[198:201], v[88:91]
	v_mfma_f32_16x16x32_bf16 v[84:87], v[166:169], v[198:201], v[84:87]
	v_mfma_f32_16x16x32_bf16 v[72:75], v[152:155], v[206:209], v[72:75]
	v_mfma_f32_16x16x32_bf16 v[68:71], v[166:169], v[206:209], v[68:71]
	v_mfma_f32_16x16x32_bf16 v[128:131], v[156:159], v[184:187], v[128:131]
	v_mfma_f32_16x16x32_bf16 v[124:127], v[170:173], v[184:187], v[124:127]
	v_mfma_f32_16x16x32_bf16 v[104:107], v[156:159], v[194:197], v[104:107]
	v_mfma_f32_16x16x32_bf16 v[100:103], v[170:173], v[194:197], v[100:103]
	v_mfma_f32_16x16x32_bf16 v[88:91], v[156:159], v[202:205], v[88:91]
	v_mfma_f32_16x16x32_bf16 v[84:87], v[170:173], v[202:205], v[84:87]
	v_mfma_f32_16x16x32_bf16 v[72:75], v[156:159], v[216:219], v[72:75]
	v_mfma_f32_16x16x32_bf16 v[68:71], v[170:173], v[216:219], v[68:71]
	s_barrier
	s_mov_b32 m0, s5
	v_lshl_add_u64 v[188:189], s[52:53], 0, v[162:163]
	ds_read_b128 v[180:183], v178 offset:16384
	ds_read_b128 v[184:187], v178 offset:17408
	ds_read_b128 v[190:193], v178 offset:18432
	ds_read_b128 v[194:197], v178 offset:19456
	ds_read_b128 v[198:201], v178 offset:20480
	ds_read_b128 v[202:205], v178 offset:21504
	ds_read_b128 v[206:209], v178 offset:22528
	ds_read_b128 v[216:219], v178 offset:23552
	global_load_lds_dwordx4 v[188:189], off
	v_lshl_add_u64 v[214:215], v[188:189], 0, s[86:87]
	s_mov_b32 m0, s33
	s_nop 0
	global_load_lds_dwordx4 v[214:215], off
	v_lshl_add_u64 v[214:215], v[188:189], 0, s[54:55]
	s_mov_b32 m0, s42
	s_nop 0
	global_load_lds_dwordx4 v[214:215], off
	v_lshl_add_u64 v[214:215], v[188:189], 0, s[56:57]
	s_mov_b32 m0, s43
	s_nop 0
	global_load_lds_dwordx4 v[214:215], off
	v_lshl_add_u64 v[214:215], s[50:51], 0, v[160:161]
	s_mov_b32 m0, s31
	v_lshl_add_u64 v[220:221], v[214:215], 0, s[86:87]
	global_load_lds_dwordx4 v[214:215], off
	s_mov_b32 m0, s34
	s_nop 0
	global_load_lds_dwordx4 v[220:221], off
	s_waitcnt vmcnt(8)
	s_waitcnt lgkmcnt(0)
	s_barrier
; #define PG8_MMA(ai, bj, At, Bt) do { __builtin_amdgcn_s_setprio(1); _Pragma("unroll") for (int m = 0; m < 4; ++m) _Pragma("unroll") for (int n = 0; n < 2; ++n) _Pragma("unroll") for (int k = 0; k < 2; ++k) \
;         acc[ai][bj][m][n] = __builtin_amdgcn_mfma_f32_16x16x32_bf16(Bt[n][k], At[m][k], acc[ai][bj][m][n], 0, 0, 0); __builtin_amdgcn_s_setprio(0); } while (0)
; #define PG8_WAIT_V(n) asm volatile("s_waitcnt vmcnt(" #n ")" ::: "memory")
; #define PG8_TRIP_HEAD(T) const int t = (T); const bool last = (t == nt - 2); \
;             const char* a1 = cA + (size_t)(t + 1) * kstep; \
;             const char* a2 = last ? nA : cA + (size_t)(t + 2) * kstep; const char* b2 = last ? nB : cB + (size_t)(t + 2) * kstep; \
;             const char* a3 = a2 + kstep; const char* b3 = b2 + kstep; \
;             if (last && has_next) S.a_ready(nxt);
; template <class Epi, class Sched, bool ALIGN_EPI = false, bool SP2 = false>
; __device__ __forceinline__ void gemm_phase(PG8_LAS unsigned char* lds, const Gemm g, const Sched& S, const Epi& E) {
;     ...
;         if constexpr (SP2) {
;             { PG8_TRIP_HEAD(0) PG8_TRIP_SP2(asm volatile("s_waitcnt vmcnt(%0)" :: "n"(8 + Epi::NST) : "memory"), PG8_MMAZ) }
;             for (int tt = 2; tt < nt; tt += 2) { PG8_TRIP_HEAD(tt) PG8_TRIP_SP2(PG8_WAIT_V(8), PG8_MMA) }
	s_waitcnt lgkmcnt(0)
	v_mfma_f32_16x16x32_bf16 v[56:59], v[120:123], v[180:183], v[56:59]
	v_mfma_f32_16x16x32_bf16 v[52:55], v[144:147], v[180:183], v[52:55]
	v_mfma_f32_16x16x32_bf16 v[48:51], v[120:123], v[190:193], v[48:51]
	v_mfma_f32_16x16x32_bf16 v[44:47], v[144:147], v[190:193], v[44:47]
	v_mfma_f32_16x16x32_bf16 v[32:35], v[120:123], v[198:201], v[32:35]
	v_mfma_f32_16x16x32_bf16 v[28:31], v[144:147], v[198:201], v[28:31]
	v_mfma_f32_16x16x32_bf16 v[16:19], v[120:123], v[206:209], v[16:19]
	v_mfma_f32_16x16x32_bf16 v[12:15], v[144:147], v[206:209], v[12:15]
	v_mfma_f32_16x16x32_bf16 v[56:59], v[132:135], v[184:187], v[56:59]
	v_mfma_f32_16x16x32_bf16 v[52:55], v[148:151], v[184:187], v[52:55]
	v_mfma_f32_16x16x32_bf16 v[48:51], v[132:135], v[194:197], v[48:51]
	v_mfma_f32_16x16x32_bf16 v[44:47], v[148:151], v[194:197], v[44:47]
	v_mfma_f32_16x16x32_bf16 v[32:35], v[132:135], v[202:205], v[32:35]
	v_mfma_f32_16x16x32_bf16 v[28:31], v[148:151], v[202:205], v[28:31]
	v_mfma_f32_16x16x32_bf16 v[16:19], v[132:135], v[216:219], v[16:19]
	v_mfma_f32_16x16x32_bf16 v[12:15], v[148:151], v[216:219], v[12:15]
	v_mfma_f32_16x16x32_bf16 v[64:67], v[152:155], v[180:183], v[64:67]
	v_mfma_f32_16x16x32_bf16 v[60:63], v[166:169], v[180:183], v[60:63]
	v_mfma_f32_16x16x32_bf16 v[40:43], v[152:155], v[190:193], v[40:43]
	v_mfma_f32_16x16x32_bf16 v[36:39], v[166:169], v[190:193], v[36:39]
	v_mfma_f32_16x16x32_bf16 v[24:27], v[152:155], v[198:201], v[24:27]
	v_mfma_f32_16x16x32_bf16 v[20:23], v[166:169], v[198:201], v[20:23]
	v_mfma_f32_16x16x32_bf16 v[8:11], v[152:155], v[206:209], v[8:11]
	v_mfma_f32_16x16x32_bf16 v[4:7], v[166:169], v[206:209], v[4:7]
	v_mfma_f32_16x16x32_bf16 v[64:67], v[156:159], v[184:187], v[64:67]
	v_mfma_f32_16x16x32_bf16 v[60:63], v[170:173], v[184:187], v[60:63]
	v_mfma_f32_16x16x32_bf16 v[40:43], v[156:159], v[194:197], v[40:43]
	v_mfma_f32_16x16x32_bf16 v[36:39], v[170:173], v[194:197], v[36:39]
	v_mfma_f32_16x16x32_bf16 v[24:27], v[156:159], v[202:205], v[24:27]
	v_mfma_f32_16x16x32_bf16 v[20:23], v[170:173], v[202:205], v[20:23]
	v_mfma_f32_16x16x32_bf16 v[8:11], v[156:159], v[216:219], v[8:11]
	v_mfma_f32_16x16x32_bf16 v[4:7], v[170:173], v[216:219], v[4:7]
	s_barrier
	ds_read_b128 v[120:123], v118
	ds_read_b128 v[132:135], v118 offset:1024
	ds_read_b128 v[144:147], v118 offset:2048
	ds_read_b128 v[148:151], v118 offset:3072
	ds_read_b128 v[152:155], v119
	ds_read_b128 v[156:159], v119 offset:1024
	ds_read_b128 v[166:169], v119 offset:2048
	ds_read_b128 v[170:173], v119 offset:3072
	s_mov_b32 m0, s35
	v_lshl_add_u64 v[220:221], v[214:215], 0, s[54:55]
	ds_read_b128 v[180:183], v178 offset:32768
	ds_read_b128 v[184:187], v178 offset:33792
	ds_read_b128 v[190:193], v178 offset:34816
	ds_read_b128 v[194:197], v178 offset:35840
	ds_read_b128 v[198:201], v178 offset:36864
	ds_read_b128 v[202:205], v178 offset:37888
	ds_read_b128 v[206:209], v178 offset:38912
	ds_read_b128 v[216:219], v178 offset:39936
	global_load_lds_dwordx4 v[220:221], off
	v_lshl_add_u64 v[220:221], v[214:215], 0, s[56:57]
	s_mov_b32 m0, s36
	s_nop 0
	global_load_lds_dwordx4 v[220:221], off
	s_waitcnt vmcnt(8)
	s_waitcnt lgkmcnt(0)
	s_barrier
	s_waitcnt lgkmcnt(0)
	v_mfma_f32_16x16x32_bf16 v[140:143], v[120:123], v[180:183], v[140:143]
	v_mfma_f32_16x16x32_bf16 v[136:139], v[144:147], v[180:183], v[136:139]
	v_mfma_f32_16x16x32_bf16 v[112:115], v[120:123], v[190:193], v[112:115]
	v_mfma_f32_16x16x32_bf16 v[108:111], v[144:147], v[190:193], v[108:111]
	v_mfma_f32_16x16x32_bf16 v[96:99], v[120:123], v[198:201], v[96:99]
	v_mfma_f32_16x16x32_bf16 v[92:95], v[144:147], v[198:201], v[92:95]
	v_mfma_f32_16x16x32_bf16 v[80:83], v[120:123], v[206:209], v[80:83]
	v_mfma_f32_16x16x32_bf16 v[76:79], v[144:147], v[206:209], v[76:79]
	v_mfma_f32_16x16x32_bf16 v[140:143], v[132:135], v[184:187], v[140:143]
	v_mfma_f32_16x16x32_bf16 v[136:139], v[148:151], v[184:187], v[136:139]
	v_mfma_f32_16x16x32_bf16 v[112:115], v[132:135], v[194:197], v[112:115]
	v_mfma_f32_16x16x32_bf16 v[108:111], v[148:151], v[194:197], v[108:111]
	v_mfma_f32_16x16x32_bf16 v[96:99], v[132:135], v[202:205], v[96:99]
	v_mfma_f32_16x16x32_bf16 v[92:95], v[148:151], v[202:205], v[92:95]
	v_mfma_f32_16x16x32_bf16 v[80:83], v[132:135], v[216:219], v[80:83]
	v_mfma_f32_16x16x32_bf16 v[76:79], v[148:151], v[216:219], v[76:79]
	v_mfma_f32_16x16x32_bf16 v[128:131], v[152:155], v[180:183], v[128:131]
	v_mfma_f32_16x16x32_bf16 v[124:127], v[166:169], v[180:183], v[124:127]
	v_mfma_f32_16x16x32_bf16 v[104:107], v[152:155], v[190:193], v[104:107]
	v_mfma_f32_16x16x32_bf16 v[100:103], v[166:169], v[190:193], v[100:103]
	v_mfma_f32_16x16x32_bf16 v[88:91], v[152:155], v[198:201], v[88:91]
	v_mfma_f32_16x16x32_bf16 v[84:87], v[166:169], v[198:201], v[84:87]
	v_mfma_f32_16x16x32_bf16 v[72:75], v[152:155], v[206:209], v[72:75]
	v_mfma_f32_16x16x32_bf16 v[68:71], v[166:169], v[206:209], v[68:71]
	v_mfma_f32_16x16x32_bf16 v[128:131], v[156:159], v[184:187], v[128:131]
	v_mfma_f32_16x16x32_bf16 v[124:127], v[170:173], v[184:187], v[124:127]
	v_mfma_f32_16x16x32_bf16 v[104:107], v[156:159], v[194:197], v[104:107]
	v_mfma_f32_16x16x32_bf16 v[100:103], v[170:173], v[194:197], v[100:103]
	v_mfma_f32_16x16x32_bf16 v[88:91], v[156:159], v[202:205], v[88:91]
	v_mfma_f32_16x16x32_bf16 v[84:87], v[170:173], v[202:205], v[84:87]
	v_mfma_f32_16x16x32_bf16 v[72:75], v[156:159], v[216:219], v[72:75]
	v_mfma_f32_16x16x32_bf16 v[68:71], v[170:173], v[216:219], v[68:71]
	s_barrier
; #define PG8_MMA(ai, bj, At, Bt) do { __builtin_amdgcn_s_setprio(1); _Pragma("unroll") for (int m = 0; m < 4; ++m) _Pragma("unroll") for (int n = 0; n < 2; ++n) _Pragma("unroll") for (int k = 0; k < 2; ++k) \
;         acc[ai][bj][m][n] = __builtin_amdgcn_mfma_f32_16x16x32_bf16(Bt[n][k], At[m][k], acc[ai][bj][m][n], 0, 0, 0); __builtin_amdgcn_s_setprio(0); } while (0)
; #define PG8_WAIT_V(n) asm volatile("s_waitcnt vmcnt(" #n ")" ::: "memory")
; #define PG8_BAR __builtin_amdgcn_s_barrier()
; #define PG8_TRIP_HEAD(T) const int t = (T); const bool last = (t == nt - 2); \
;             const char* a1 = cA + (size_t)(t + 1) * kstep; \
;             const char* a2 = last ? nA : cA + (size_t)(t + 2) * kstep; const char* b2 = last ? nB : cB + (size_t)(t + 2) * kstep; \
;             const char* a3 = a2 + kstep; const char* b3 = b2 + kstep; \
;             if (last && has_next) S.a_ready(nxt);
; template <class Epi, class Sched, bool ALIGN_EPI = false, bool SP2 = false>
; __device__ __forceinline__ void gemm_phase(PG8_LAS unsigned char* lds, const Gemm g, const Sched& S, const Epi& E) {
;     ...
;         if constexpr (SP2) {
;             { PG8_TRIP_HEAD(0) PG8_TRIP_SP2(asm volatile("s_waitcnt vmcnt(%0)" :: "n"(8 + Epi::NST) : "memory"), PG8_MMAZ) }
;             for (int tt = 2; tt < nt; tt += 2) { PG8_TRIP_HEAD(tt) PG8_TRIP_SP2(PG8_WAIT_V(8), PG8_MMA) }
;     ...
;         if constexpr (ALIGN_EPI) { if (wr == 0) PG8_BAR; }
	s_mov_b32 m0, s44
	v_lshl_add_u64 v[220:221], v[188:189], 0, s[78:79]
	ds_read_b128 v[180:183], v178 offset:49152
	ds_read_b128 v[184:187], v178 offset:50176
	ds_read_b128 v[190:193], v178 offset:51200
	ds_read_b128 v[194:197], v178 offset:52224
	ds_read_b128 v[198:201], v178 offset:53248
	ds_read_b128 v[202:205], v178 offset:54272
	ds_read_b128 v[206:209], v178 offset:55296
	ds_read_b128 v[216:219], v178 offset:56320
	global_load_lds_dwordx4 v[220:221], off
	v_lshl_add_u64 v[220:221], v[188:189], 0, s[60:61]
	s_mov_b32 m0, s45
	s_nop 0
	global_load_lds_dwordx4 v[220:221], off
	v_lshl_add_u64 v[220:221], v[188:189], 0, s[62:63]
	s_mov_b32 m0, s46
	v_lshl_add_u64 v[188:189], v[188:189], 0, s[64:65]
	global_load_lds_dwordx4 v[220:221], off
	s_mov_b32 m0, s47
	s_nop 0
	global_load_lds_dwordx4 v[188:189], off
	v_lshl_add_u64 v[188:189], v[214:215], 0, s[78:79]
	s_mov_b32 m0, s37
	s_nop 0
	global_load_lds_dwordx4 v[188:189], off
	v_lshl_add_u64 v[188:189], v[214:215], 0, s[60:61]
	s_mov_b32 m0, s38
	s_nop 0
	global_load_lds_dwordx4 v[188:189], off
	s_waitcnt vmcnt(8)
	s_waitcnt lgkmcnt(0)
	s_barrier
	s_waitcnt lgkmcnt(0)
	v_mfma_f32_16x16x32_bf16 v[56:59], v[120:123], v[180:183], v[56:59]
	v_mfma_f32_16x16x32_bf16 v[52:55], v[144:147], v[180:183], v[52:55]
	v_mfma_f32_16x16x32_bf16 v[48:51], v[120:123], v[190:193], v[48:51]
	v_mfma_f32_16x16x32_bf16 v[44:47], v[144:147], v[190:193], v[44:47]
	v_mfma_f32_16x16x32_bf16 v[32:35], v[120:123], v[198:201], v[32:35]
	v_mfma_f32_16x16x32_bf16 v[28:31], v[144:147], v[198:201], v[28:31]
	v_mfma_f32_16x16x32_bf16 v[16:19], v[120:123], v[206:209], v[16:19]
	v_mfma_f32_16x16x32_bf16 v[12:15], v[144:147], v[206:209], v[12:15]
	v_mfma_f32_16x16x32_bf16 v[56:59], v[132:135], v[184:187], v[56:59]
	v_mfma_f32_16x16x32_bf16 v[52:55], v[148:151], v[184:187], v[52:55]
	v_mfma_f32_16x16x32_bf16 v[48:51], v[132:135], v[194:197], v[48:51]
	v_mfma_f32_16x16x32_bf16 v[44:47], v[148:151], v[194:197], v[44:47]
	v_mfma_f32_16x16x32_bf16 v[32:35], v[132:135], v[202:205], v[32:35]
	v_mfma_f32_16x16x32_bf16 v[28:31], v[148:151], v[202:205], v[28:31]
	v_mfma_f32_16x16x32_bf16 v[16:19], v[132:135], v[216:219], v[16:19]
	v_mfma_f32_16x16x32_bf16 v[12:15], v[148:151], v[216:219], v[12:15]
	v_mfma_f32_16x16x32_bf16 v[64:67], v[152:155], v[180:183], v[64:67]
	v_mfma_f32_16x16x32_bf16 v[60:63], v[166:169], v[180:183], v[60:63]
	v_mfma_f32_16x16x32_bf16 v[40:43], v[152:155], v[190:193], v[40:43]
	v_mfma_f32_16x16x32_bf16 v[36:39], v[166:169], v[190:193], v[36:39]
	v_mfma_f32_16x16x32_bf16 v[24:27], v[152:155], v[198:201], v[24:27]
	v_mfma_f32_16x16x32_bf16 v[20:23], v[166:169], v[198:201], v[20:23]
	v_mfma_f32_16x16x32_bf16 v[8:11], v[152:155], v[206:209], v[8:11]
	v_mfma_f32_16x16x32_bf16 v[4:7], v[166:169], v[206:209], v[4:7]
	v_mfma_f32_16x16x32_bf16 v[64:67], v[156:159], v[184:187], v[64:67]
	v_mfma_f32_16x16x32_bf16 v[60:63], v[170:173], v[184:187], v[60:63]
	v_mfma_f32_16x16x32_bf16 v[40:43], v[156:159], v[194:197], v[40:43]
	v_mfma_f32_16x16x32_bf16 v[36:39], v[170:173], v[194:197], v[36:39]
	v_mfma_f32_16x16x32_bf16 v[24:27], v[156:159], v[202:205], v[24:27]
	v_mfma_f32_16x16x32_bf16 v[20:23], v[170:173], v[202:205], v[20:23]
	v_mfma_f32_16x16x32_bf16 v[8:11], v[156:159], v[216:219], v[8:11]
	v_mfma_f32_16x16x32_bf16 v[4:7], v[170:173], v[216:219], v[4:7]
	s_barrier
	s_add_i32 s48, s48, 2
	s_add_u32 s26, s26, 0x100
	s_addc_u32 s27, s27, 0
	s_add_u32 s24, s24, 0x100
	s_addc_u32 s25, s25, 0
	s_cmpk_gt_u32 s48, 0x55
	s_cbranch_scc0 .LBB0_233
	s_and_b64 vcc, exec, s[18:19]
	s_cbranch_vccz .LBB0_236
	s_barrier

; #define PG8_WAIT_V(n) asm volatile("s_waitcnt vmcnt(" #n ")" ::: "memory")
; #define PG8_BAR __builtin_amdgcn_s_barrier()
; __device__ __forceinline__ unsigned xb_xcc_id() { return (unsigned)__builtin_amdgcn_s_getreg((3 << 11) | 20) & 0xFu; }
; template <class Epi, class Sched, bool ALIGN_EPI = false, bool SP2 = false>
; __device__ __forceinline__ void gemm_phase(PG8_LAS unsigned char* lds, const Gemm g, const Sched& S, const Epi& E) {
;     ...
;     PG8_WAIT_V(0);
;     if constexpr (!ALIGN_EPI) { if (wr == 0) PG8_BAR; }
;     PG8_BAR;
; __device__ __forceinline__ void xcd_barrier(const XcdBarrier& b) {
;     asm volatile("s_waitcnt vmcnt(0)" ::: "memory");
;     __syncthreads();
;     if (threadIdx.x == 0) {
;         unsigned* bar = b.bar; const unsigned bx_ = xb_xcc_id();
;         __builtin_amdgcn_s_waitcnt(0);
;         unsigned nloc = b.st[0], nx = b.st[1];
;         if (nloc == 0u) { xcd_barrier_complete(bar, bx_, nloc, nx); b.st[0] = nloc; b.st[1] = nx; }
.LBB0_256:
	s_setprio 0
	s_waitcnt vmcnt(0)
	s_barrier
	s_mov_b64 s[6:7], exec
	v_readlane_b32 s2, v252, 15
	v_readlane_b32 s3, v252, 16
	s_and_b64 s[2:3], s[6:7], s[2:3]
	s_mov_b64 exec, s[2:3]
	s_cbranch_execz .LBB0_308
	v_readlane_b32 s2, v255, 32
	s_getreg_b32 s0, hwreg(HW_REG_XCC_ID, 0, 4)
	s_waitcnt vmcnt(0) expcnt(0) lgkmcnt(0)
	v_mov_b32_e32 v3, s2
	ds_read_b32 v5, v3
	v_readlane_b32 s2, v255, 33
	s_and_b32 s0, s0, 15
	s_waitcnt lgkmcnt(0)
	v_cmp_ne_u32_e32 vcc, 0, v5
	v_mov_b32_e32 v3, s2
	ds_read_b32 v4, v3
	s_cbranch_vccnz .LBB0_272
	v_readlane_b32 s4, v252, 8
	v_readlane_b32 s5, v252, 9
	s_load_dwordx2 s[2:3], s[4:5], 0x4
	v_readlane_b32 s4, v252, 10
	v_readlane_b32 s5, v252, 11
	s_waitcnt lgkmcnt(0)
	s_mul_i32 s2, s2, s4
	s_mul_i32 s2, s2, s3
	s_mov_b32 s3, 1
	s_branch .LBB0_260

;     __device__ bool next(int i, Unit& u) const { const int rounds = nwg / G; if (i >= rounds) return false; return StaticOrder::next(rounds - 1 - i, u); }
; #define PG8_WAIT_V(n) asm volatile("s_waitcnt vmcnt(" #n ")" ::: "memory")
; template <class Epi, class Sched, bool ALIGN_EPI = false, bool SP2 = false>
; __device__ __forceinline__ void gemm_phase(PG8_LAS unsigned char* lds, const Gemm g, const Sched& S, const Epi& E) {
;     ...
;     { int R, C; stage_rc(tid * 16, R, C); const int Rb = Epi::PERM ? ((R & ~31) + perm32(R & 31)) : R;
;         voffA = (unsigned)(R * g.lda + C) * 2u; voffB = (unsigned)(Rb * g.ldb + C) * 2u; }
;     const size_t voffA_step = (size_t)64 * g.lda * 2, voffB_step = (size_t)64 * g.ldb * 2;
;     const size_t kstep = (size_t)(BK * 2);
;     const size_t hstepA = (size_t)HALF * g.lda * 2, hstepB = (size_t)HALF * g.ldb * 2;
;     const size_t tstepA = 2 * hstepA, tstepB = 2 * hstepB;
;     const unsigned ldsw = (unsigned)wid * 1024u;
;     const int aoff = lds_byte(wr * 64 + fr, fq * 8), boff = lds_byte(wc * 32 + fr, fq * 8);
;     ...
;     Unit cur, nxt; int ui = 0;
;     if (!S.next(0, cur)) return;
;     f32x4 acc[2][2][4][2];
;     if constexpr (!SP2) {
; #pragma unroll
;     for (int a = 0; a < 2; ++a)
; #pragma unroll
;         for (int b = 0; b < 2; ++b)
; #pragma unroll
;             for (int m = 0; m < 4; ++m)
; #pragma unroll
;                 for (int n = 0; n < 2; ++n) acc[a][b][m][n] = (f32x4){0.f, 0.f, 0.f, 0.f};
;     }
;     bf16x8 At[4][2], B0[2][2], B1[2][2];
;     const char* cA = (const char*)S.opA(g, cur) + (size_t)cur.pm * tstepA; const char* cB = (const char*)S.opB(g, cur) + (size_t)cur.pn * tstepB;
;     S.a_ready(cur);
;     if constexpr (SP2) {
;         PG8_STAGE(PG8_SB(0, 0), cB, voffB); PG8_STAGE(PG8_SB(0, 1), cB + hstepB, voffB); PG8_STAGE(PG8_SA(0, 0), cA, voffA); PG8_STAGE(PG8_SA(0, 1), cA + hstepA, voffA);
;         if (wr == 1) PG8_BAR;
;         PG8_WAIT_V(2); PG8_BAR;
;         PG8_STAGE(PG8_SB(1, 0), cB + kstep, voffB); PG8_STAGE(PG8_SA(1, 0), cA + kstep, voffA); PG8_STAGE(PG8_SB(1, 1), cB + hstepB + kstep, voffB);
;         if (Epi::NST > 0) PG8_WAIT_V(0); else PG8_WAIT_V(6);
;         PG8_BAR;
;     } else {
;         PG8_STAGE(PG8_SB(0, 0), cB, voffB); PG8_STAGE(PG8_SA(0, 0), cA, voffA); PG8_STAGE(PG8_SB(0, 1), cB + hstepB, voffB); PG8_STAGE(PG8_SA(0, 1), cA + hstepA, voffA);
;         if (wr == 1) PG8_BAR;
.LBB0_308:
	s_or_b64 exec, exec, s[6:7]
	s_andn2_b64 vcc, exec, s[12:13]
	s_waitcnt lgkmcnt(0)
	s_barrier
	s_cbranch_vccnz .LBB0_19
	v_readlane_b32 s2, v255, 47
	v_readlane_b32 s3, v255, 48
	s_mov_b32 s3, s1
	v_writelane_b32 v255, s2, 47
	s_mov_b32 s15, s1
	v_readlane_b32 s0, v253, 2
	v_writelane_b32 v255, s3, 48
	s_lshl_b64 s[2:3], s[14:15], 2
	s_add_u32 s2, s0, s2
	v_readlane_b32 s0, v253, 3
	s_addc_u32 s3, s0, s3
	v_writelane_b32 v255, s2, 51
	v_mov_b32_e32 v3, v212
	s_nop 0
	v_writelane_b32 v255, s3, 52
	v_readlane_b32 s2, v254, 4
	v_readlane_b32 s3, v254, 5
	s_andn2_b64 vcc, exec, s[2:3]
	v_readfirstlane_b32 s2, v3
	s_cbranch_vccnz .LBB0_367
	v_bfe_i32 v5, v3, 27, 1
	v_lshlrev_b32_e32 v4, 4, v3
	v_lshrrev_b32_e32 v5, 22, v5
	v_add_u32_e32 v5, v4, v5
	v_and_b32_e32 v5, 0xfffffc00, v5
	v_sub_u32_e32 v4, v4, v5
	v_lshrrev_b32_e32 v5, 4, v4
	v_ashrrev_i32_e32 v6, 31, v3
	v_bitop3_b32 v4, v5, v4, 32 bitop3:0x6c
	v_lshrrev_b32_e32 v6, 26, v6
	v_ashrrev_i32_e32 v5, 31, v4
	v_add_u32_e32 v6, v3, v6
	v_lshrrev_b32_e32 v5, 26, v5
	v_ashrrev_i32_e32 v9, 6, v6
	v_add_u32_e32 v5, v4, v5
	v_lshlrev_b32_e32 v6, 3, v9
	v_ashrrev_i32_e32 v8, 6, v5
	v_and_b32_e32 v6, -16, v6
	v_add_u32_e32 v6, v8, v6
	v_and_b32_e32 v7, 3, v8
	s_mov_b32 s4, 0xfffe0
	v_lshrrev_b32_e32 v10, 2, v6
	v_lshlrev_b32_e32 v11, 1, v6
	v_and_b32_e32 v5, 0xc0, v5
	v_and_or_b32 v7, v6, s4, v7
	v_and_b32_e32 v10, 4, v10
	v_and_b32_e32 v11, 24, v11
	v_sub_u32_e32 v4, v4, v5
	v_mov_b32_e32 v5, 1
	v_or3_b32 v7, v7, v10, v11
	v_lshlrev_b32_e32 v10, 5, v9
	v_ashrrev_i16_sdwa v4, v5, sext(v4) dst_sel:DWORD dst_unused:UNUSED_PAD src0_sel:DWORD src1_sel:BYTE_0
	v_and_b32_e32 v10, 32, v10
	v_bfe_i32 v11, v4, 0, 16
	s_ashr_i32 s3, s2, 6
	v_add_u32_e32 v4, v10, v11
	s_lshl_b32 s0, s3, 10
	v_lshlrev_b32_e32 v5, 1, v4
	s_movk_i32 s4, 0x840
	v_lshl_add_u32 v164, v7, 12, v5
	v_mul_lo_u32 v5, v6, s4
	v_readlane_b32 s4, v254, 29
	s_add_i32 s30, s0, 0
	v_mov_b32_e32 v165, v2
	v_readlane_b32 s5, v254, 30
	s_add_i32 m0, s30, 0x10000
	v_add_lshl_u32 v166, v4, v5, 1
	v_lshl_add_u64 v[4:5], s[4:5], 0, v[164:165]
	v_lshl_add_u64 v[6:7], v[4:5], 0, s[90:91]
	v_mov_b32_e32 v167, v2
	global_load_lds_dwordx4 v164, s[4:5]
	v_readlane_b32 s4, v254, 20
	s_add_i32 m0, s30, 0x12000
	v_readlane_b32 s5, v254, 21
	global_load_lds_dwordx4 v[6:7], off
	s_nop 0
	v_lshl_add_u64 v[6:7], s[4:5], 0, v[164:165]
	s_add_i32 m0, s30, 0x14000
	v_lshl_add_u64 v[6:7], v[6:7], 0, s[90:91]
	global_load_lds_dwordx4 v164, s[4:5]
	s_add_i32 m0, s30, 0x16000
	v_readlane_b32 s4, v254, 25
	global_load_lds_dwordx4 v[6:7], off
	v_readlane_b32 s5, v254, 26
	s_mov_b32 m0, s30
	s_add_i32 s31, s30, 0x2000
	v_lshl_add_u64 v[6:7], s[4:5], 0, v[166:167]
	v_lshl_add_u64 v[12:13], v[6:7], 0, s[96:97]
	s_add_i32 s34, s30, 0x4000
	global_load_lds_dwordx4 v166, s[4:5]
	v_readlane_b32 s4, v254, 27
	s_mov_b32 m0, s31
	v_readlane_b32 s5, v254, 28
	global_load_lds_dwordx4 v[12:13], off
	s_nop 0
	v_lshl_add_u64 v[12:13], s[4:5], 0, v[166:167]
	s_mov_b32 m0, s34
	s_add_i32 s35, s30, 0x6000
	global_load_lds_dwordx4 v166, s[4:5]
	v_lshl_add_u64 v[12:13], v[12:13], 0, s[96:97]
	s_mov_b32 m0, s35
	s_ashr_i32 s4, s2, 8
	s_cmp_eq_u32 s4, 0
	s_cbranch_scc0 .Lsp_in
	s_setprio 1
.Lsp_in:
	global_load_lds_dwordx4 v[12:13], off
	s_cmp_eq_u32 s4, 1
	s_cselect_b64 s[16:17], -1, 0
	s_cmp_lg_u32 s4, 1
	s_cbranch_scc1 .LBB0_312
	s_barrier

;     __device__ bool next(int i, Unit& u) const { const int rounds = nwg / G; if (i >= rounds) return false; return StaticOrder::next(rounds - 1 - i, u); }
;     __device__ bool next(int i, Unit& u) const { const int rounds = nwg / G; if (i >= 2 * rounds) return false; const bool ok = StaticOrder::next(i >= rounds ? i - rounds : i, u); u.z = (i >= rounds) ? 1 : 0; return ok; }
; #define PG8_TRIP_HEAD(T) const int t = (T); const bool last = (t == nt - 2); \
;             const char* a1 = cA + (size_t)(t + 1) * kstep; \
;             const char* a2 = last ? nA : cA + (size_t)(t + 2) * kstep; const char* b2 = last ? nB : cB + (size_t)(t + 2) * kstep; \
;             const char* a3 = a2 + kstep; const char* b3 = b2 + kstep; \
;             if (last && has_next) S.a_ready(nxt);
; template <class Epi, class Sched, bool ALIGN_EPI = false, bool SP2 = false>
; __device__ __forceinline__ void gemm_phase(PG8_LAS unsigned char* lds, const Gemm g, const Sched& S, const Epi& E) {
;     ...
;         const bool has_next = S.next(ui + 1, nxt);
;         const char* nA = has_next ? (const char*)S.opA(g, nxt) + (size_t)nxt.pm * tstepA : cA; const char* nB = has_next ? (const char*)S.opB(g, nxt) + (size_t)nxt.pn * tstepB : cB;
;     ...
;         if constexpr (SP2) {
;             { PG8_TRIP_HEAD(0) PG8_TRIP_SP2(asm volatile("s_waitcnt vmcnt(%0)" :: "n"(8 + Epi::NST) : "memory"), PG8_MMAZ) }
.LBB0_323:
	s_ashr_i32 s23, s22, 31
	s_lshl_b64 s[4:5], s[22:23], 20
	v_readlane_b32 s26, v254, 18
	v_readlane_b32 s27, v254, 19
	s_add_u32 s26, s26, s4
	s_addc_u32 s27, s27, s5
	s_add_i32 s28, 0, 0x10000
	s_add_i32 s33, 0, 0x14000
	v_add_u32_e32 v132, s28, v197
	s_waitcnt lgkmcnt(0)
	v_add_u32_e32 v133, s33, v197
	ds_read_b128 v[4:7], v132
	ds_read_b128 v[8:11], v132 offset:1024
	ds_read_b128 v[12:15], v132 offset:2048
	ds_read_b128 v[16:19], v132 offset:3072
	ds_read_b128 v[20:23], v133
	ds_read_b128 v[24:27], v133 offset:1024
	ds_read_b128 v[28:31], v133 offset:2048
	ds_read_b128 v[32:35], v133 offset:3072
	s_and_b64 s[4:5], s[10:11], exec
	s_cselect_b32 s3, s27, s13
	s_cselect_b32 s4, s26, s12
	v_lshl_add_u64 v[194:195], s[14:15], 0, v[166:167]
	s_mov_b64 s[10:11], 0x84080
	s_add_i32 s5, s30, 0xc000
	v_lshl_add_u64 v[68:69], v[194:195], 0, s[10:11]
	s_mov_b32 m0, s5
	s_mov_b64 s[10:11], 0xc6080
	s_add_i32 s23, s30, 0xe000
	ds_read_b128 v[36:39], v200
	ds_read_b128 v[40:43], v200 offset:1024
	ds_read_b128 v[44:47], v200 offset:2048
	ds_read_b128 v[48:51], v200 offset:3072
	ds_read_b128 v[52:55], v200 offset:4096
	ds_read_b128 v[56:59], v200 offset:5120
	ds_read_b128 v[60:63], v200 offset:6144
	ds_read_b128 v[64:67], v200 offset:7168
	global_load_lds_dwordx4 v[68:69], off
	v_lshl_add_u64 v[68:69], v[194:195], 0, s[10:11]
	s_mov_b32 m0, s23
	s_nop 0
	global_load_lds_dwordx4 v[68:69], off
	s_waitcnt vmcnt(16)
	s_waitcnt lgkmcnt(0)
	s_barrier
	s_waitcnt lgkmcnt(0)
	v_mfma_f32_16x16x32_bf16 v[88:91], v[12:15], v[52:55], 0
	v_mfma_f32_16x16x32_bf16 v[92:95], v[16:19], v[56:59], v[88:91]
	v_mfma_f32_16x16x32_bf16 v[88:91], v[4:7], v[60:63], 0
	v_mfma_f32_16x16x32_bf16 v[68:71], v[4:7], v[36:39], 0
	v_mfma_f32_16x16x32_bf16 v[72:75], v[12:15], v[36:39], 0
	v_mfma_f32_16x16x32_bf16 v[76:79], v[4:7], v[44:47], 0
	v_mfma_f32_16x16x32_bf16 v[80:83], v[12:15], v[44:47], 0
	v_mfma_f32_16x16x32_bf16 v[84:87], v[4:7], v[52:55], 0
	v_mfma_f32_16x16x32_bf16 v[96:99], v[8:11], v[64:67], v[88:91]
	v_mfma_f32_16x16x32_bf16 v[88:91], v[12:15], v[60:63], 0
	v_mfma_f32_16x16x32_bf16 v[68:71], v[8:11], v[40:43], v[68:71]
	v_mfma_f32_16x16x32_bf16 v[72:75], v[16:19], v[40:43], v[72:75]
	v_mfma_f32_16x16x32_bf16 v[76:79], v[8:11], v[48:51], v[76:79]
	v_mfma_f32_16x16x32_bf16 v[80:83], v[16:19], v[48:51], v[80:83]
	v_mfma_f32_16x16x32_bf16 v[84:87], v[8:11], v[56:59], v[84:87]
	v_mfma_f32_16x16x32_bf16 v[108:111], v[16:19], v[64:67], v[88:91]
	v_mfma_f32_16x16x32_bf16 v[88:91], v[20:23], v[36:39], 0
	v_mfma_f32_16x16x32_bf16 v[36:39], v[28:31], v[36:39], 0
	v_mfma_f32_16x16x32_bf16 v[112:115], v[24:27], v[40:43], v[88:91]
	v_mfma_f32_16x16x32_bf16 v[36:39], v[32:35], v[40:43], v[36:39]
	v_mfma_f32_16x16x32_bf16 v[40:43], v[20:23], v[44:47], 0
	v_mfma_f32_16x16x32_bf16 v[44:47], v[28:31], v[44:47], 0
	v_mfma_f32_16x16x32_bf16 v[40:43], v[24:27], v[48:51], v[40:43]
	v_mfma_f32_16x16x32_bf16 v[44:47], v[32:35], v[48:51], v[44:47]
	v_mfma_f32_16x16x32_bf16 v[48:51], v[20:23], v[52:55], 0
	v_mfma_f32_16x16x32_bf16 v[52:55], v[28:31], v[52:55], 0
	v_mfma_f32_16x16x32_bf16 v[48:51], v[24:27], v[56:59], v[48:51]
	v_mfma_f32_16x16x32_bf16 v[52:55], v[32:35], v[56:59], v[52:55]
	v_mfma_f32_16x16x32_bf16 v[56:59], v[20:23], v[60:63], 0
	v_mfma_f32_16x16x32_bf16 v[60:63], v[28:31], v[60:63], 0
	v_mfma_f32_16x16x32_bf16 v[56:59], v[24:27], v[64:67], v[56:59]
	v_mfma_f32_16x16x32_bf16 v[60:63], v[32:35], v[64:67], v[60:63]
	s_barrier
	v_lshl_add_u64 v[214:215], s[12:13], 0, v[164:165]
	s_mov_b64 s[10:11], 0x100
	s_add_i32 s28, s28, s0
	v_lshl_add_u64 v[134:135], v[214:215], 0, s[10:11]
	s_mov_b32 m0, s28
	s_mov_b64 s[46:47], 0x40100
	s_add_i32 s29, s28, 0x2000
	ds_read_b128 v[64:67], v200 offset:16384
	ds_read_b128 v[88:91], v200 offset:17408
	ds_read_b128 v[100:103], v200 offset:18432
	ds_read_b128 v[104:107], v200 offset:19456
	ds_read_b128 v[116:119], v200 offset:20480
	ds_read_b128 v[120:123], v200 offset:21504
	ds_read_b128 v[124:127], v200 offset:22528
	ds_read_b128 v[128:131], v200 offset:23552
	global_load_lds_dwordx4 v[134:135], off
	v_lshl_add_u64 v[134:135], v[214:215], 0, s[46:47]
	s_mov_b32 m0, s29
	s_mov_b64 s[46:47], 0x80100
	s_add_i32 s33, s33, s0
	global_load_lds_dwordx4 v[134:135], off
	v_lshl_add_u64 v[134:135], v[214:215], 0, s[46:47]
	s_mov_b32 m0, s33
	s_mov_b64 s[46:47], 0xc0100
	s_add_i32 s45, s33, 0x2000
	global_load_lds_dwordx4 v[134:135], off
	v_lshl_add_u64 v[134:135], v[214:215], 0, s[46:47]
	s_mov_b32 m0, s45
	s_nop 0
	global_load_lds_dwordx4 v[134:135], off
	v_lshl_add_u64 v[134:135], v[194:195], 0, s[10:11]
	s_mov_b32 m0, s30
	s_mov_b64 s[10:11], 0x42100
	global_load_lds_dwordx4 v[134:135], off
	v_lshl_add_u64 v[134:135], v[194:195], 0, s[10:11]
	s_mov_b32 m0, s31
	s_nop 0
	global_load_lds_dwordx4 v[134:135], off
	s_waitcnt vmcnt(16)
	s_waitcnt lgkmcnt(0)
	s_barrier
; #define PG8_TRIP_HEAD(T) const int t = (T); const bool last = (t == nt - 2); \
;             const char* a1 = cA + (size_t)(t + 1) * kstep; \
;             const char* a2 = last ? nA : cA + (size_t)(t + 2) * kstep; const char* b2 = last ? nB : cB + (size_t)(t + 2) * kstep; \
;             const char* a3 = a2 + kstep; const char* b3 = b2 + kstep; \
;             if (last && has_next) S.a_ready(nxt);
; template <class Epi, class Sched, bool ALIGN_EPI = false, bool SP2 = false>
; __device__ __forceinline__ void gemm_phase(PG8_LAS unsigned char* lds, const Gemm g, const Sched& S, const Epi& E) {
;     ...
;         if constexpr (SP2) {
;             { PG8_TRIP_HEAD(0) PG8_TRIP_SP2(asm volatile("s_waitcnt vmcnt(%0)" :: "n"(8 + Epi::NST) : "memory"), PG8_MMAZ) }
	s_waitcnt lgkmcnt(0)
	v_mfma_f32_16x16x32_bf16 v[134:137], v[4:7], v[64:67], 0
	v_mfma_f32_16x16x32_bf16 v[144:147], v[4:7], v[100:103], 0
	v_mfma_f32_16x16x32_bf16 v[152:155], v[4:7], v[116:119], 0
	v_mfma_f32_16x16x32_bf16 v[4:7], v[4:7], v[124:127], 0
	v_mfma_f32_16x16x32_bf16 v[136:139], v[8:11], v[88:91], v[134:137]
	v_mfma_f32_16x16x32_bf16 v[144:147], v[8:11], v[104:107], v[144:147]
	v_mfma_f32_16x16x32_bf16 v[152:155], v[8:11], v[120:123], v[152:155]
	v_mfma_f32_16x16x32_bf16 v[4:7], v[8:11], v[128:131], v[4:7]
	v_mfma_f32_16x16x32_bf16 v[8:11], v[12:15], v[124:127], 0
	v_mfma_f32_16x16x32_bf16 v[140:143], v[12:15], v[64:67], 0
	v_mfma_f32_16x16x32_bf16 v[148:151], v[12:15], v[100:103], 0
	v_mfma_f32_16x16x32_bf16 v[156:159], v[12:15], v[116:119], 0
	v_mfma_f32_16x16x32_bf16 v[12:15], v[16:19], v[128:131], v[8:11]
	v_mfma_f32_16x16x32_bf16 v[140:143], v[16:19], v[88:91], v[140:143]
	v_mfma_f32_16x16x32_bf16 v[148:151], v[16:19], v[104:107], v[148:151]
	v_mfma_f32_16x16x32_bf16 v[156:159], v[16:19], v[120:123], v[156:159]
	v_mfma_f32_16x16x32_bf16 v[8:11], v[20:23], v[64:67], 0
	v_mfma_f32_16x16x32_bf16 v[16:19], v[24:27], v[88:91], v[8:11]
	v_mfma_f32_16x16x32_bf16 v[8:11], v[28:31], v[64:67], 0
	v_mfma_f32_16x16x32_bf16 v[160:163], v[32:35], v[88:91], v[8:11]
	v_mfma_f32_16x16x32_bf16 v[8:11], v[20:23], v[100:103], 0
	v_mfma_f32_16x16x32_bf16 v[174:177], v[24:27], v[104:107], v[8:11]
	v_mfma_f32_16x16x32_bf16 v[8:11], v[28:31], v[100:103], 0
	v_mfma_f32_16x16x32_bf16 v[178:181], v[32:35], v[104:107], v[8:11]
	v_mfma_f32_16x16x32_bf16 v[8:11], v[20:23], v[116:119], 0
	v_mfma_f32_16x16x32_bf16 v[182:185], v[24:27], v[120:123], v[8:11]
	v_mfma_f32_16x16x32_bf16 v[8:11], v[28:31], v[116:119], 0
	v_mfma_f32_16x16x32_bf16 v[190:193], v[32:35], v[120:123], v[8:11]
	v_mfma_f32_16x16x32_bf16 v[8:11], v[20:23], v[124:127], 0
	v_mfma_f32_16x16x32_bf16 v[202:205], v[24:27], v[128:131], v[8:11]
	v_mfma_f32_16x16x32_bf16 v[8:11], v[28:31], v[124:127], 0
	v_mfma_f32_16x16x32_bf16 v[206:209], v[32:35], v[128:131], v[8:11]
	s_barrier
	s_add_i32 s46, 0, 0x18000
	s_add_i32 s48, 0, 0x1c000
	v_add_u32_e32 v134, s46, v197
	v_add_u32_e32 v135, s48, v197
	s_nop 0
	ds_read_b128 v[8:11], v134
	ds_read_b128 v[28:31], v134 offset:1024
	ds_read_b128 v[32:35], v134 offset:2048
	ds_read_b128 v[64:67], v134 offset:3072
	ds_read_b128 v[216:219], v135
	ds_read_b128 v[220:223], v135 offset:1024
	ds_read_b128 v[224:227], v135 offset:2048
	ds_read_b128 v[228:231], v135 offset:3072
	s_mov_b64 s[10:11], 0x84100
	s_mov_b32 m0, s34
	v_lshl_add_u64 v[88:89], v[194:195], 0, s[10:11]
	s_mov_b64 s[10:11], 0xc6100
	ds_read_b128 v[20:23], v200 offset:32768
	ds_read_b128 v[24:27], v200 offset:33792
	ds_read_b128 v[232:235], v200 offset:34816
	ds_read_b128 v[236:239], v200 offset:35840
	ds_read_b128 v[240:243], v200 offset:36864
	ds_read_b128 v[244:247], v200 offset:37888
	ds_read_b128 v[248:251], v200 offset:38912
	ds_read_b128 v[186:189], v200 offset:39936
	global_load_lds_dwordx4 v[88:89], off
	v_lshl_add_u64 v[88:89], v[194:195], 0, s[10:11]
	s_mov_b32 m0, s35
	s_nop 0
	global_load_lds_dwordx4 v[88:89], off
	s_waitcnt vmcnt(8)
	s_waitcnt lgkmcnt(0)
	s_barrier
	s_waitcnt lgkmcnt(0)
	v_mfma_f32_16x16x32_bf16 v[68:71], v[8:11], v[20:23], v[68:71]
	v_mfma_f32_16x16x32_bf16 v[120:123], v[28:31], v[24:27], v[68:71]
	v_mfma_f32_16x16x32_bf16 v[68:71], v[32:35], v[20:23], v[72:75]
	v_mfma_f32_16x16x32_bf16 v[116:119], v[64:67], v[24:27], v[68:71]
	v_mfma_f32_16x16x32_bf16 v[68:71], v[8:11], v[232:235], v[76:79]
	v_mfma_f32_16x16x32_bf16 v[104:107], v[28:31], v[236:239], v[68:71]
	v_mfma_f32_16x16x32_bf16 v[68:71], v[32:35], v[232:235], v[80:83]
	v_mfma_f32_16x16x32_bf16 v[100:103], v[64:67], v[236:239], v[68:71]
	v_mfma_f32_16x16x32_bf16 v[68:71], v[8:11], v[240:243], v[84:87]
	v_mfma_f32_16x16x32_bf16 v[88:91], v[28:31], v[244:247], v[68:71]
	v_mfma_f32_16x16x32_bf16 v[68:71], v[32:35], v[240:243], v[92:95]
	v_mfma_f32_16x16x32_bf16 v[84:87], v[64:67], v[244:247], v[68:71]
	v_mfma_f32_16x16x32_bf16 v[68:71], v[8:11], v[248:251], v[96:99]
	v_mfma_f32_16x16x32_bf16 v[72:75], v[28:31], v[186:189], v[68:71]
	v_mfma_f32_16x16x32_bf16 v[68:71], v[32:35], v[248:251], v[108:111]
	v_mfma_f32_16x16x32_bf16 v[68:71], v[64:67], v[186:189], v[68:71]
	v_mfma_f32_16x16x32_bf16 v[76:79], v[216:219], v[20:23], v[112:115]
	v_mfma_f32_16x16x32_bf16 v[20:23], v[224:227], v[20:23], v[36:39]
	v_mfma_f32_16x16x32_bf16 v[124:127], v[228:231], v[24:27], v[20:23]
	v_mfma_f32_16x16x32_bf16 v[20:23], v[216:219], v[232:235], v[40:43]
	v_mfma_f32_16x16x32_bf16 v[112:115], v[220:223], v[236:239], v[20:23]
	v_mfma_f32_16x16x32_bf16 v[20:23], v[224:227], v[232:235], v[44:47]
	v_mfma_f32_16x16x32_bf16 v[108:111], v[228:231], v[236:239], v[20:23]
	v_mfma_f32_16x16x32_bf16 v[20:23], v[216:219], v[240:243], v[48:51]
	v_mfma_f32_16x16x32_bf16 v[96:99], v[220:223], v[244:247], v[20:23]
	v_mfma_f32_16x16x32_bf16 v[20:23], v[224:227], v[240:243], v[52:55]
	v_mfma_f32_16x16x32_bf16 v[92:95], v[228:231], v[244:247], v[20:23]
	v_mfma_f32_16x16x32_bf16 v[20:23], v[216:219], v[248:251], v[56:59]
	v_mfma_f32_16x16x32_bf16 v[80:83], v[220:223], v[186:189], v[20:23]
	v_mfma_f32_16x16x32_bf16 v[20:23], v[224:227], v[248:251], v[60:63]
	v_mfma_f32_16x16x32_bf16 v[128:131], v[220:223], v[24:27], v[76:79]
	v_mfma_f32_16x16x32_bf16 v[76:79], v[228:231], v[186:189], v[20:23]
	s_barrier
; #define PG8_MMA(ai, bj, At, Bt) do { __builtin_amdgcn_s_setprio(1); _Pragma("unroll") for (int m = 0; m < 4; ++m) _Pragma("unroll") for (int n = 0; n < 2; ++n) _Pragma("unroll") for (int k = 0; k < 2; ++k) \
;         acc[ai][bj][m][n] = __builtin_amdgcn_mfma_f32_16x16x32_bf16(Bt[n][k], At[m][k], acc[ai][bj][m][n], 0, 0, 0); __builtin_amdgcn_s_setprio(0); } while (0)
; #define PG8_WAIT_V(n) asm volatile("s_waitcnt vmcnt(" #n ")" ::: "memory")
; #define PG8_TRIP_HEAD(T) const int t = (T); const bool last = (t == nt - 2); \
;             const char* a1 = cA + (size_t)(t + 1) * kstep; \
;             const char* a2 = last ? nA : cA + (size_t)(t + 2) * kstep; const char* b2 = last ? nB : cB + (size_t)(t + 2) * kstep; \
;             const char* a3 = a2 + kstep; const char* b3 = b2 + kstep; \
;             if (last && has_next) S.a_ready(nxt);
; template <class Epi, class Sched, bool ALIGN_EPI = false, bool SP2 = false>
; __device__ __forceinline__ void gemm_phase(PG8_LAS unsigned char* lds, const Gemm g, const Sched& S, const Epi& E) {
;     ...
;         if constexpr (SP2) {
;             { PG8_TRIP_HEAD(0) PG8_TRIP_SP2(asm volatile("s_waitcnt vmcnt(%0)" :: "n"(8 + Epi::NST) : "memory"), PG8_MMAZ) }
;             for (int tt = 2; tt < nt; tt += 2) { PG8_TRIP_HEAD(tt) PG8_TRIP_SP2(PG8_WAIT_V(8), PG8_MMA) }
	s_mov_b64 s[10:11], 0x180
	s_add_i32 s46, s46, s0
	s_nop 1
	v_lshl_add_u64 v[20:21], v[214:215], 0, s[10:11]
	s_mov_b32 m0, s46
	s_mov_b64 s[50:51], 0x40180
	s_add_i32 s47, s46, 0x2000
	ds_read_b128 v[44:47], v200 offset:49152
	ds_read_b128 v[48:51], v200 offset:50176
	ds_read_b128 v[186:189], v200 offset:51200
	ds_read_b128 v[232:235], v200 offset:52224
	ds_read_b128 v[236:239], v200 offset:53248
	ds_read_b128 v[240:243], v200 offset:54272
	ds_read_b128 v[244:247], v200 offset:55296
	ds_read_b128 v[248:251], v200 offset:56320
	global_load_lds_dwordx4 v[20:21], off
	v_lshl_add_u64 v[20:21], v[214:215], 0, s[50:51]
	s_mov_b32 m0, s47
	s_mov_b64 s[50:51], 0x80180
	s_add_i32 s48, s48, s0
	global_load_lds_dwordx4 v[20:21], off
	v_lshl_add_u64 v[20:21], v[214:215], 0, s[50:51]
	s_mov_b32 m0, s48
	s_mov_b64 s[50:51], 0xc0180
	s_add_i32 s49, s48, 0x2000
	global_load_lds_dwordx4 v[20:21], off
	v_lshl_add_u64 v[20:21], v[214:215], 0, s[50:51]
	s_mov_b32 m0, s49
	s_nop 0
	global_load_lds_dwordx4 v[20:21], off
	v_lshl_add_u64 v[20:21], v[194:195], 0, s[10:11]
	s_mov_b32 m0, s38
	s_mov_b64 s[10:11], 0x42180
	global_load_lds_dwordx4 v[20:21], off
	v_lshl_add_u64 v[20:21], v[194:195], 0, s[10:11]
	s_mov_b32 m0, s39
	s_nop 0
	global_load_lds_dwordx4 v[20:21], off
	s_waitcnt vmcnt(8)
	s_waitcnt lgkmcnt(0)
	s_barrier
	s_waitcnt lgkmcnt(0)
	v_mfma_f32_16x16x32_bf16 v[20:23], v[8:11], v[44:47], v[136:139]
	v_mfma_f32_16x16x32_bf16 v[56:59], v[28:31], v[48:51], v[20:23]
	v_mfma_f32_16x16x32_bf16 v[20:23], v[32:35], v[44:47], v[140:143]
	v_mfma_f32_16x16x32_bf16 v[52:55], v[64:67], v[48:51], v[20:23]
	v_mfma_f32_16x16x32_bf16 v[20:23], v[8:11], v[186:189], v[144:147]
	v_mfma_f32_16x16x32_bf16 v[40:43], v[28:31], v[232:235], v[20:23]
	v_mfma_f32_16x16x32_bf16 v[20:23], v[32:35], v[186:189], v[148:151]
	v_mfma_f32_16x16x32_bf16 v[36:39], v[64:67], v[232:235], v[20:23]
	v_mfma_f32_16x16x32_bf16 v[20:23], v[8:11], v[236:239], v[152:155]
	v_mfma_f32_16x16x32_bf16 v[4:7], v[8:11], v[244:247], v[4:7]
	v_mfma_f32_16x16x32_bf16 v[24:27], v[28:31], v[240:243], v[20:23]
	v_mfma_f32_16x16x32_bf16 v[20:23], v[32:35], v[236:239], v[156:159]
	v_mfma_f32_16x16x32_bf16 v[8:11], v[28:31], v[248:251], v[4:7]
	v_mfma_f32_16x16x32_bf16 v[4:7], v[32:35], v[244:247], v[12:15]
	v_mfma_f32_16x16x32_bf16 v[20:23], v[64:67], v[240:243], v[20:23]
	v_mfma_f32_16x16x32_bf16 v[4:7], v[64:67], v[248:251], v[4:7]
	v_mfma_f32_16x16x32_bf16 v[12:15], v[216:219], v[44:47], v[16:19]
	v_mfma_f32_16x16x32_bf16 v[64:67], v[220:223], v[48:51], v[12:15]
	v_mfma_f32_16x16x32_bf16 v[12:15], v[224:227], v[44:47], v[160:163]
	v_mfma_f32_16x16x32_bf16 v[60:63], v[228:231], v[48:51], v[12:15]
	v_mfma_f32_16x16x32_bf16 v[12:15], v[216:219], v[186:189], v[174:177]
	v_mfma_f32_16x16x32_bf16 v[48:51], v[220:223], v[232:235], v[12:15]
	v_mfma_f32_16x16x32_bf16 v[12:15], v[224:227], v[186:189], v[178:181]
	v_mfma_f32_16x16x32_bf16 v[44:47], v[228:231], v[232:235], v[12:15]
	v_mfma_f32_16x16x32_bf16 v[12:15], v[216:219], v[236:239], v[182:185]
	v_mfma_f32_16x16x32_bf16 v[32:35], v[220:223], v[240:243], v[12:15]
	v_mfma_f32_16x16x32_bf16 v[12:15], v[224:227], v[236:239], v[190:193]
	v_mfma_f32_16x16x32_bf16 v[28:31], v[228:231], v[240:243], v[12:15]
	v_mfma_f32_16x16x32_bf16 v[12:15], v[216:219], v[244:247], v[202:205]
	v_mfma_f32_16x16x32_bf16 v[16:19], v[220:223], v[248:251], v[12:15]
	v_mfma_f32_16x16x32_bf16 v[12:15], v[224:227], v[244:247], v[206:209]
	v_mfma_f32_16x16x32_bf16 v[12:15], v[228:231], v[248:251], v[12:15]
	s_barrier
	s_add_u32 s10, s14, 0x84180
	s_addc_u32 s11, s15, 0
	s_add_u32 s12, s12, 0x200
	s_addc_u32 s13, s13, 0
	s_mov_b32 s14, 0
	s_mov_b64 s[54:55], 0x80000
	s_mov_b64 s[56:57], 0x80080
	s_mov_b64 s[60:61], 0xc0000
	s_mov_b64 s[62:63], 0xc0080
	s_mov_b64 s[64:65], 0xc6000
.LBB0_324:
	ds_read_b128 v[136:139], v132
	ds_read_b128 v[140:143], v132 offset:1024
	ds_read_b128 v[144:147], v132 offset:2048
	ds_read_b128 v[148:151], v132 offset:3072
	ds_read_b128 v[152:155], v133
	ds_read_b128 v[156:159], v133 offset:1024
	ds_read_b128 v[160:163], v133 offset:2048
	ds_read_b128 v[174:177], v133 offset:3072
	s_add_u32 s15, s10, 0xfff7c080
	s_addc_u32 s50, s11, -1
	s_cmp_eq_u32 s14, 28
	s_cselect_b32 s51, s25, s50
	s_cselect_b32 s50, s24, s15
	s_cselect_b32 s53, s3, s13
	s_cselect_b32 s52, s4, s12
	s_mov_b32 m0, s5
	v_lshl_add_u64 v[194:195], s[10:11], 0, v[172:173]
	ds_read_b128 v[178:181], v200
	ds_read_b128 v[182:185], v200 offset:1024
	ds_read_b128 v[186:189], v200 offset:2048
	ds_read_b128 v[190:193], v200 offset:3072
	ds_read_b128 v[202:205], v200 offset:4096
	ds_read_b128 v[206:209], v200 offset:5120
	ds_read_b128 v[216:219], v200 offset:6144
	ds_read_b128 v[220:223], v200 offset:7168
	global_load_lds_dwordx4 v[194:195], off
	v_lshl_add_u64 v[194:195], v[194:195], 0, s[96:97]
	s_mov_b32 m0, s23
	s_nop 0
	global_load_lds_dwordx4 v[194:195], off
	s_waitcnt vmcnt(8)
	s_waitcnt lgkmcnt(0)
	s_barrier
; #define PG8_MMA(ai, bj, At, Bt) do { __builtin_amdgcn_s_setprio(1); _Pragma("unroll") for (int m = 0; m < 4; ++m) _Pragma("unroll") for (int n = 0; n < 2; ++n) _Pragma("unroll") for (int k = 0; k < 2; ++k) \
;         acc[ai][bj][m][n] = __builtin_amdgcn_mfma_f32_16x16x32_bf16(Bt[n][k], At[m][k], acc[ai][bj][m][n], 0, 0, 0); __builtin_amdgcn_s_setprio(0); } while (0)
; #define PG8_WAIT_V(n) asm volatile("s_waitcnt vmcnt(" #n ")" ::: "memory")
; #define PG8_TRIP_HEAD(T) const int t = (T); const bool last = (t == nt - 2); \
;             const char* a1 = cA + (size_t)(t + 1) * kstep; \
;             const char* a2 = last ? nA : cA + (size_t)(t + 2) * kstep; const char* b2 = last ? nB : cB + (size_t)(t + 2) * kstep; \
;             const char* a3 = a2 + kstep; const char* b3 = b2 + kstep; \
;             if (last && has_next) S.a_ready(nxt);
; template <class Epi, class Sched, bool ALIGN_EPI = false, bool SP2 = false>
; __device__ __forceinline__ void gemm_phase(PG8_LAS unsigned char* lds, const Gemm g, const Sched& S, const Epi& E) {
;     ...
;         if constexpr (SP2) {
;             { PG8_TRIP_HEAD(0) PG8_TRIP_SP2(asm volatile("s_waitcnt vmcnt(%0)" :: "n"(8 + Epi::NST) : "memory"), PG8_MMAZ) }
;             for (int tt = 2; tt < nt; tt += 2) { PG8_TRIP_HEAD(tt) PG8_TRIP_SP2(PG8_WAIT_V(8), PG8_MMA) }
	s_waitcnt lgkmcnt(0)
	v_mfma_f32_16x16x32_bf16 v[120:123], v[136:139], v[178:181], v[120:123]
	v_mfma_f32_16x16x32_bf16 v[116:119], v[144:147], v[178:181], v[116:119]
	v_mfma_f32_16x16x32_bf16 v[104:107], v[136:139], v[186:189], v[104:107]
	v_mfma_f32_16x16x32_bf16 v[100:103], v[144:147], v[186:189], v[100:103]
	v_mfma_f32_16x16x32_bf16 v[88:91], v[136:139], v[202:205], v[88:91]
	v_mfma_f32_16x16x32_bf16 v[84:87], v[144:147], v[202:205], v[84:87]
	v_mfma_f32_16x16x32_bf16 v[72:75], v[136:139], v[216:219], v[72:75]
	v_mfma_f32_16x16x32_bf16 v[68:71], v[144:147], v[216:219], v[68:71]
	v_mfma_f32_16x16x32_bf16 v[120:123], v[140:143], v[182:185], v[120:123]
	v_mfma_f32_16x16x32_bf16 v[116:119], v[148:151], v[182:185], v[116:119]
	v_mfma_f32_16x16x32_bf16 v[104:107], v[140:143], v[190:193], v[104:107]
	v_mfma_f32_16x16x32_bf16 v[100:103], v[148:151], v[190:193], v[100:103]
	v_mfma_f32_16x16x32_bf16 v[88:91], v[140:143], v[206:209], v[88:91]
	v_mfma_f32_16x16x32_bf16 v[84:87], v[148:151], v[206:209], v[84:87]
	v_mfma_f32_16x16x32_bf16 v[72:75], v[140:143], v[220:223], v[72:75]
	v_mfma_f32_16x16x32_bf16 v[68:71], v[148:151], v[220:223], v[68:71]
	v_mfma_f32_16x16x32_bf16 v[128:131], v[152:155], v[178:181], v[128:131]
	v_mfma_f32_16x16x32_bf16 v[124:127], v[160:163], v[178:181], v[124:127]
	v_mfma_f32_16x16x32_bf16 v[112:115], v[152:155], v[186:189], v[112:115]
	v_mfma_f32_16x16x32_bf16 v[108:111], v[160:163], v[186:189], v[108:111]
	v_mfma_f32_16x16x32_bf16 v[96:99], v[152:155], v[202:205], v[96:99]
	v_mfma_f32_16x16x32_bf16 v[92:95], v[160:163], v[202:205], v[92:95]
	v_mfma_f32_16x16x32_bf16 v[80:83], v[152:155], v[216:219], v[80:83]
	v_mfma_f32_16x16x32_bf16 v[76:79], v[160:163], v[216:219], v[76:79]
	v_mfma_f32_16x16x32_bf16 v[128:131], v[156:159], v[182:185], v[128:131]
	v_mfma_f32_16x16x32_bf16 v[124:127], v[174:177], v[182:185], v[124:127]
	v_mfma_f32_16x16x32_bf16 v[112:115], v[156:159], v[190:193], v[112:115]
	v_mfma_f32_16x16x32_bf16 v[108:111], v[174:177], v[190:193], v[108:111]
	v_mfma_f32_16x16x32_bf16 v[96:99], v[156:159], v[206:209], v[96:99]
	v_mfma_f32_16x16x32_bf16 v[92:95], v[174:177], v[206:209], v[92:95]
	v_mfma_f32_16x16x32_bf16 v[80:83], v[156:159], v[220:223], v[80:83]
	v_mfma_f32_16x16x32_bf16 v[76:79], v[174:177], v[220:223], v[76:79]
	s_barrier
	s_mov_b32 m0, s28
	v_lshl_add_u64 v[194:195], s[52:53], 0, v[164:165]
	ds_read_b128 v[178:181], v200 offset:16384
	ds_read_b128 v[182:185], v200 offset:17408
	ds_read_b128 v[186:189], v200 offset:18432
	ds_read_b128 v[190:193], v200 offset:19456
	ds_read_b128 v[202:205], v200 offset:20480
	ds_read_b128 v[206:209], v200 offset:21504
	ds_read_b128 v[216:219], v200 offset:22528
	ds_read_b128 v[220:223], v200 offset:23552
	global_load_lds_dwordx4 v[194:195], off
	v_lshl_add_u64 v[214:215], v[194:195], 0, s[90:91]
	s_mov_b32 m0, s29
	s_nop 0
	global_load_lds_dwordx4 v[214:215], off
	v_lshl_add_u64 v[214:215], v[194:195], 0, s[54:55]
	s_mov_b32 m0, s33
	s_nop 0
	global_load_lds_dwordx4 v[214:215], off
	v_lshl_add_u64 v[214:215], v[194:195], 0, s[60:61]
	s_mov_b32 m0, s45
	s_nop 0
	global_load_lds_dwordx4 v[214:215], off
	v_lshl_add_u64 v[214:215], s[50:51], 0, v[166:167]
	s_mov_b32 m0, s30
	v_lshl_add_u64 v[224:225], v[214:215], 0, s[96:97]
	global_load_lds_dwordx4 v[214:215], off
	s_mov_b32 m0, s31
	s_nop 0
	global_load_lds_dwordx4 v[224:225], off
	s_waitcnt vmcnt(8)
	s_waitcnt lgkmcnt(0)
	s_barrier
	s_waitcnt lgkmcnt(0)
	v_mfma_f32_16x16x32_bf16 v[56:59], v[136:139], v[178:181], v[56:59]
	v_mfma_f32_16x16x32_bf16 v[52:55], v[144:147], v[178:181], v[52:55]
	v_mfma_f32_16x16x32_bf16 v[40:43], v[136:139], v[186:189], v[40:43]
	v_mfma_f32_16x16x32_bf16 v[36:39], v[144:147], v[186:189], v[36:39]
	v_mfma_f32_16x16x32_bf16 v[24:27], v[136:139], v[202:205], v[24:27]
	v_mfma_f32_16x16x32_bf16 v[20:23], v[144:147], v[202:205], v[20:23]
	v_mfma_f32_16x16x32_bf16 v[8:11], v[136:139], v[216:219], v[8:11]
	v_mfma_f32_16x16x32_bf16 v[4:7], v[144:147], v[216:219], v[4:7]
	v_mfma_f32_16x16x32_bf16 v[56:59], v[140:143], v[182:185], v[56:59]
	v_mfma_f32_16x16x32_bf16 v[52:55], v[148:151], v[182:185], v[52:55]
	v_mfma_f32_16x16x32_bf16 v[40:43], v[140:143], v[190:193], v[40:43]
	v_mfma_f32_16x16x32_bf16 v[36:39], v[148:151], v[190:193], v[36:39]
	v_mfma_f32_16x16x32_bf16 v[24:27], v[140:143], v[206:209], v[24:27]
	v_mfma_f32_16x16x32_bf16 v[20:23], v[148:151], v[206:209], v[20:23]
	v_mfma_f32_16x16x32_bf16 v[8:11], v[140:143], v[220:223], v[8:11]
	v_mfma_f32_16x16x32_bf16 v[4:7], v[148:151], v[220:223], v[4:7]
	v_mfma_f32_16x16x32_bf16 v[64:67], v[152:155], v[178:181], v[64:67]
	v_mfma_f32_16x16x32_bf16 v[60:63], v[160:163], v[178:181], v[60:63]
	v_mfma_f32_16x16x32_bf16 v[48:51], v[152:155], v[186:189], v[48:51]
	v_mfma_f32_16x16x32_bf16 v[44:47], v[160:163], v[186:189], v[44:47]
	v_mfma_f32_16x16x32_bf16 v[32:35], v[152:155], v[202:205], v[32:35]
	v_mfma_f32_16x16x32_bf16 v[28:31], v[160:163], v[202:205], v[28:31]
	v_mfma_f32_16x16x32_bf16 v[16:19], v[152:155], v[216:219], v[16:19]
	v_mfma_f32_16x16x32_bf16 v[12:15], v[160:163], v[216:219], v[12:15]
	v_mfma_f32_16x16x32_bf16 v[64:67], v[156:159], v[182:185], v[64:67]
	v_mfma_f32_16x16x32_bf16 v[60:63], v[174:177], v[182:185], v[60:63]
	v_mfma_f32_16x16x32_bf16 v[48:51], v[156:159], v[190:193], v[48:51]
	v_mfma_f32_16x16x32_bf16 v[44:47], v[174:177], v[190:193], v[44:47]
	v_mfma_f32_16x16x32_bf16 v[32:35], v[156:159], v[206:209], v[32:35]
	v_mfma_f32_16x16x32_bf16 v[28:31], v[174:177], v[206:209], v[28:31]
	v_mfma_f32_16x16x32_bf16 v[16:19], v[156:159], v[220:223], v[16:19]
	v_mfma_f32_16x16x32_bf16 v[12:15], v[174:177], v[220:223], v[12:15]
	s_barrier
; #define PG8_MMA(ai, bj, At, Bt) do { __builtin_amdgcn_s_setprio(1); _Pragma("unroll") for (int m = 0; m < 4; ++m) _Pragma("unroll") for (int n = 0; n < 2; ++n) _Pragma("unroll") for (int k = 0; k < 2; ++k) \
;         acc[ai][bj][m][n] = __builtin_amdgcn_mfma_f32_16x16x32_bf16(Bt[n][k], At[m][k], acc[ai][bj][m][n], 0, 0, 0); __builtin_amdgcn_s_setprio(0); } while (0)
; #define PG8_WAIT_V(n) asm volatile("s_waitcnt vmcnt(" #n ")" ::: "memory")
; #define PG8_BAR __builtin_amdgcn_s_barrier()
; #define PG8_TRIP_HEAD(T) const int t = (T); const bool last = (t == nt - 2); \
;             const char* a1 = cA + (size_t)(t + 1) * kstep; \
;             const char* a2 = last ? nA : cA + (size_t)(t + 2) * kstep; const char* b2 = last ? nB : cB + (size_t)(t + 2) * kstep; \
;             const char* a3 = a2 + kstep; const char* b3 = b2 + kstep; \
;             if (last && has_next) S.a_ready(nxt);
; template <class Epi, class Sched, bool ALIGN_EPI = false, bool SP2 = false>
; __device__ __forceinline__ void gemm_phase(PG8_LAS unsigned char* lds, const Gemm g, const Sched& S, const Epi& E) {
;     ...
;         if constexpr (SP2) {
;             { PG8_TRIP_HEAD(0) PG8_TRIP_SP2(asm volatile("s_waitcnt vmcnt(%0)" :: "n"(8 + Epi::NST) : "memory"), PG8_MMAZ) }
;             for (int tt = 2; tt < nt; tt += 2) { PG8_TRIP_HEAD(tt) PG8_TRIP_SP2(PG8_WAIT_V(8), PG8_MMA) }
;     ...
;         if constexpr (ALIGN_EPI) { if (wr == 0) PG8_BAR; }
	ds_read_b128 v[136:139], v134
	ds_read_b128 v[140:143], v134 offset:1024
	ds_read_b128 v[144:147], v134 offset:2048
	ds_read_b128 v[148:151], v134 offset:3072
	ds_read_b128 v[152:155], v135
	ds_read_b128 v[156:159], v135 offset:1024
	ds_read_b128 v[160:163], v135 offset:2048
	ds_read_b128 v[174:177], v135 offset:3072
	s_mov_b32 m0, s34
	v_lshl_add_u64 v[224:225], v[214:215], 0, s[82:83]
	ds_read_b128 v[178:181], v200 offset:32768
	ds_read_b128 v[182:185], v200 offset:33792
	ds_read_b128 v[186:189], v200 offset:34816
	ds_read_b128 v[190:193], v200 offset:35840
	ds_read_b128 v[202:205], v200 offset:36864
	ds_read_b128 v[206:209], v200 offset:37888
	ds_read_b128 v[216:219], v200 offset:38912
	ds_read_b128 v[220:223], v200 offset:39936
	global_load_lds_dwordx4 v[224:225], off
	v_lshl_add_u64 v[224:225], v[214:215], 0, s[64:65]
	s_mov_b32 m0, s35
	s_nop 0
	global_load_lds_dwordx4 v[224:225], off
	s_waitcnt vmcnt(8)
	s_waitcnt lgkmcnt(0)
	s_barrier
	s_waitcnt lgkmcnt(0)
	v_mfma_f32_16x16x32_bf16 v[120:123], v[136:139], v[178:181], v[120:123]
	v_mfma_f32_16x16x32_bf16 v[116:119], v[144:147], v[178:181], v[116:119]
	v_mfma_f32_16x16x32_bf16 v[104:107], v[136:139], v[186:189], v[104:107]
	v_mfma_f32_16x16x32_bf16 v[100:103], v[144:147], v[186:189], v[100:103]
	v_mfma_f32_16x16x32_bf16 v[88:91], v[136:139], v[202:205], v[88:91]
	v_mfma_f32_16x16x32_bf16 v[84:87], v[144:147], v[202:205], v[84:87]
	v_mfma_f32_16x16x32_bf16 v[72:75], v[136:139], v[216:219], v[72:75]
	v_mfma_f32_16x16x32_bf16 v[68:71], v[144:147], v[216:219], v[68:71]
	v_mfma_f32_16x16x32_bf16 v[120:123], v[140:143], v[182:185], v[120:123]
	v_mfma_f32_16x16x32_bf16 v[116:119], v[148:151], v[182:185], v[116:119]
	v_mfma_f32_16x16x32_bf16 v[104:107], v[140:143], v[190:193], v[104:107]
	v_mfma_f32_16x16x32_bf16 v[100:103], v[148:151], v[190:193], v[100:103]
	v_mfma_f32_16x16x32_bf16 v[88:91], v[140:143], v[206:209], v[88:91]
	v_mfma_f32_16x16x32_bf16 v[84:87], v[148:151], v[206:209], v[84:87]
	v_mfma_f32_16x16x32_bf16 v[72:75], v[140:143], v[220:223], v[72:75]
	v_mfma_f32_16x16x32_bf16 v[68:71], v[148:151], v[220:223], v[68:71]
	v_mfma_f32_16x16x32_bf16 v[128:131], v[152:155], v[178:181], v[128:131]
	v_mfma_f32_16x16x32_bf16 v[124:127], v[160:163], v[178:181], v[124:127]
	v_mfma_f32_16x16x32_bf16 v[112:115], v[152:155], v[186:189], v[112:115]
	v_mfma_f32_16x16x32_bf16 v[108:111], v[160:163], v[186:189], v[108:111]
	v_mfma_f32_16x16x32_bf16 v[96:99], v[152:155], v[202:205], v[96:99]
	v_mfma_f32_16x16x32_bf16 v[92:95], v[160:163], v[202:205], v[92:95]
	v_mfma_f32_16x16x32_bf16 v[80:83], v[152:155], v[216:219], v[80:83]
	v_mfma_f32_16x16x32_bf16 v[76:79], v[160:163], v[216:219], v[76:79]
	v_mfma_f32_16x16x32_bf16 v[128:131], v[156:159], v[182:185], v[128:131]
	v_mfma_f32_16x16x32_bf16 v[124:127], v[174:177], v[182:185], v[124:127]
	v_mfma_f32_16x16x32_bf16 v[112:115], v[156:159], v[190:193], v[112:115]
	v_mfma_f32_16x16x32_bf16 v[108:111], v[174:177], v[190:193], v[108:111]
	v_mfma_f32_16x16x32_bf16 v[96:99], v[156:159], v[206:209], v[96:99]
	v_mfma_f32_16x16x32_bf16 v[92:95], v[174:177], v[206:209], v[92:95]
	v_mfma_f32_16x16x32_bf16 v[80:83], v[156:159], v[220:223], v[80:83]
	v_mfma_f32_16x16x32_bf16 v[76:79], v[174:177], v[220:223], v[76:79]
	s_barrier
	s_mov_b32 m0, s46
	v_lshl_add_u64 v[224:225], v[194:195], 0, s[78:79]
	ds_read_b128 v[178:181], v200 offset:49152
	ds_read_b128 v[182:185], v200 offset:50176
	ds_read_b128 v[186:189], v200 offset:51200
	ds_read_b128 v[190:193], v200 offset:52224
	ds_read_b128 v[202:205], v200 offset:53248
	ds_read_b128 v[206:209], v200 offset:54272
	ds_read_b128 v[216:219], v200 offset:55296
	ds_read_b128 v[220:223], v200 offset:56320
	global_load_lds_dwordx4 v[224:225], off
	v_lshl_add_u64 v[224:225], v[194:195], 0, s[84:85]
	s_mov_b32 m0, s47
	s_nop 0
	global_load_lds_dwordx4 v[224:225], off
	v_lshl_add_u64 v[224:225], v[194:195], 0, s[56:57]
	s_mov_b32 m0, s48
	v_lshl_add_u64 v[194:195], v[194:195], 0, s[62:63]
	global_load_lds_dwordx4 v[224:225], off
	s_mov_b32 m0, s49
	s_nop 0
	global_load_lds_dwordx4 v[194:195], off
	v_lshl_add_u64 v[194:195], v[214:215], 0, s[78:79]
	s_mov_b32 m0, s38
	s_nop 0
	global_load_lds_dwordx4 v[194:195], off
	v_lshl_add_u64 v[194:195], v[214:215], 0, s[92:93]
	s_mov_b32 m0, s39
	s_nop 0
	global_load_lds_dwordx4 v[194:195], off
	s_waitcnt vmcnt(8)
	s_waitcnt lgkmcnt(0)
	s_barrier
	s_waitcnt lgkmcnt(0)
	v_mfma_f32_16x16x32_bf16 v[56:59], v[136:139], v[178:181], v[56:59]
	v_mfma_f32_16x16x32_bf16 v[52:55], v[144:147], v[178:181], v[52:55]
	v_mfma_f32_16x16x32_bf16 v[40:43], v[136:139], v[186:189], v[40:43]
	v_mfma_f32_16x16x32_bf16 v[36:39], v[144:147], v[186:189], v[36:39]
	v_mfma_f32_16x16x32_bf16 v[24:27], v[136:139], v[202:205], v[24:27]
	v_mfma_f32_16x16x32_bf16 v[20:23], v[144:147], v[202:205], v[20:23]
	v_mfma_f32_16x16x32_bf16 v[8:11], v[136:139], v[216:219], v[8:11]
	v_mfma_f32_16x16x32_bf16 v[4:7], v[144:147], v[216:219], v[4:7]
	v_mfma_f32_16x16x32_bf16 v[56:59], v[140:143], v[182:185], v[56:59]
	v_mfma_f32_16x16x32_bf16 v[52:55], v[148:151], v[182:185], v[52:55]
	v_mfma_f32_16x16x32_bf16 v[40:43], v[140:143], v[190:193], v[40:43]
	v_mfma_f32_16x16x32_bf16 v[36:39], v[148:151], v[190:193], v[36:39]
	v_mfma_f32_16x16x32_bf16 v[24:27], v[140:143], v[206:209], v[24:27]
	v_mfma_f32_16x16x32_bf16 v[20:23], v[148:151], v[206:209], v[20:23]
	v_mfma_f32_16x16x32_bf16 v[8:11], v[140:143], v[220:223], v[8:11]
	v_mfma_f32_16x16x32_bf16 v[4:7], v[148:151], v[220:223], v[4:7]
	v_mfma_f32_16x16x32_bf16 v[64:67], v[152:155], v[178:181], v[64:67]
	v_mfma_f32_16x16x32_bf16 v[60:63], v[160:163], v[178:181], v[60:63]
	v_mfma_f32_16x16x32_bf16 v[48:51], v[152:155], v[186:189], v[48:51]
	v_mfma_f32_16x16x32_bf16 v[44:47], v[160:163], v[186:189], v[44:47]
	v_mfma_f32_16x16x32_bf16 v[32:35], v[152:155], v[202:205], v[32:35]
	v_mfma_f32_16x16x32_bf16 v[28:31], v[160:163], v[202:205], v[28:31]
	v_mfma_f32_16x16x32_bf16 v[16:19], v[152:155], v[216:219], v[16:19]
	v_mfma_f32_16x16x32_bf16 v[12:15], v[160:163], v[216:219], v[12:15]
	v_mfma_f32_16x16x32_bf16 v[64:67], v[156:159], v[182:185], v[64:67]
	v_mfma_f32_16x16x32_bf16 v[60:63], v[174:177], v[182:185], v[60:63]
	v_mfma_f32_16x16x32_bf16 v[48:51], v[156:159], v[190:193], v[48:51]
	v_mfma_f32_16x16x32_bf16 v[44:47], v[174:177], v[190:193], v[44:47]
	v_mfma_f32_16x16x32_bf16 v[32:35], v[156:159], v[206:209], v[32:35]
	v_mfma_f32_16x16x32_bf16 v[28:31], v[174:177], v[206:209], v[28:31]
	v_mfma_f32_16x16x32_bf16 v[16:19], v[156:159], v[220:223], v[16:19]
	v_mfma_f32_16x16x32_bf16 v[12:15], v[174:177], v[220:223], v[12:15]
	s_barrier
	s_add_i32 s14, s14, 2
	s_add_u32 s10, s10, 0x100
	s_addc_u32 s11, s11, 0
	s_add_u32 s12, s12, 0x100
	s_addc_u32 s13, s13, 0
	s_cmp_gt_u32 s14, 29
	s_cbranch_scc0 .LBB0_324
	s_and_b64 vcc, exec, s[18:19]
	s_cbranch_vccz .LBB0_327
	s_barrier

;     __device__ bool next(int i, Unit& u) const { const int rounds = nwg / G; if (i >= rounds) return false; return StaticOrder::next(rounds - 1 - i, u); }
; #define PG8_WAIT_V(n) asm volatile("s_waitcnt vmcnt(" #n ")" ::: "memory")
; template <class Epi, class Sched, bool ALIGN_EPI = false, bool SP2 = false>
; __device__ __forceinline__ void gemm_phase(PG8_LAS unsigned char* lds, const Gemm g, const Sched& S, const Epi& E) {
;     ...
;     { int R, C; stage_rc(tid * 16, R, C); const int Rb = Epi::PERM ? ((R & ~31) + perm32(R & 31)) : R;
;         voffA = (unsigned)(R * g.lda + C) * 2u; voffB = (unsigned)(Rb * g.ldb + C) * 2u; }
;     const size_t voffA_step = (size_t)64 * g.lda * 2, voffB_step = (size_t)64 * g.ldb * 2;
;     const size_t kstep = (size_t)(BK * 2);
;     const size_t hstepA = (size_t)HALF * g.lda * 2, hstepB = (size_t)HALF * g.ldb * 2;
;     const size_t tstepA = 2 * hstepA, tstepB = 2 * hstepB;
;     const unsigned ldsw = (unsigned)wid * 1024u;
;     const int aoff = lds_byte(wr * 64 + fr, fq * 8), boff = lds_byte(wc * 32 + fr, fq * 8);
;     ...
;     Unit cur, nxt; int ui = 0;
;     if (!S.next(0, cur)) return;
;     f32x4 acc[2][2][4][2];
;     if constexpr (!SP2) {
; #pragma unroll
;     for (int a = 0; a < 2; ++a)
; #pragma unroll
;         for (int b = 0; b < 2; ++b)
; #pragma unroll
;             for (int m = 0; m < 4; ++m)
; #pragma unroll
;                 for (int n = 0; n < 2; ++n) acc[a][b][m][n] = (f32x4){0.f, 0.f, 0.f, 0.f};
;     }
;     bf16x8 At[4][2], B0[2][2], B1[2][2];
;     const char* cA = (const char*)S.opA(g, cur) + (size_t)cur.pm * tstepA; const char* cB = (const char*)S.opB(g, cur) + (size_t)cur.pn * tstepB;
;     S.a_ready(cur);
;     if constexpr (SP2) {
;         PG8_STAGE(PG8_SB(0, 0), cB, voffB); PG8_STAGE(PG8_SB(0, 1), cB + hstepB, voffB); PG8_STAGE(PG8_SA(0, 0), cA, voffA); PG8_STAGE(PG8_SA(0, 1), cA + hstepA, voffA);
;         if (wr == 1) PG8_BAR;
;         PG8_WAIT_V(2); PG8_BAR;
;         PG8_STAGE(PG8_SB(1, 0), cB + kstep, voffB); PG8_STAGE(PG8_SA(1, 0), cA + kstep, voffA); PG8_STAGE(PG8_SB(1, 1), cB + hstepB + kstep, voffB);
;         if (Epi::NST > 0) PG8_WAIT_V(0); else PG8_WAIT_V(6);
;         PG8_BAR;
;     } else {
;         PG8_STAGE(PG8_SB(0, 0), cB, voffB); PG8_STAGE(PG8_SA(0, 0), cA, voffA); PG8_STAGE(PG8_SB(0, 1), cB + hstepB, voffB); PG8_STAGE(PG8_SA(0, 1), cA + hstepA, voffA);
;         if (wr == 1) PG8_BAR;
.LBB0_577:
	s_or_b64 exec, exec, s[6:7]
	v_readlane_b32 s2, v254, 55
	v_mov_b32_e32 v12, v212
	v_readlane_b32 s3, v254, 56
	s_waitcnt lgkmcnt(0)
	s_barrier
	s_andn2_b64 vcc, exec, s[2:3]
	v_readfirstlane_b32 s0, v12
	s_cbranch_vccnz .LBB0_633
	v_bfe_i32 v4, v12, 27, 1
	v_lshlrev_b32_e32 v3, 4, v12
	v_lshrrev_b32_e32 v4, 22, v4
	v_add_u32_e32 v4, v3, v4
	v_and_b32_e32 v4, 0xfffffc00, v4
	v_sub_u32_e32 v3, v3, v4
	v_lshrrev_b32_e32 v4, 4, v3
	v_ashrrev_i32_e32 v5, 31, v12
	v_bitop3_b32 v3, v4, v3, 32 bitop3:0x6c
	v_lshrrev_b32_e32 v5, 26, v5
	v_ashrrev_i32_e32 v4, 31, v3
	v_add_u32_e32 v5, v12, v5
	v_lshrrev_b32_e32 v4, 26, v4
	v_ashrrev_i32_e32 v9, 6, v5
	v_add_u32_e32 v4, v3, v4
	v_lshlrev_b32_e32 v5, 3, v9
	v_ashrrev_i32_e32 v8, 6, v4
	v_and_b32_e32 v5, -16, v5
	v_add_u32_e32 v5, v8, v5
	v_and_b32_e32 v6, 3, v8
	s_mov_b32 s3, 0xfffe0
	v_lshrrev_b32_e32 v7, 2, v5
	v_lshlrev_b32_e32 v10, 1, v5
	v_and_b32_e32 v4, 0xc0, v4
	v_and_or_b32 v6, v5, s3, v6
	v_and_b32_e32 v7, 4, v7
	v_and_b32_e32 v10, 24, v10
	v_sub_u32_e32 v3, v3, v4
	v_mov_b32_e32 v4, 1
	v_or3_b32 v6, v6, v7, v10
	v_lshlrev_b32_e32 v7, 5, v9
	v_ashrrev_i16_sdwa v3, v4, sext(v3) dst_sel:DWORD dst_unused:UNUSED_PAD src0_sel:DWORD src1_sel:BYTE_0
	s_ashr_i32 s2, s0, 6
	v_and_b32_e32 v10, 32, v7
	v_bfe_i32 v11, v3, 0, 16
	s_lshl_b32 s22, s2, 10
	v_add_u32_e32 v3, v10, v11
	v_lshlrev_b32_e32 v4, 1, v3
	s_movk_i32 s3, 0x840
	v_readlane_b32 s4, v255, 3
	s_add_i32 s23, s22, 0
	v_lshl_add_u32 v194, v6, 12, v4
	v_mul_lo_u32 v4, v5, s3
	v_mov_b32_e32 v195, v2
	v_readlane_b32 s5, v255, 4
	s_add_i32 m0, s23, 0x10000
	v_add_lshl_u32 v196, v3, v4, 1
	v_lshl_add_u64 v[4:5], s[4:5], 0, v[194:195]
	v_lshl_add_u64 v[6:7], v[4:5], 0, s[90:91]
	v_mov_b32_e32 v197, v2
	global_load_lds_dwordx4 v194, s[4:5]
	v_readlane_b32 s4, v254, 61
	s_add_i32 m0, s23, 0x12000
	v_readlane_b32 s5, v254, 62
	global_load_lds_dwordx4 v[6:7], off
	s_nop 0
	v_lshl_add_u64 v[6:7], s[4:5], 0, v[194:195]
	s_add_i32 m0, s23, 0x14000
	v_lshl_add_u64 v[6:7], v[6:7], 0, s[90:91]
	global_load_lds_dwordx4 v194, s[4:5]
	s_add_i32 m0, s23, 0x16000
	v_readlane_b32 s4, v254, 63
	global_load_lds_dwordx4 v[6:7], off
	v_readlane_b32 s5, v255, 0
	s_mov_b32 m0, s23
	s_add_i32 s24, s23, 0x2000
	v_lshl_add_u64 v[6:7], s[4:5], 0, v[196:197]
	v_lshl_add_u64 v[14:15], v[6:7], 0, s[96:97]
	s_add_i32 s25, s23, 0x4000
	global_load_lds_dwordx4 v196, s[4:5]
	v_readlane_b32 s4, v255, 1
	s_mov_b32 m0, s24
	v_readlane_b32 s5, v255, 2
	global_load_lds_dwordx4 v[14:15], off
	s_nop 0
	v_lshl_add_u64 v[14:15], s[4:5], 0, v[196:197]
	s_mov_b32 m0, s25
	s_add_i32 s26, s23, 0x6000
	global_load_lds_dwordx4 v196, s[4:5]
	v_lshl_add_u64 v[14:15], v[14:15], 0, s[96:97]
	s_mov_b32 m0, s26
	s_ashr_i32 s3, s0, 8
	s_cmp_eq_u32 s3, 0
	s_cbranch_scc0 .Lsp_br
	s_setprio 1
.Lsp_br:
	global_load_lds_dwordx4 v[14:15], off
	s_cmp_eq_u32 s3, 1
	s_cselect_b64 s[10:11], -1, 0
	s_cmp_lg_u32 s3, 1
	s_cbranch_scc1 .LBB0_580
	s_barrier

;     __device__ bool next(int i, Unit& u) const { const int rounds = nwg / G; if (i >= rounds) return false; return StaticOrder::next(rounds - 1 - i, u); }
;     __device__ bool next(int i, Unit& u) const { const int rounds = nwg / G; if (i >= 2 * rounds) return false; const bool ok = StaticOrder::next(i >= rounds ? i - rounds : i, u); u.z = (i >= rounds) ? 1 : 0; return ok; }
; #define PG8_TRIP_HEAD(T) const int t = (T); const bool last = (t == nt - 2); \
;             const char* a1 = cA + (size_t)(t + 1) * kstep; \
;             const char* a2 = last ? nA : cA + (size_t)(t + 2) * kstep; const char* b2 = last ? nB : cB + (size_t)(t + 2) * kstep; \
;             const char* a3 = a2 + kstep; const char* b3 = b2 + kstep; \
;             if (last && has_next) S.a_ready(nxt);
; template <class Epi, class Sched, bool ALIGN_EPI = false, bool SP2 = false>
; __device__ __forceinline__ void gemm_phase(PG8_LAS unsigned char* lds, const Gemm g, const Sched& S, const Epi& E) {
;     ...
;         const bool has_next = S.next(ui + 1, nxt);
;         const char* nA = has_next ? (const char*)S.opA(g, nxt) + (size_t)nxt.pm * tstepA : cA; const char* nB = has_next ? (const char*)S.opB(g, nxt) + (size_t)nxt.pn * tstepB : cB;
;     ...
;         if constexpr (SP2) {
;             { PG8_TRIP_HEAD(0) PG8_TRIP_SP2(asm volatile("s_waitcnt vmcnt(%0)" :: "n"(8 + Epi::NST) : "memory"), PG8_MMAZ) }
.LBB0_593:
	v_readlane_b32 s18, v253, 7
	v_readlane_b32 s34, v254, 59
	s_cmp_eq_u32 s29, 0
	v_readlane_b32 s19, v253, 8
	v_readlane_b32 s35, v254, 60
	s_cselect_b32 s33, s35, s19
	s_cselect_b32 s34, s34, s18
	s_ashr_i32 s15, s14, 31
	s_lshl_b64 s[18:19], s[14:15], 20
	s_add_u32 s18, s34, s18
	s_addc_u32 s19, s33, s19
	s_and_b64 s[4:5], s[4:5], exec
	s_cselect_b32 s4, s19, s9
	s_cselect_b32 s5, s18, s8
	s_add_i32 s35, 0, 0x10000
	s_add_i32 s37, 0, 0x14000
	v_add_u32_e32 v116, s35, v219
	v_add_u32_e32 v117, s37, v219
	ds_read_b128 v[4:7], v116
	ds_read_b128 v[8:11], v116 offset:1024
	ds_read_b128 v[12:15], v116 offset:2048
	ds_read_b128 v[16:19], v116 offset:3072
	ds_read_b128 v[20:23], v117
	ds_read_b128 v[24:27], v117 offset:1024
	ds_read_b128 v[28:31], v117 offset:2048
	ds_read_b128 v[32:35], v117 offset:3072
	s_mov_b32 s15, 0
	v_lshl_add_u64 v[192:193], s[20:21], 0, v[196:197]
	s_mov_b64 s[38:39], 0x84080
	s_add_i32 s33, s23, 0xc000
	s_waitcnt vmcnt(0)
	v_lshl_add_u64 v[68:69], v[192:193], 0, s[38:39]
	s_mov_b32 m0, s33
	s_mov_b64 s[38:39], 0xc6080
	s_add_i32 s34, s23, 0xe000
	ds_read_b128 v[36:39], v221
	ds_read_b128 v[40:43], v221 offset:1024
	ds_read_b128 v[44:47], v221 offset:2048
	ds_read_b128 v[48:51], v221 offset:3072
	ds_read_b128 v[52:55], v221 offset:4096
	ds_read_b128 v[56:59], v221 offset:5120
	ds_read_b128 v[60:63], v221 offset:6144
	ds_read_b128 v[64:67], v221 offset:7168
	global_load_lds_dwordx4 v[68:69], off
	v_lshl_add_u64 v[68:69], v[192:193], 0, s[38:39]
	s_mov_b32 m0, s34
	s_nop 0
	global_load_lds_dwordx4 v[68:69], off
	s_waitcnt vmcnt(8)
	s_waitcnt lgkmcnt(0)
	s_barrier
	s_waitcnt lgkmcnt(0)
	v_mfma_f32_16x16x32_bf16 v[92:95], v[4:7], v[60:63], 0
	v_mfma_f32_16x16x32_bf16 v[68:71], v[4:7], v[36:39], 0
	v_mfma_f32_16x16x32_bf16 v[72:75], v[12:15], v[36:39], 0
	v_mfma_f32_16x16x32_bf16 v[76:79], v[4:7], v[44:47], 0
	v_mfma_f32_16x16x32_bf16 v[80:83], v[12:15], v[44:47], 0
	v_mfma_f32_16x16x32_bf16 v[84:87], v[4:7], v[52:55], 0
	v_mfma_f32_16x16x32_bf16 v[88:91], v[12:15], v[52:55], 0
	v_mfma_f32_16x16x32_bf16 v[100:103], v[8:11], v[64:67], v[92:95]
	v_mfma_f32_16x16x32_bf16 v[92:95], v[12:15], v[60:63], 0
	v_mfma_f32_16x16x32_bf16 v[68:71], v[8:11], v[40:43], v[68:71]
	v_mfma_f32_16x16x32_bf16 v[72:75], v[16:19], v[40:43], v[72:75]
	v_mfma_f32_16x16x32_bf16 v[76:79], v[8:11], v[48:51], v[76:79]
	v_mfma_f32_16x16x32_bf16 v[80:83], v[16:19], v[48:51], v[80:83]
	v_mfma_f32_16x16x32_bf16 v[84:87], v[8:11], v[56:59], v[84:87]
	v_mfma_f32_16x16x32_bf16 v[88:91], v[16:19], v[56:59], v[88:91]
	v_mfma_f32_16x16x32_bf16 v[104:107], v[16:19], v[64:67], v[92:95]
	v_mfma_f32_16x16x32_bf16 v[92:95], v[20:23], v[36:39], 0
	v_mfma_f32_16x16x32_bf16 v[36:39], v[28:31], v[36:39], 0
	v_mfma_f32_16x16x32_bf16 v[118:121], v[24:27], v[40:43], v[92:95]
	v_mfma_f32_16x16x32_bf16 v[36:39], v[32:35], v[40:43], v[36:39]
	v_mfma_f32_16x16x32_bf16 v[40:43], v[20:23], v[44:47], 0
	v_mfma_f32_16x16x32_bf16 v[44:47], v[28:31], v[44:47], 0
	v_mfma_f32_16x16x32_bf16 v[40:43], v[24:27], v[48:51], v[40:43]
	v_mfma_f32_16x16x32_bf16 v[44:47], v[32:35], v[48:51], v[44:47]
	v_mfma_f32_16x16x32_bf16 v[48:51], v[20:23], v[52:55], 0
	v_mfma_f32_16x16x32_bf16 v[52:55], v[28:31], v[52:55], 0
	v_mfma_f32_16x16x32_bf16 v[48:51], v[24:27], v[56:59], v[48:51]
	v_mfma_f32_16x16x32_bf16 v[52:55], v[32:35], v[56:59], v[52:55]
	v_mfma_f32_16x16x32_bf16 v[56:59], v[20:23], v[60:63], 0
	v_mfma_f32_16x16x32_bf16 v[60:63], v[28:31], v[60:63], 0
	v_mfma_f32_16x16x32_bf16 v[56:59], v[24:27], v[64:67], v[56:59]
	v_mfma_f32_16x16x32_bf16 v[60:63], v[32:35], v[64:67], v[60:63]
	s_barrier
	v_lshl_add_u64 v[250:251], s[8:9], 0, v[194:195]
	s_mov_b64 s[40:41], 0x100
	s_add_i32 s35, s35, s22
	v_lshl_add_u64 v[134:135], v[250:251], 0, s[40:41]
	s_mov_b32 m0, s35
	s_mov_b64 s[38:39], 0x40100
	s_add_i32 s36, s35, 0x2000
	ds_read_b128 v[64:67], v221 offset:16384
	ds_read_b128 v[92:95], v221 offset:17408
	ds_read_b128 v[96:99], v221 offset:18432
	ds_read_b128 v[108:111], v221 offset:19456
	ds_read_b128 v[112:115], v221 offset:20480
	ds_read_b128 v[122:125], v221 offset:21504
	ds_read_b128 v[126:129], v221 offset:22528
	ds_read_b128 v[130:133], v221 offset:23552
	global_load_lds_dwordx4 v[134:135], off
	v_lshl_add_u64 v[134:135], v[250:251], 0, s[38:39]
	s_mov_b32 m0, s36
	s_mov_b64 s[38:39], 0x80100
	s_add_i32 s37, s37, s22
	global_load_lds_dwordx4 v[134:135], off
	v_lshl_add_u64 v[134:135], v[250:251], 0, s[38:39]
	s_mov_b32 m0, s37
	s_mov_b64 s[38:39], 0xc0100
	global_load_lds_dwordx4 v[134:135], off
	v_lshl_add_u64 v[134:135], v[250:251], 0, s[38:39]
	s_add_i32 s38, s37, 0x2000
	s_mov_b32 m0, s38
	s_nop 0
	global_load_lds_dwordx4 v[134:135], off
	v_lshl_add_u64 v[134:135], v[192:193], 0, s[40:41]
	s_mov_b32 m0, s23
	s_mov_b64 s[40:41], 0x42100
	global_load_lds_dwordx4 v[134:135], off
	v_lshl_add_u64 v[134:135], v[192:193], 0, s[40:41]
	s_mov_b32 m0, s24
	s_nop 0
	global_load_lds_dwordx4 v[134:135], off
	s_waitcnt vmcnt(8)
	s_waitcnt lgkmcnt(0)
	s_barrier
; #define PG8_TRIP_HEAD(T) const int t = (T); const bool last = (t == nt - 2); \
;             const char* a1 = cA + (size_t)(t + 1) * kstep; \
;             const char* a2 = last ? nA : cA + (size_t)(t + 2) * kstep; const char* b2 = last ? nB : cB + (size_t)(t + 2) * kstep; \
;             const char* a3 = a2 + kstep; const char* b3 = b2 + kstep; \
;             if (last && has_next) S.a_ready(nxt);
; template <class Epi, class Sched, bool ALIGN_EPI = false, bool SP2 = false>
; __device__ __forceinline__ void gemm_phase(PG8_LAS unsigned char* lds, const Gemm g, const Sched& S, const Epi& E) {
;     ...
;         if constexpr (SP2) {
;             { PG8_TRIP_HEAD(0) PG8_TRIP_SP2(asm volatile("s_waitcnt vmcnt(%0)" :: "n"(8 + Epi::NST) : "memory"), PG8_MMAZ) }
	s_waitcnt lgkmcnt(0)
	v_mfma_f32_16x16x32_bf16 v[134:137], v[4:7], v[64:67], 0
	v_mfma_f32_16x16x32_bf16 v[144:147], v[4:7], v[96:99], 0
	v_mfma_f32_16x16x32_bf16 v[152:155], v[4:7], v[112:115], 0
	v_mfma_f32_16x16x32_bf16 v[4:7], v[4:7], v[126:129], 0
	v_mfma_f32_16x16x32_bf16 v[136:139], v[8:11], v[92:95], v[134:137]
	v_mfma_f32_16x16x32_bf16 v[144:147], v[8:11], v[108:111], v[144:147]
	v_mfma_f32_16x16x32_bf16 v[152:155], v[8:11], v[122:125], v[152:155]
	v_mfma_f32_16x16x32_bf16 v[4:7], v[8:11], v[130:133], v[4:7]
	v_mfma_f32_16x16x32_bf16 v[8:11], v[12:15], v[126:129], 0
	v_mfma_f32_16x16x32_bf16 v[140:143], v[12:15], v[64:67], 0
	v_mfma_f32_16x16x32_bf16 v[148:151], v[12:15], v[96:99], 0
	v_mfma_f32_16x16x32_bf16 v[156:159], v[12:15], v[112:115], 0
	v_mfma_f32_16x16x32_bf16 v[8:11], v[16:19], v[130:133], v[8:11]
	v_mfma_f32_16x16x32_bf16 v[140:143], v[16:19], v[92:95], v[140:143]
	v_mfma_f32_16x16x32_bf16 v[148:151], v[16:19], v[108:111], v[148:151]
	v_mfma_f32_16x16x32_bf16 v[156:159], v[16:19], v[122:125], v[156:159]
	v_mfma_f32_16x16x32_bf16 v[12:15], v[20:23], v[64:67], 0
	v_mfma_f32_16x16x32_bf16 v[160:163], v[24:27], v[92:95], v[12:15]
	v_mfma_f32_16x16x32_bf16 v[12:15], v[28:31], v[64:67], 0
	v_mfma_f32_16x16x32_bf16 v[164:167], v[32:35], v[92:95], v[12:15]
	v_mfma_f32_16x16x32_bf16 v[12:15], v[20:23], v[96:99], 0
	v_mfma_f32_16x16x32_bf16 v[168:171], v[24:27], v[108:111], v[12:15]
	v_mfma_f32_16x16x32_bf16 v[12:15], v[28:31], v[96:99], 0
	v_mfma_f32_16x16x32_bf16 v[172:175], v[32:35], v[108:111], v[12:15]
	v_mfma_f32_16x16x32_bf16 v[12:15], v[20:23], v[112:115], 0
	v_mfma_f32_16x16x32_bf16 v[176:179], v[24:27], v[122:125], v[12:15]
	v_mfma_f32_16x16x32_bf16 v[12:15], v[28:31], v[112:115], 0
	v_mfma_f32_16x16x32_bf16 v[180:183], v[32:35], v[122:125], v[12:15]
	v_mfma_f32_16x16x32_bf16 v[12:15], v[20:23], v[126:129], 0
	v_mfma_f32_16x16x32_bf16 v[184:187], v[24:27], v[130:133], v[12:15]
	v_mfma_f32_16x16x32_bf16 v[12:15], v[28:31], v[126:129], 0
	v_mfma_f32_16x16x32_bf16 v[188:191], v[32:35], v[130:133], v[12:15]
	s_barrier
	s_add_i32 s39, 0, 0x18000
	s_add_i32 s41, 0, 0x1c000
	v_add_u32_e32 v134, s39, v219
	v_add_u32_e32 v135, s41, v219
	s_nop 0
	ds_read_b128 v[12:15], v134
	ds_read_b128 v[16:19], v134 offset:1024
	ds_read_b128 v[20:23], v134 offset:2048
	ds_read_b128 v[24:27], v134 offset:3072
	ds_read_b128 v[202:205], v135
	ds_read_b128 v[206:209], v135 offset:1024
	ds_read_b128 v[222:225], v135 offset:2048
	ds_read_b128 v[226:229], v135 offset:3072
	s_mov_b64 s[42:43], 0x84100
	s_mov_b32 m0, s25
	v_lshl_add_u64 v[92:93], v[192:193], 0, s[42:43]
	s_mov_b64 s[42:43], 0xc6100
	ds_read_b128 v[28:31], v221 offset:32768
	ds_read_b128 v[32:35], v221 offset:33792
	ds_read_b128 v[64:67], v221 offset:34816
	ds_read_b128 v[230:233], v221 offset:35840
	ds_read_b128 v[234:237], v221 offset:36864
	ds_read_b128 v[238:241], v221 offset:37888
	ds_read_b128 v[242:245], v221 offset:38912
	ds_read_b128 v[246:249], v221 offset:39936
	global_load_lds_dwordx4 v[92:93], off
	v_lshl_add_u64 v[92:93], v[192:193], 0, s[42:43]
	s_mov_b32 m0, s26
	s_nop 0
	global_load_lds_dwordx4 v[92:93], off
	s_waitcnt vmcnt(8)
	s_waitcnt lgkmcnt(0)
	s_barrier
	s_waitcnt lgkmcnt(0)
	v_mfma_f32_16x16x32_bf16 v[68:71], v[12:15], v[28:31], v[68:71]
	v_mfma_f32_16x16x32_bf16 v[130:133], v[16:19], v[32:35], v[68:71]
	v_mfma_f32_16x16x32_bf16 v[68:71], v[20:23], v[28:31], v[72:75]
	v_mfma_f32_16x16x32_bf16 v[126:129], v[24:27], v[32:35], v[68:71]
	v_mfma_f32_16x16x32_bf16 v[68:71], v[12:15], v[64:67], v[76:79]
	v_mfma_f32_16x16x32_bf16 v[112:115], v[16:19], v[230:233], v[68:71]
	v_mfma_f32_16x16x32_bf16 v[68:71], v[20:23], v[64:67], v[80:83]
	v_mfma_f32_16x16x32_bf16 v[108:111], v[24:27], v[230:233], v[68:71]
	v_mfma_f32_16x16x32_bf16 v[68:71], v[12:15], v[234:237], v[84:87]
	v_mfma_f32_16x16x32_bf16 v[96:99], v[16:19], v[238:241], v[68:71]
	v_mfma_f32_16x16x32_bf16 v[68:71], v[20:23], v[234:237], v[88:91]
	v_mfma_f32_16x16x32_bf16 v[92:95], v[24:27], v[238:241], v[68:71]
	v_mfma_f32_16x16x32_bf16 v[68:71], v[12:15], v[242:245], v[100:103]
	v_mfma_f32_16x16x32_bf16 v[80:83], v[16:19], v[246:249], v[68:71]
	v_mfma_f32_16x16x32_bf16 v[68:71], v[20:23], v[242:245], v[104:107]
	v_mfma_f32_16x16x32_bf16 v[76:79], v[24:27], v[246:249], v[68:71]
	v_mfma_f32_16x16x32_bf16 v[68:71], v[202:205], v[28:31], v[118:121]
	v_mfma_f32_16x16x32_bf16 v[28:31], v[222:225], v[28:31], v[36:39]
	v_mfma_f32_16x16x32_bf16 v[118:121], v[226:229], v[32:35], v[28:31]
	v_mfma_f32_16x16x32_bf16 v[28:31], v[202:205], v[64:67], v[40:43]
	v_mfma_f32_16x16x32_bf16 v[104:107], v[206:209], v[230:233], v[28:31]
	v_mfma_f32_16x16x32_bf16 v[28:31], v[222:225], v[64:67], v[44:47]
	v_mfma_f32_16x16x32_bf16 v[100:103], v[226:229], v[230:233], v[28:31]
	v_mfma_f32_16x16x32_bf16 v[28:31], v[202:205], v[234:237], v[48:51]
	v_mfma_f32_16x16x32_bf16 v[88:91], v[206:209], v[238:241], v[28:31]
	v_mfma_f32_16x16x32_bf16 v[28:31], v[222:225], v[234:237], v[52:55]
	v_mfma_f32_16x16x32_bf16 v[84:87], v[226:229], v[238:241], v[28:31]
	v_mfma_f32_16x16x32_bf16 v[28:31], v[202:205], v[242:245], v[56:59]
	v_mfma_f32_16x16x32_bf16 v[72:75], v[206:209], v[246:249], v[28:31]
	v_mfma_f32_16x16x32_bf16 v[28:31], v[222:225], v[242:245], v[60:63]
	v_mfma_f32_16x16x32_bf16 v[122:125], v[206:209], v[32:35], v[68:71]
	v_mfma_f32_16x16x32_bf16 v[68:71], v[226:229], v[246:249], v[28:31]
	s_barrier
; #define PG8_MMA(ai, bj, At, Bt) do { __builtin_amdgcn_s_setprio(1); _Pragma("unroll") for (int m = 0; m < 4; ++m) _Pragma("unroll") for (int n = 0; n < 2; ++n) _Pragma("unroll") for (int k = 0; k < 2; ++k) \
;         acc[ai][bj][m][n] = __builtin_amdgcn_mfma_f32_16x16x32_bf16(Bt[n][k], At[m][k], acc[ai][bj][m][n], 0, 0, 0); __builtin_amdgcn_s_setprio(0); } while (0)
; #define PG8_WAIT_V(n) asm volatile("s_waitcnt vmcnt(" #n ")" ::: "memory")
; #define PG8_TRIP_HEAD(T) const int t = (T); const bool last = (t == nt - 2); \
;             const char* a1 = cA + (size_t)(t + 1) * kstep; \
;             const char* a2 = last ? nA : cA + (size_t)(t + 2) * kstep; const char* b2 = last ? nB : cB + (size_t)(t + 2) * kstep; \
;             const char* a3 = a2 + kstep; const char* b3 = b2 + kstep; \
;             if (last && has_next) S.a_ready(nxt);
; template <class Epi, class Sched, bool ALIGN_EPI = false, bool SP2 = false>
; __device__ __forceinline__ void gemm_phase(PG8_LAS unsigned char* lds, const Gemm g, const Sched& S, const Epi& E) {
;     ...
;         if constexpr (SP2) {
;             { PG8_TRIP_HEAD(0) PG8_TRIP_SP2(asm volatile("s_waitcnt vmcnt(%0)" :: "n"(8 + Epi::NST) : "memory"), PG8_MMAZ) }
;             for (int tt = 2; tt < nt; tt += 2) { PG8_TRIP_HEAD(tt) PG8_TRIP_SP2(PG8_WAIT_V(8), PG8_MMA) }
	s_mov_b64 s[44:45], 0x180
	s_add_i32 s39, s39, s22
	s_nop 1
	v_lshl_add_u64 v[28:29], v[250:251], 0, s[44:45]
	s_mov_b32 m0, s39
	s_mov_b64 s[42:43], 0x40180
	s_add_i32 s40, s39, 0x2000
	ds_read_b128 v[36:39], v221 offset:49152
	ds_read_b128 v[40:43], v221 offset:50176
	ds_read_b128 v[230:233], v221 offset:51200
	ds_read_b128 v[234:237], v221 offset:52224
	ds_read_b128 v[238:241], v221 offset:53248
	ds_read_b128 v[242:245], v221 offset:54272
	ds_read_b128 v[246:249], v221 offset:55296
	ds_read_b128 v[214:217], v221 offset:56320
	global_load_lds_dwordx4 v[28:29], off
	v_lshl_add_u64 v[28:29], v[250:251], 0, s[42:43]
	s_mov_b32 m0, s40
	s_mov_b64 s[42:43], 0x80180
	s_add_i32 s41, s41, s22
	global_load_lds_dwordx4 v[28:29], off
	v_lshl_add_u64 v[28:29], v[250:251], 0, s[42:43]
	s_mov_b32 m0, s41
	s_mov_b64 s[42:43], 0xc0180
	global_load_lds_dwordx4 v[28:29], off
	v_lshl_add_u64 v[28:29], v[250:251], 0, s[42:43]
	s_add_i32 s42, s41, 0x2000
	s_mov_b32 m0, s42
	s_nop 0
	global_load_lds_dwordx4 v[28:29], off
	v_lshl_add_u64 v[28:29], v[192:193], 0, s[44:45]
	s_mov_b32 m0, s27
	s_mov_b64 s[44:45], 0x42180
	global_load_lds_dwordx4 v[28:29], off
	v_lshl_add_u64 v[28:29], v[192:193], 0, s[44:45]
	s_mov_b32 m0, s28
	s_nop 0
	global_load_lds_dwordx4 v[28:29], off
	s_waitcnt vmcnt(8)
	s_waitcnt lgkmcnt(0)
	s_barrier
	s_waitcnt lgkmcnt(0)
	v_mfma_f32_16x16x32_bf16 v[28:31], v[12:15], v[36:39], v[136:139]
	v_mfma_f32_16x16x32_bf16 v[64:67], v[16:19], v[40:43], v[28:31]
	v_mfma_f32_16x16x32_bf16 v[28:31], v[20:23], v[36:39], v[140:143]
	v_mfma_f32_16x16x32_bf16 v[60:63], v[24:27], v[40:43], v[28:31]
	v_mfma_f32_16x16x32_bf16 v[28:31], v[12:15], v[230:233], v[144:147]
	v_mfma_f32_16x16x32_bf16 v[48:51], v[16:19], v[234:237], v[28:31]
	v_mfma_f32_16x16x32_bf16 v[28:31], v[20:23], v[230:233], v[148:151]
	v_mfma_f32_16x16x32_bf16 v[44:47], v[24:27], v[234:237], v[28:31]
	v_mfma_f32_16x16x32_bf16 v[28:31], v[12:15], v[238:241], v[152:155]
	v_mfma_f32_16x16x32_bf16 v[4:7], v[12:15], v[246:249], v[4:7]
	v_mfma_f32_16x16x32_bf16 v[32:35], v[16:19], v[242:245], v[28:31]
	v_mfma_f32_16x16x32_bf16 v[28:31], v[20:23], v[238:241], v[156:159]
	v_mfma_f32_16x16x32_bf16 v[16:19], v[16:19], v[214:217], v[4:7]
	v_mfma_f32_16x16x32_bf16 v[4:7], v[20:23], v[246:249], v[8:11]
	v_mfma_f32_16x16x32_bf16 v[28:31], v[24:27], v[242:245], v[28:31]
	v_mfma_f32_16x16x32_bf16 v[12:15], v[24:27], v[214:217], v[4:7]
	v_mfma_f32_16x16x32_bf16 v[4:7], v[202:205], v[36:39], v[160:163]
	v_mfma_f32_16x16x32_bf16 v[56:59], v[206:209], v[40:43], v[4:7]
	v_mfma_f32_16x16x32_bf16 v[4:7], v[222:225], v[36:39], v[164:167]
	v_mfma_f32_16x16x32_bf16 v[52:55], v[226:229], v[40:43], v[4:7]
	v_mfma_f32_16x16x32_bf16 v[4:7], v[202:205], v[230:233], v[168:171]
	v_mfma_f32_16x16x32_bf16 v[40:43], v[206:209], v[234:237], v[4:7]
	v_mfma_f32_16x16x32_bf16 v[4:7], v[222:225], v[230:233], v[172:175]
	v_mfma_f32_16x16x32_bf16 v[36:39], v[226:229], v[234:237], v[4:7]
	v_mfma_f32_16x16x32_bf16 v[4:7], v[202:205], v[238:241], v[176:179]
	v_mfma_f32_16x16x32_bf16 v[24:27], v[206:209], v[242:245], v[4:7]
	v_mfma_f32_16x16x32_bf16 v[4:7], v[222:225], v[238:241], v[180:183]
	v_mfma_f32_16x16x32_bf16 v[20:23], v[226:229], v[242:245], v[4:7]
	v_mfma_f32_16x16x32_bf16 v[4:7], v[202:205], v[246:249], v[184:187]
	v_mfma_f32_16x16x32_bf16 v[8:11], v[206:209], v[214:217], v[4:7]
	v_mfma_f32_16x16x32_bf16 v[4:7], v[222:225], v[246:249], v[188:191]
	v_mfma_f32_16x16x32_bf16 v[4:7], v[226:229], v[214:217], v[4:7]
	s_barrier
	s_add_u32 s20, s20, 0x84180
	s_addc_u32 s21, s21, 0
	s_add_u32 s8, s8, 0x200
	s_addc_u32 s9, s9, 0
	s_mov_b64 s[48:49], 0x80000
	s_mov_b64 s[50:51], 0x80080
	s_mov_b64 s[52:53], 0xc0000
	s_mov_b64 s[54:55], 0xc0080
	s_mov_b64 s[56:57], 0xc6000
.LBB0_594:
	ds_read_b128 v[136:139], v116
	ds_read_b128 v[140:143], v116 offset:1024
	ds_read_b128 v[144:147], v116 offset:2048
	ds_read_b128 v[148:151], v116 offset:3072
	ds_read_b128 v[152:155], v117
	ds_read_b128 v[156:159], v117 offset:1024
	ds_read_b128 v[160:163], v117 offset:2048
	ds_read_b128 v[164:167], v117 offset:3072
	s_add_u32 s43, s20, 0xfff7c080
	s_addc_u32 s44, s21, -1
	s_cmp_eq_u32 s15, 28
	s_cselect_b32 s45, s17, s44
	s_cselect_b32 s44, s16, s43
	s_cselect_b32 s47, s4, s9
	s_cselect_b32 s46, s5, s8
	s_mov_b32 m0, s33
	v_lshl_add_u64 v[192:193], s[20:21], 0, v[200:201]
	ds_read_b128 v[168:171], v221
	ds_read_b128 v[172:175], v221 offset:1024
	ds_read_b128 v[176:179], v221 offset:2048
	ds_read_b128 v[180:183], v221 offset:3072
	ds_read_b128 v[184:187], v221 offset:4096
	ds_read_b128 v[188:191], v221 offset:5120
	ds_read_b128 v[202:205], v221 offset:6144
	ds_read_b128 v[206:209], v221 offset:7168
	global_load_lds_dwordx4 v[192:193], off
	v_lshl_add_u64 v[192:193], v[192:193], 0, s[96:97]
	s_mov_b32 m0, s34
	s_nop 0
	global_load_lds_dwordx4 v[192:193], off
	s_waitcnt vmcnt(8)
	s_waitcnt lgkmcnt(0)
	s_barrier
; #define PG8_MMA(ai, bj, At, Bt) do { __builtin_amdgcn_s_setprio(1); _Pragma("unroll") for (int m = 0; m < 4; ++m) _Pragma("unroll") for (int n = 0; n < 2; ++n) _Pragma("unroll") for (int k = 0; k < 2; ++k) \
;         acc[ai][bj][m][n] = __builtin_amdgcn_mfma_f32_16x16x32_bf16(Bt[n][k], At[m][k], acc[ai][bj][m][n], 0, 0, 0); __builtin_amdgcn_s_setprio(0); } while (0)
; #define PG8_WAIT_V(n) asm volatile("s_waitcnt vmcnt(" #n ")" ::: "memory")
; #define PG8_TRIP_HEAD(T) const int t = (T); const bool last = (t == nt - 2); \
;             const char* a1 = cA + (size_t)(t + 1) * kstep; \
;             const char* a2 = last ? nA : cA + (size_t)(t + 2) * kstep; const char* b2 = last ? nB : cB + (size_t)(t + 2) * kstep; \
;             const char* a3 = a2 + kstep; const char* b3 = b2 + kstep; \
;             if (last && has_next) S.a_ready(nxt);
; template <class Epi, class Sched, bool ALIGN_EPI = false, bool SP2 = false>
; __device__ __forceinline__ void gemm_phase(PG8_LAS unsigned char* lds, const Gemm g, const Sched& S, const Epi& E) {
;     ...
;         if constexpr (SP2) {
;             { PG8_TRIP_HEAD(0) PG8_TRIP_SP2(asm volatile("s_waitcnt vmcnt(%0)" :: "n"(8 + Epi::NST) : "memory"), PG8_MMAZ) }
;             for (int tt = 2; tt < nt; tt += 2) { PG8_TRIP_HEAD(tt) PG8_TRIP_SP2(PG8_WAIT_V(8), PG8_MMA) }
	s_waitcnt lgkmcnt(0)
	v_mfma_f32_16x16x32_bf16 v[130:133], v[136:139], v[168:171], v[130:133]
	v_mfma_f32_16x16x32_bf16 v[126:129], v[144:147], v[168:171], v[126:129]
	v_mfma_f32_16x16x32_bf16 v[112:115], v[136:139], v[176:179], v[112:115]
	v_mfma_f32_16x16x32_bf16 v[108:111], v[144:147], v[176:179], v[108:111]
	v_mfma_f32_16x16x32_bf16 v[96:99], v[136:139], v[184:187], v[96:99]
	v_mfma_f32_16x16x32_bf16 v[92:95], v[144:147], v[184:187], v[92:95]
	v_mfma_f32_16x16x32_bf16 v[80:83], v[136:139], v[202:205], v[80:83]
	v_mfma_f32_16x16x32_bf16 v[76:79], v[144:147], v[202:205], v[76:79]
	v_mfma_f32_16x16x32_bf16 v[130:133], v[140:143], v[172:175], v[130:133]
	v_mfma_f32_16x16x32_bf16 v[126:129], v[148:151], v[172:175], v[126:129]
	v_mfma_f32_16x16x32_bf16 v[112:115], v[140:143], v[180:183], v[112:115]
	v_mfma_f32_16x16x32_bf16 v[108:111], v[148:151], v[180:183], v[108:111]
	v_mfma_f32_16x16x32_bf16 v[96:99], v[140:143], v[188:191], v[96:99]
	v_mfma_f32_16x16x32_bf16 v[92:95], v[148:151], v[188:191], v[92:95]
	v_mfma_f32_16x16x32_bf16 v[80:83], v[140:143], v[206:209], v[80:83]
	v_mfma_f32_16x16x32_bf16 v[76:79], v[148:151], v[206:209], v[76:79]
	v_mfma_f32_16x16x32_bf16 v[122:125], v[152:155], v[168:171], v[122:125]
	v_mfma_f32_16x16x32_bf16 v[118:121], v[160:163], v[168:171], v[118:121]
	v_mfma_f32_16x16x32_bf16 v[104:107], v[152:155], v[176:179], v[104:107]
	v_mfma_f32_16x16x32_bf16 v[100:103], v[160:163], v[176:179], v[100:103]
	v_mfma_f32_16x16x32_bf16 v[88:91], v[152:155], v[184:187], v[88:91]
	v_mfma_f32_16x16x32_bf16 v[84:87], v[160:163], v[184:187], v[84:87]
	v_mfma_f32_16x16x32_bf16 v[72:75], v[152:155], v[202:205], v[72:75]
	v_mfma_f32_16x16x32_bf16 v[68:71], v[160:163], v[202:205], v[68:71]
	v_mfma_f32_16x16x32_bf16 v[122:125], v[156:159], v[172:175], v[122:125]
	v_mfma_f32_16x16x32_bf16 v[118:121], v[164:167], v[172:175], v[118:121]
	v_mfma_f32_16x16x32_bf16 v[104:107], v[156:159], v[180:183], v[104:107]
	v_mfma_f32_16x16x32_bf16 v[100:103], v[164:167], v[180:183], v[100:103]
	v_mfma_f32_16x16x32_bf16 v[88:91], v[156:159], v[188:191], v[88:91]
	v_mfma_f32_16x16x32_bf16 v[84:87], v[164:167], v[188:191], v[84:87]
	v_mfma_f32_16x16x32_bf16 v[72:75], v[156:159], v[206:209], v[72:75]
	v_mfma_f32_16x16x32_bf16 v[68:71], v[164:167], v[206:209], v[68:71]
	s_barrier
	s_mov_b32 m0, s35
	v_lshl_add_u64 v[192:193], s[46:47], 0, v[194:195]
	ds_read_b128 v[168:171], v221 offset:16384
	ds_read_b128 v[172:175], v221 offset:17408
	ds_read_b128 v[176:179], v221 offset:18432
	ds_read_b128 v[180:183], v221 offset:19456
	ds_read_b128 v[184:187], v221 offset:20480
	ds_read_b128 v[188:191], v221 offset:21504
	ds_read_b128 v[202:205], v221 offset:22528
	ds_read_b128 v[206:209], v221 offset:23552
	global_load_lds_dwordx4 v[192:193], off
	v_lshl_add_u64 v[214:215], v[192:193], 0, s[90:91]
	s_mov_b32 m0, s36
	s_nop 0
	global_load_lds_dwordx4 v[214:215], off
	v_lshl_add_u64 v[214:215], v[192:193], 0, s[48:49]
	s_mov_b32 m0, s37
	s_nop 0
	global_load_lds_dwordx4 v[214:215], off
	v_lshl_add_u64 v[214:215], v[192:193], 0, s[52:53]
	s_mov_b32 m0, s38
	s_nop 0
	global_load_lds_dwordx4 v[214:215], off
	v_lshl_add_u64 v[214:215], s[44:45], 0, v[196:197]
	s_mov_b32 m0, s23
	v_lshl_add_u64 v[216:217], v[214:215], 0, s[96:97]
	global_load_lds_dwordx4 v[214:215], off
	s_mov_b32 m0, s24
	s_nop 0
	global_load_lds_dwordx4 v[216:217], off
	s_waitcnt vmcnt(8)
	s_waitcnt lgkmcnt(0)
	s_barrier
	s_waitcnt lgkmcnt(0)
	v_mfma_f32_16x16x32_bf16 v[64:67], v[136:139], v[168:171], v[64:67]
	v_mfma_f32_16x16x32_bf16 v[60:63], v[144:147], v[168:171], v[60:63]
	v_mfma_f32_16x16x32_bf16 v[48:51], v[136:139], v[176:179], v[48:51]
	v_mfma_f32_16x16x32_bf16 v[44:47], v[144:147], v[176:179], v[44:47]
	v_mfma_f32_16x16x32_bf16 v[32:35], v[136:139], v[184:187], v[32:35]
	v_mfma_f32_16x16x32_bf16 v[28:31], v[144:147], v[184:187], v[28:31]
	v_mfma_f32_16x16x32_bf16 v[16:19], v[136:139], v[202:205], v[16:19]
	v_mfma_f32_16x16x32_bf16 v[12:15], v[144:147], v[202:205], v[12:15]
	v_mfma_f32_16x16x32_bf16 v[64:67], v[140:143], v[172:175], v[64:67]
	v_mfma_f32_16x16x32_bf16 v[60:63], v[148:151], v[172:175], v[60:63]
	v_mfma_f32_16x16x32_bf16 v[48:51], v[140:143], v[180:183], v[48:51]
	v_mfma_f32_16x16x32_bf16 v[44:47], v[148:151], v[180:183], v[44:47]
	v_mfma_f32_16x16x32_bf16 v[32:35], v[140:143], v[188:191], v[32:35]
	v_mfma_f32_16x16x32_bf16 v[28:31], v[148:151], v[188:191], v[28:31]
	v_mfma_f32_16x16x32_bf16 v[16:19], v[140:143], v[206:209], v[16:19]
	v_mfma_f32_16x16x32_bf16 v[12:15], v[148:151], v[206:209], v[12:15]
	v_mfma_f32_16x16x32_bf16 v[56:59], v[152:155], v[168:171], v[56:59]
	v_mfma_f32_16x16x32_bf16 v[52:55], v[160:163], v[168:171], v[52:55]
	v_mfma_f32_16x16x32_bf16 v[40:43], v[152:155], v[176:179], v[40:43]
	v_mfma_f32_16x16x32_bf16 v[36:39], v[160:163], v[176:179], v[36:39]
	v_mfma_f32_16x16x32_bf16 v[24:27], v[152:155], v[184:187], v[24:27]
	v_mfma_f32_16x16x32_bf16 v[20:23], v[160:163], v[184:187], v[20:23]
	v_mfma_f32_16x16x32_bf16 v[8:11], v[152:155], v[202:205], v[8:11]
	v_mfma_f32_16x16x32_bf16 v[4:7], v[160:163], v[202:205], v[4:7]
	v_mfma_f32_16x16x32_bf16 v[56:59], v[156:159], v[172:175], v[56:59]
	v_mfma_f32_16x16x32_bf16 v[52:55], v[164:167], v[172:175], v[52:55]
	v_mfma_f32_16x16x32_bf16 v[40:43], v[156:159], v[180:183], v[40:43]
	v_mfma_f32_16x16x32_bf16 v[36:39], v[164:167], v[180:183], v[36:39]
	v_mfma_f32_16x16x32_bf16 v[24:27], v[156:159], v[188:191], v[24:27]
	v_mfma_f32_16x16x32_bf16 v[20:23], v[164:167], v[188:191], v[20:23]
	v_mfma_f32_16x16x32_bf16 v[8:11], v[156:159], v[206:209], v[8:11]
	v_mfma_f32_16x16x32_bf16 v[4:7], v[164:167], v[206:209], v[4:7]
	s_barrier
; #define PG8_MMA(ai, bj, At, Bt) do { __builtin_amdgcn_s_setprio(1); _Pragma("unroll") for (int m = 0; m < 4; ++m) _Pragma("unroll") for (int n = 0; n < 2; ++n) _Pragma("unroll") for (int k = 0; k < 2; ++k) \
;         acc[ai][bj][m][n] = __builtin_amdgcn_mfma_f32_16x16x32_bf16(Bt[n][k], At[m][k], acc[ai][bj][m][n], 0, 0, 0); __builtin_amdgcn_s_setprio(0); } while (0)
; #define PG8_WAIT_V(n) asm volatile("s_waitcnt vmcnt(" #n ")" ::: "memory")
; #define PG8_BAR __builtin_amdgcn_s_barrier()
; #define PG8_TRIP_HEAD(T) const int t = (T); const bool last = (t == nt - 2); \
;             const char* a1 = cA + (size_t)(t + 1) * kstep; \
;             const char* a2 = last ? nA : cA + (size_t)(t + 2) * kstep; const char* b2 = last ? nB : cB + (size_t)(t + 2) * kstep; \
;             const char* a3 = a2 + kstep; const char* b3 = b2 + kstep; \
;             if (last && has_next) S.a_ready(nxt);
; template <class Epi, class Sched, bool ALIGN_EPI = false, bool SP2 = false>
; __device__ __forceinline__ void gemm_phase(PG8_LAS unsigned char* lds, const Gemm g, const Sched& S, const Epi& E) {
;     ...
;         if constexpr (SP2) {
;             { PG8_TRIP_HEAD(0) PG8_TRIP_SP2(asm volatile("s_waitcnt vmcnt(%0)" :: "n"(8 + Epi::NST) : "memory"), PG8_MMAZ) }
;             for (int tt = 2; tt < nt; tt += 2) { PG8_TRIP_HEAD(tt) PG8_TRIP_SP2(PG8_WAIT_V(8), PG8_MMA) }
;     ...
;         if constexpr (ALIGN_EPI) { if (wr == 0) PG8_BAR; }
	ds_read_b128 v[136:139], v134
	ds_read_b128 v[140:143], v134 offset:1024
	ds_read_b128 v[144:147], v134 offset:2048
	ds_read_b128 v[148:151], v134 offset:3072
	ds_read_b128 v[152:155], v135
	ds_read_b128 v[156:159], v135 offset:1024
	ds_read_b128 v[160:163], v135 offset:2048
	ds_read_b128 v[164:167], v135 offset:3072
	s_mov_b32 m0, s25
	v_lshl_add_u64 v[216:217], v[214:215], 0, s[82:83]
	ds_read_b128 v[168:171], v221 offset:32768
	ds_read_b128 v[172:175], v221 offset:33792
	ds_read_b128 v[176:179], v221 offset:34816
	ds_read_b128 v[180:183], v221 offset:35840
	ds_read_b128 v[184:187], v221 offset:36864
	ds_read_b128 v[188:191], v221 offset:37888
	ds_read_b128 v[202:205], v221 offset:38912
	ds_read_b128 v[206:209], v221 offset:39936
	global_load_lds_dwordx4 v[216:217], off
	v_lshl_add_u64 v[216:217], v[214:215], 0, s[56:57]
	s_mov_b32 m0, s26
	s_nop 0
	global_load_lds_dwordx4 v[216:217], off
	s_waitcnt vmcnt(8)
	s_waitcnt lgkmcnt(0)
	s_barrier
	s_waitcnt lgkmcnt(0)
	v_mfma_f32_16x16x32_bf16 v[130:133], v[136:139], v[168:171], v[130:133]
	v_mfma_f32_16x16x32_bf16 v[126:129], v[144:147], v[168:171], v[126:129]
	v_mfma_f32_16x16x32_bf16 v[112:115], v[136:139], v[176:179], v[112:115]
	v_mfma_f32_16x16x32_bf16 v[108:111], v[144:147], v[176:179], v[108:111]
	v_mfma_f32_16x16x32_bf16 v[96:99], v[136:139], v[184:187], v[96:99]
	v_mfma_f32_16x16x32_bf16 v[92:95], v[144:147], v[184:187], v[92:95]
	v_mfma_f32_16x16x32_bf16 v[80:83], v[136:139], v[202:205], v[80:83]
	v_mfma_f32_16x16x32_bf16 v[76:79], v[144:147], v[202:205], v[76:79]
	v_mfma_f32_16x16x32_bf16 v[130:133], v[140:143], v[172:175], v[130:133]
	v_mfma_f32_16x16x32_bf16 v[126:129], v[148:151], v[172:175], v[126:129]
	v_mfma_f32_16x16x32_bf16 v[112:115], v[140:143], v[180:183], v[112:115]
	v_mfma_f32_16x16x32_bf16 v[108:111], v[148:151], v[180:183], v[108:111]
	v_mfma_f32_16x16x32_bf16 v[96:99], v[140:143], v[188:191], v[96:99]
	v_mfma_f32_16x16x32_bf16 v[92:95], v[148:151], v[188:191], v[92:95]
	v_mfma_f32_16x16x32_bf16 v[80:83], v[140:143], v[206:209], v[80:83]
	v_mfma_f32_16x16x32_bf16 v[76:79], v[148:151], v[206:209], v[76:79]
	v_mfma_f32_16x16x32_bf16 v[122:125], v[152:155], v[168:171], v[122:125]
	v_mfma_f32_16x16x32_bf16 v[118:121], v[160:163], v[168:171], v[118:121]
	v_mfma_f32_16x16x32_bf16 v[104:107], v[152:155], v[176:179], v[104:107]
	v_mfma_f32_16x16x32_bf16 v[100:103], v[160:163], v[176:179], v[100:103]
	v_mfma_f32_16x16x32_bf16 v[88:91], v[152:155], v[184:187], v[88:91]
	v_mfma_f32_16x16x32_bf16 v[84:87], v[160:163], v[184:187], v[84:87]
	v_mfma_f32_16x16x32_bf16 v[72:75], v[152:155], v[202:205], v[72:75]
	v_mfma_f32_16x16x32_bf16 v[68:71], v[160:163], v[202:205], v[68:71]
	v_mfma_f32_16x16x32_bf16 v[122:125], v[156:159], v[172:175], v[122:125]
	v_mfma_f32_16x16x32_bf16 v[118:121], v[164:167], v[172:175], v[118:121]
	v_mfma_f32_16x16x32_bf16 v[104:107], v[156:159], v[180:183], v[104:107]
	v_mfma_f32_16x16x32_bf16 v[100:103], v[164:167], v[180:183], v[100:103]
	v_mfma_f32_16x16x32_bf16 v[88:91], v[156:159], v[188:191], v[88:91]
	v_mfma_f32_16x16x32_bf16 v[84:87], v[164:167], v[188:191], v[84:87]
	v_mfma_f32_16x16x32_bf16 v[72:75], v[156:159], v[206:209], v[72:75]
	v_mfma_f32_16x16x32_bf16 v[68:71], v[164:167], v[206:209], v[68:71]
	s_barrier
	s_mov_b32 m0, s39
	v_lshl_add_u64 v[216:217], v[192:193], 0, s[78:79]
	ds_read_b128 v[168:171], v221 offset:49152
	ds_read_b128 v[172:175], v221 offset:50176
	ds_read_b128 v[176:179], v221 offset:51200
	ds_read_b128 v[180:183], v221 offset:52224
	ds_read_b128 v[184:187], v221 offset:53248
	ds_read_b128 v[188:191], v221 offset:54272
	ds_read_b128 v[202:205], v221 offset:55296
	ds_read_b128 v[206:209], v221 offset:56320
	global_load_lds_dwordx4 v[216:217], off
	v_lshl_add_u64 v[216:217], v[192:193], 0, s[84:85]
	s_mov_b32 m0, s40
	s_nop 0
	global_load_lds_dwordx4 v[216:217], off
	v_lshl_add_u64 v[216:217], v[192:193], 0, s[50:51]
	s_mov_b32 m0, s41
	v_lshl_add_u64 v[192:193], v[192:193], 0, s[54:55]
	global_load_lds_dwordx4 v[216:217], off
	s_mov_b32 m0, s42
	s_nop 0
	global_load_lds_dwordx4 v[192:193], off
	v_lshl_add_u64 v[192:193], v[214:215], 0, s[78:79]
	s_mov_b32 m0, s27
	s_nop 0
	global_load_lds_dwordx4 v[192:193], off
	v_lshl_add_u64 v[192:193], v[214:215], 0, s[92:93]
	s_mov_b32 m0, s28
	s_nop 0
	global_load_lds_dwordx4 v[192:193], off
	s_waitcnt vmcnt(8)
	s_waitcnt lgkmcnt(0)
	s_barrier
	s_waitcnt lgkmcnt(0)
	v_mfma_f32_16x16x32_bf16 v[64:67], v[136:139], v[168:171], v[64:67]
	v_mfma_f32_16x16x32_bf16 v[60:63], v[144:147], v[168:171], v[60:63]
	v_mfma_f32_16x16x32_bf16 v[48:51], v[136:139], v[176:179], v[48:51]
	v_mfma_f32_16x16x32_bf16 v[44:47], v[144:147], v[176:179], v[44:47]
	v_mfma_f32_16x16x32_bf16 v[32:35], v[136:139], v[184:187], v[32:35]
	v_mfma_f32_16x16x32_bf16 v[28:31], v[144:147], v[184:187], v[28:31]
	v_mfma_f32_16x16x32_bf16 v[16:19], v[136:139], v[202:205], v[16:19]
	v_mfma_f32_16x16x32_bf16 v[12:15], v[144:147], v[202:205], v[12:15]
	v_mfma_f32_16x16x32_bf16 v[64:67], v[140:143], v[172:175], v[64:67]
	v_mfma_f32_16x16x32_bf16 v[60:63], v[148:151], v[172:175], v[60:63]
	v_mfma_f32_16x16x32_bf16 v[48:51], v[140:143], v[180:183], v[48:51]
	v_mfma_f32_16x16x32_bf16 v[44:47], v[148:151], v[180:183], v[44:47]
	v_mfma_f32_16x16x32_bf16 v[32:35], v[140:143], v[188:191], v[32:35]
	v_mfma_f32_16x16x32_bf16 v[28:31], v[148:151], v[188:191], v[28:31]
	v_mfma_f32_16x16x32_bf16 v[16:19], v[140:143], v[206:209], v[16:19]
	v_mfma_f32_16x16x32_bf16 v[12:15], v[148:151], v[206:209], v[12:15]
	v_mfma_f32_16x16x32_bf16 v[56:59], v[152:155], v[168:171], v[56:59]
	v_mfma_f32_16x16x32_bf16 v[52:55], v[160:163], v[168:171], v[52:55]
	v_mfma_f32_16x16x32_bf16 v[40:43], v[152:155], v[176:179], v[40:43]
	v_mfma_f32_16x16x32_bf16 v[36:39], v[160:163], v[176:179], v[36:39]
	v_mfma_f32_16x16x32_bf16 v[24:27], v[152:155], v[184:187], v[24:27]
	v_mfma_f32_16x16x32_bf16 v[20:23], v[160:163], v[184:187], v[20:23]
	v_mfma_f32_16x16x32_bf16 v[8:11], v[152:155], v[202:205], v[8:11]
	v_mfma_f32_16x16x32_bf16 v[4:7], v[160:163], v[202:205], v[4:7]
	v_mfma_f32_16x16x32_bf16 v[56:59], v[156:159], v[172:175], v[56:59]
	v_mfma_f32_16x16x32_bf16 v[52:55], v[164:167], v[172:175], v[52:55]
	v_mfma_f32_16x16x32_bf16 v[40:43], v[156:159], v[180:183], v[40:43]
	v_mfma_f32_16x16x32_bf16 v[36:39], v[164:167], v[180:183], v[36:39]
	v_mfma_f32_16x16x32_bf16 v[24:27], v[156:159], v[188:191], v[24:27]
	v_mfma_f32_16x16x32_bf16 v[20:23], v[164:167], v[188:191], v[20:23]
	v_mfma_f32_16x16x32_bf16 v[8:11], v[156:159], v[206:209], v[8:11]
	v_mfma_f32_16x16x32_bf16 v[4:7], v[164:167], v[206:209], v[4:7]
	s_barrier
	s_add_i32 s15, s15, 2
	s_add_u32 s20, s20, 0x100
	s_addc_u32 s21, s21, 0
	s_add_u32 s8, s8, 0x100
	s_addc_u32 s9, s9, 0
	s_cmp_gt_u32 s15, 29
	s_cbranch_scc0 .LBB0_594
	s_and_b64 vcc, exec, s[12:13]
	s_cbranch_vccz .LBB0_597
	s_barrier

;     __device__ bool next(int i, Unit& u) const { const int rounds = nwg / G; if (i >= rounds) return false; return StaticOrder::next(rounds - 1 - i, u); }
; #define PG8_WAIT_V(n) asm volatile("s_waitcnt vmcnt(" #n ")" ::: "memory")
; template <class Epi, class Sched, bool ALIGN_EPI = false, bool SP2 = false>
; __device__ __forceinline__ void gemm_phase(PG8_LAS unsigned char* lds, const Gemm g, const Sched& S, const Epi& E) {
;     ...
;     { int R, C; stage_rc(tid * 16, R, C); const int Rb = Epi::PERM ? ((R & ~31) + perm32(R & 31)) : R;
;         voffA = (unsigned)(R * g.lda + C) * 2u; voffB = (unsigned)(Rb * g.ldb + C) * 2u; }
;     const size_t voffA_step = (size_t)64 * g.lda * 2, voffB_step = (size_t)64 * g.ldb * 2;
;     const size_t kstep = (size_t)(BK * 2);
;     const size_t hstepA = (size_t)HALF * g.lda * 2, hstepB = (size_t)HALF * g.ldb * 2;
;     const size_t tstepA = 2 * hstepA, tstepB = 2 * hstepB;
;     const unsigned ldsw = (unsigned)wid * 1024u;
;     const int aoff = lds_byte(wr * 64 + fr, fq * 8), boff = lds_byte(wc * 32 + fr, fq * 8);
;     ...
;     Unit cur, nxt; int ui = 0;
;     if (!S.next(0, cur)) return;
;     f32x4 acc[2][2][4][2];
;     if constexpr (!SP2) {
; #pragma unroll
;     for (int a = 0; a < 2; ++a)
; #pragma unroll
;         for (int b = 0; b < 2; ++b)
; #pragma unroll
;             for (int m = 0; m < 4; ++m)
; #pragma unroll
;                 for (int n = 0; n < 2; ++n) acc[a][b][m][n] = (f32x4){0.f, 0.f, 0.f, 0.f};
;     }
;     bf16x8 At[4][2], B0[2][2], B1[2][2];
;     const char* cA = (const char*)S.opA(g, cur) + (size_t)cur.pm * tstepA; const char* cB = (const char*)S.opB(g, cur) + (size_t)cur.pn * tstepB;
;     S.a_ready(cur);
;     if constexpr (SP2) {
;         PG8_STAGE(PG8_SB(0, 0), cB, voffB); PG8_STAGE(PG8_SB(0, 1), cB + hstepB, voffB); PG8_STAGE(PG8_SA(0, 0), cA, voffA); PG8_STAGE(PG8_SA(0, 1), cA + hstepA, voffA);
;         if (wr == 1) PG8_BAR;
;         PG8_WAIT_V(2); PG8_BAR;
;         PG8_STAGE(PG8_SB(1, 0), cB + kstep, voffB); PG8_STAGE(PG8_SA(1, 0), cA + kstep, voffA); PG8_STAGE(PG8_SB(1, 1), cB + hstepB + kstep, voffB);
;         if (Epi::NST > 0) PG8_WAIT_V(0); else PG8_WAIT_V(6);
;         PG8_BAR;
;     } else {
;         PG8_STAGE(PG8_SB(0, 0), cB, voffB); PG8_STAGE(PG8_SA(0, 0), cA, voffA); PG8_STAGE(PG8_SB(0, 1), cB + hstepB, voffB); PG8_STAGE(PG8_SA(0, 1), cA + hstepA, voffA);
;         if (wr == 1) PG8_BAR;
.LBB0_685:
	s_or_b64 exec, exec, s[6:7]
	v_readlane_b32 s2, v254, 51
	v_mov_b32_e32 v12, v212
	v_readlane_b32 s3, v254, 52
	s_waitcnt lgkmcnt(0)
	s_barrier
	s_andn2_b64 vcc, exec, s[2:3]
	v_readfirstlane_b32 s0, v12
	s_cbranch_vccnz .LBB0_723
	v_bfe_i32 v4, v12, 27, 1
	v_lshlrev_b32_e32 v3, 4, v12
	v_lshrrev_b32_e32 v4, 22, v4
	v_add_u32_e32 v4, v3, v4
	v_and_b32_e32 v4, 0xfffffc00, v4
	v_sub_u32_e32 v3, v3, v4
	v_lshrrev_b32_e32 v4, 4, v3
	v_ashrrev_i32_e32 v5, 31, v12
	v_bitop3_b32 v3, v4, v3, 32 bitop3:0x6c
	v_lshrrev_b32_e32 v5, 26, v5
	v_ashrrev_i32_e32 v4, 31, v3
	v_add_u32_e32 v5, v12, v5
	v_lshrrev_b32_e32 v4, 26, v4
	v_ashrrev_i32_e32 v9, 6, v5
	v_add_u32_e32 v4, v3, v4
	v_lshlrev_b32_e32 v5, 3, v9
	v_ashrrev_i32_e32 v8, 6, v4
	v_and_b32_e32 v5, -16, v5
	v_add_u32_e32 v5, v8, v5
	v_and_b32_e32 v6, 3, v8
	s_mov_b32 s3, 0xfffe0
	v_lshrrev_b32_e32 v7, 2, v5
	v_lshlrev_b32_e32 v10, 1, v5
	v_and_b32_e32 v4, 0xc0, v4
	v_and_or_b32 v6, v5, s3, v6
	v_and_b32_e32 v7, 4, v7
	v_and_b32_e32 v10, 24, v10
	v_sub_u32_e32 v3, v3, v4
	v_mov_b32_e32 v4, 1
	v_or3_b32 v6, v6, v7, v10
	v_lshlrev_b32_e32 v7, 5, v9
	v_ashrrev_i16_sdwa v3, v4, sext(v3) dst_sel:DWORD dst_unused:UNUSED_PAD src0_sel:DWORD src1_sel:BYTE_0
	s_ashr_i32 s2, s0, 6
	v_and_b32_e32 v10, 32, v7
	v_bfe_i32 v11, v3, 0, 16
	s_lshl_b32 s28, s2, 10
	v_add_u32_e32 v3, v10, v11
	v_lshlrev_b32_e32 v4, 1, v3
	s_movk_i32 s3, 0x840
	v_readlane_b32 s4, v254, 42
	s_add_i32 s29, s28, 0
	v_lshl_add_u32 v160, v6, 12, v4
	v_mul_lo_u32 v4, v5, s3
	v_mov_b32_e32 v161, v2
	v_readlane_b32 s5, v254, 43
	s_add_i32 m0, s29, 0x10000
	v_add_lshl_u32 v162, v3, v4, 1
	v_lshl_add_u64 v[4:5], s[4:5], 0, v[160:161]
	v_lshl_add_u64 v[6:7], v[4:5], 0, s[90:91]
	v_mov_b32_e32 v163, v2
	global_load_lds_dwordx4 v160, s[4:5]
	v_readlane_b32 s4, v254, 35
	s_add_i32 m0, s29, 0x12000
	v_readlane_b32 s5, v254, 36
	global_load_lds_dwordx4 v[6:7], off
	s_nop 0
	v_lshl_add_u64 v[6:7], s[4:5], 0, v[160:161]
	s_add_i32 m0, s29, 0x14000
	v_lshl_add_u64 v[6:7], v[6:7], 0, s[90:91]
	global_load_lds_dwordx4 v160, s[4:5]
	s_add_i32 m0, s29, 0x16000
	v_readlane_b32 s4, v254, 38
	global_load_lds_dwordx4 v[6:7], off
	v_readlane_b32 s5, v254, 39
	s_mov_b32 m0, s29
	s_add_i32 s30, s29, 0x2000
	v_lshl_add_u64 v[6:7], s[4:5], 0, v[162:163]
	v_lshl_add_u64 v[14:15], v[6:7], 0, s[96:97]
	s_add_i32 s31, s29, 0x4000
	global_load_lds_dwordx4 v162, s[4:5]
	v_readlane_b32 s4, v254, 40
	s_mov_b32 m0, s30
	v_readlane_b32 s5, v254, 41
	global_load_lds_dwordx4 v[14:15], off
	s_nop 0
	v_lshl_add_u64 v[14:15], s[4:5], 0, v[162:163]
	s_mov_b32 m0, s31
	s_add_i32 s34, s29, 0x6000
	global_load_lds_dwordx4 v162, s[4:5]
	v_lshl_add_u64 v[14:15], v[14:15], 0, s[96:97]
	s_mov_b32 m0, s34
	s_ashr_i32 s3, s0, 8
	s_cmp_eq_u32 s3, 0
	s_cbranch_scc0 .Lsp_out
	s_setprio 1
.Lsp_out:
	global_load_lds_dwordx4 v[14:15], off
	s_cmp_eq_u32 s3, 1
	s_cselect_b64 s[12:13], -1, 0
	s_cmp_lg_u32 s3, 1
	s_cbranch_scc1 .LBB0_688
	s_barrier

;     __device__ bool next(int i, Unit& u) const { const int rounds = nwg / G; if (i >= rounds) return false; return StaticOrder::next(rounds - 1 - i, u); }
;     __device__ bool next(int i, Unit& u) const { const int rounds = nwg / G; if (i >= 2 * rounds) return false; const bool ok = StaticOrder::next(i >= rounds ? i - rounds : i, u); u.z = (i >= rounds) ? 1 : 0; return ok; }
; #define PG8_TRIP_HEAD(T) const int t = (T); const bool last = (t == nt - 2); \
;             const char* a1 = cA + (size_t)(t + 1) * kstep; \
;             const char* a2 = last ? nA : cA + (size_t)(t + 2) * kstep; const char* b2 = last ? nB : cB + (size_t)(t + 2) * kstep; \
;             const char* a3 = a2 + kstep; const char* b3 = b2 + kstep; \
;             if (last && has_next) S.a_ready(nxt);
; template <class Epi, class Sched, bool ALIGN_EPI = false, bool SP2 = false>
; __device__ __forceinline__ void gemm_phase(PG8_LAS unsigned char* lds, const Gemm g, const Sched& S, const Epi& E) {
;     ...
;         const bool has_next = S.next(ui + 1, nxt);
;         const char* nA = has_next ? (const char*)S.opA(g, nxt) + (size_t)nxt.pm * tstepA : cA; const char* nB = has_next ? (const char*)S.opB(g, nxt) + (size_t)nxt.pn * tstepB : cB;
;     ...
;         if constexpr (SP2) {
;             { PG8_TRIP_HEAD(0) PG8_TRIP_SP2(asm volatile("s_waitcnt vmcnt(%0)" :: "n"(8 + Epi::NST) : "memory"), PG8_MMAZ) }
.LBB0_699:
	s_ashr_i32 s19, s18, 31
	s_lshl_b64 s[4:5], s[18:19], 20
	v_readlane_b32 s22, v254, 33
	v_readlane_b32 s23, v254, 34
	s_add_u32 s22, s22, s4
	s_addc_u32 s23, s23, s5
	s_add_i32 s33, 0, 0x10000
	s_add_i32 s41, 0, 0x14000
	v_add_u32_e32 v116, s33, v176
	v_add_u32_e32 v117, s41, v176
	ds_read_b128 v[4:7], v116
	ds_read_b128 v[8:11], v116 offset:1024
	ds_read_b128 v[12:15], v116 offset:2048
	ds_read_b128 v[16:19], v116 offset:3072
	ds_read_b128 v[20:23], v117
	ds_read_b128 v[24:27], v117 offset:1024
	ds_read_b128 v[28:31], v117 offset:2048
	ds_read_b128 v[32:35], v117 offset:3072
	s_and_b64 s[4:5], s[10:11], exec
	s_cselect_b32 s3, s23, s25
	s_cselect_b32 s4, s22, s24
	v_lshl_add_u64 v[208:209], s[26:27], 0, v[162:163]
	s_mov_b64 s[10:11], 0x84080
	s_add_i32 s5, s29, 0xc000
	s_waitcnt vmcnt(0)
	v_lshl_add_u64 v[68:69], v[208:209], 0, s[10:11]
	s_mov_b32 m0, s5
	s_mov_b64 s[10:11], 0xc6080
	s_add_i32 s19, s29, 0xe000
	ds_read_b128 v[36:39], v178
	ds_read_b128 v[40:43], v178 offset:1024
	ds_read_b128 v[44:47], v178 offset:2048
	ds_read_b128 v[48:51], v178 offset:3072
	ds_read_b128 v[52:55], v178 offset:4096
	ds_read_b128 v[56:59], v178 offset:5120
	ds_read_b128 v[60:63], v178 offset:6144
	ds_read_b128 v[64:67], v178 offset:7168
	global_load_lds_dwordx4 v[68:69], off
	v_lshl_add_u64 v[68:69], v[208:209], 0, s[10:11]
	s_mov_b32 m0, s19
	s_nop 0
	global_load_lds_dwordx4 v[68:69], off
	s_waitcnt vmcnt(16)
	s_waitcnt lgkmcnt(0)
	s_barrier
	s_waitcnt lgkmcnt(0)
	v_mfma_f32_16x16x32_bf16 v[92:95], v[4:7], v[60:63], 0
	v_mfma_f32_16x16x32_bf16 v[68:71], v[4:7], v[36:39], 0
	v_mfma_f32_16x16x32_bf16 v[72:75], v[12:15], v[36:39], 0
	v_mfma_f32_16x16x32_bf16 v[76:79], v[4:7], v[44:47], 0
	v_mfma_f32_16x16x32_bf16 v[80:83], v[12:15], v[44:47], 0
	v_mfma_f32_16x16x32_bf16 v[84:87], v[4:7], v[52:55], 0
	v_mfma_f32_16x16x32_bf16 v[88:91], v[12:15], v[52:55], 0
	v_mfma_f32_16x16x32_bf16 v[100:103], v[8:11], v[64:67], v[92:95]
	v_mfma_f32_16x16x32_bf16 v[92:95], v[12:15], v[60:63], 0
	v_mfma_f32_16x16x32_bf16 v[68:71], v[8:11], v[40:43], v[68:71]
	v_mfma_f32_16x16x32_bf16 v[72:75], v[16:19], v[40:43], v[72:75]
	v_mfma_f32_16x16x32_bf16 v[76:79], v[8:11], v[48:51], v[76:79]
	v_mfma_f32_16x16x32_bf16 v[80:83], v[16:19], v[48:51], v[80:83]
	v_mfma_f32_16x16x32_bf16 v[84:87], v[8:11], v[56:59], v[84:87]
	v_mfma_f32_16x16x32_bf16 v[88:91], v[16:19], v[56:59], v[88:91]
	v_mfma_f32_16x16x32_bf16 v[104:107], v[16:19], v[64:67], v[92:95]
	v_mfma_f32_16x16x32_bf16 v[92:95], v[20:23], v[36:39], 0
	v_mfma_f32_16x16x32_bf16 v[36:39], v[28:31], v[36:39], 0
	v_mfma_f32_16x16x32_bf16 v[120:123], v[24:27], v[40:43], v[92:95]
	v_mfma_f32_16x16x32_bf16 v[36:39], v[32:35], v[40:43], v[36:39]
	v_mfma_f32_16x16x32_bf16 v[40:43], v[20:23], v[44:47], 0
	v_mfma_f32_16x16x32_bf16 v[44:47], v[28:31], v[44:47], 0
	v_mfma_f32_16x16x32_bf16 v[40:43], v[24:27], v[48:51], v[40:43]
	v_mfma_f32_16x16x32_bf16 v[44:47], v[32:35], v[48:51], v[44:47]
	v_mfma_f32_16x16x32_bf16 v[48:51], v[20:23], v[52:55], 0
	v_mfma_f32_16x16x32_bf16 v[52:55], v[28:31], v[52:55], 0
	v_mfma_f32_16x16x32_bf16 v[48:51], v[24:27], v[56:59], v[48:51]
	v_mfma_f32_16x16x32_bf16 v[52:55], v[32:35], v[56:59], v[52:55]
	v_mfma_f32_16x16x32_bf16 v[56:59], v[20:23], v[60:63], 0
	v_mfma_f32_16x16x32_bf16 v[60:63], v[28:31], v[60:63], 0
	v_mfma_f32_16x16x32_bf16 v[56:59], v[24:27], v[64:67], v[56:59]
	v_mfma_f32_16x16x32_bf16 v[60:63], v[32:35], v[64:67], v[60:63]
	s_barrier
	v_lshl_add_u64 v[250:251], s[24:25], 0, v[160:161]
	s_mov_b64 s[10:11], 0x100
	s_add_i32 s33, s33, s28
	v_lshl_add_u64 v[118:119], v[250:251], 0, s[10:11]
	s_mov_b32 m0, s33
	s_mov_b64 s[42:43], 0x40100
	s_add_i32 s40, s33, 0x2000
	ds_read_b128 v[64:67], v178 offset:16384
	ds_read_b128 v[92:95], v178 offset:17408
	ds_read_b128 v[96:99], v178 offset:18432
	ds_read_b128 v[108:111], v178 offset:19456
	ds_read_b128 v[112:115], v178 offset:20480
	ds_read_b128 v[124:127], v178 offset:21504
	ds_read_b128 v[128:131], v178 offset:22528
	ds_read_b128 v[132:135], v178 offset:23552
	global_load_lds_dwordx4 v[118:119], off
	v_lshl_add_u64 v[118:119], v[250:251], 0, s[42:43]
	s_mov_b32 m0, s40
	s_mov_b64 s[42:43], 0x80100
	s_add_i32 s41, s41, s28
	global_load_lds_dwordx4 v[118:119], off
	v_lshl_add_u64 v[118:119], v[250:251], 0, s[42:43]
	s_mov_b32 m0, s41
	s_mov_b64 s[42:43], 0xc0100
	global_load_lds_dwordx4 v[118:119], off
	v_lshl_add_u64 v[118:119], v[250:251], 0, s[42:43]
	s_add_i32 s42, s41, 0x2000
	s_mov_b32 m0, s42
	s_nop 0
	global_load_lds_dwordx4 v[118:119], off
	v_lshl_add_u64 v[118:119], v[208:209], 0, s[10:11]
	s_mov_b32 m0, s29
	s_mov_b64 s[10:11], 0x42100
	global_load_lds_dwordx4 v[118:119], off
	v_lshl_add_u64 v[118:119], v[208:209], 0, s[10:11]
	s_mov_b32 m0, s30
	s_nop 0
	global_load_lds_dwordx4 v[118:119], off
	s_waitcnt vmcnt(16)
	s_waitcnt lgkmcnt(0)
	s_barrier
; #define PG8_TRIP_HEAD(T) const int t = (T); const bool last = (t == nt - 2); \
;             const char* a1 = cA + (size_t)(t + 1) * kstep; \
;             const char* a2 = last ? nA : cA + (size_t)(t + 2) * kstep; const char* b2 = last ? nB : cB + (size_t)(t + 2) * kstep; \
;             const char* a3 = a2 + kstep; const char* b3 = b2 + kstep; \
;             if (last && has_next) S.a_ready(nxt);
; template <class Epi, class Sched, bool ALIGN_EPI = false, bool SP2 = false>
; __device__ __forceinline__ void gemm_phase(PG8_LAS unsigned char* lds, const Gemm g, const Sched& S, const Epi& E) {
;     ...
;         if constexpr (SP2) {
;             { PG8_TRIP_HEAD(0) PG8_TRIP_SP2(asm volatile("s_waitcnt vmcnt(%0)" :: "n"(8 + Epi::NST) : "memory"), PG8_MMAZ) }
	s_waitcnt lgkmcnt(0)
	v_mfma_f32_16x16x32_bf16 v[136:139], v[4:7], v[64:67], 0
	v_mfma_f32_16x16x32_bf16 v[144:147], v[8:11], v[92:95], v[136:139]
	v_mfma_f32_16x16x32_bf16 v[136:139], v[12:15], v[64:67], 0
	v_mfma_f32_16x16x32_bf16 v[148:151], v[16:19], v[92:95], v[136:139]
	v_mfma_f32_16x16x32_bf16 v[136:139], v[4:7], v[96:99], 0
	v_mfma_f32_16x16x32_bf16 v[152:155], v[8:11], v[108:111], v[136:139]
	v_mfma_f32_16x16x32_bf16 v[136:139], v[12:15], v[96:99], 0
	v_mfma_f32_16x16x32_bf16 v[156:159], v[16:19], v[108:111], v[136:139]
	v_mfma_f32_16x16x32_bf16 v[136:139], v[4:7], v[112:115], 0
	v_mfma_f32_16x16x32_bf16 v[4:7], v[4:7], v[128:131], 0
	v_mfma_f32_16x16x32_bf16 v[166:169], v[8:11], v[124:127], v[136:139]
	v_mfma_f32_16x16x32_bf16 v[4:7], v[8:11], v[132:135], v[4:7]
	v_mfma_f32_16x16x32_bf16 v[8:11], v[12:15], v[128:131], 0
	v_mfma_f32_16x16x32_bf16 v[136:139], v[12:15], v[112:115], 0
	v_mfma_f32_16x16x32_bf16 v[8:11], v[16:19], v[132:135], v[8:11]
	v_mfma_f32_16x16x32_bf16 v[170:173], v[16:19], v[124:127], v[136:139]
	v_mfma_f32_16x16x32_bf16 v[12:15], v[20:23], v[64:67], 0
	v_mfma_f32_16x16x32_bf16 v[180:183], v[24:27], v[92:95], v[12:15]
	v_mfma_f32_16x16x32_bf16 v[12:15], v[28:31], v[64:67], 0
	v_mfma_f32_16x16x32_bf16 v[184:187], v[32:35], v[92:95], v[12:15]
	v_mfma_f32_16x16x32_bf16 v[12:15], v[20:23], v[96:99], 0
	v_mfma_f32_16x16x32_bf16 v[188:191], v[24:27], v[108:111], v[12:15]
	v_mfma_f32_16x16x32_bf16 v[12:15], v[28:31], v[96:99], 0
	v_mfma_f32_16x16x32_bf16 v[192:195], v[32:35], v[108:111], v[12:15]
	v_mfma_f32_16x16x32_bf16 v[12:15], v[20:23], v[112:115], 0
	v_mfma_f32_16x16x32_bf16 v[196:199], v[24:27], v[124:127], v[12:15]
	v_mfma_f32_16x16x32_bf16 v[12:15], v[28:31], v[112:115], 0
	v_mfma_f32_16x16x32_bf16 v[200:203], v[32:35], v[124:127], v[12:15]
	v_mfma_f32_16x16x32_bf16 v[12:15], v[20:23], v[128:131], 0
	v_mfma_f32_16x16x32_bf16 v[204:207], v[24:27], v[132:135], v[12:15]
	v_mfma_f32_16x16x32_bf16 v[12:15], v[28:31], v[128:131], 0
	v_mfma_f32_16x16x32_bf16 v[132:135], v[32:35], v[132:135], v[12:15]
	s_barrier
	s_add_i32 s43, 0, 0x18000
	s_add_i32 s45, 0, 0x1c000
	v_add_u32_e32 v118, s43, v176
	v_add_u32_e32 v119, s45, v176
	s_nop 0
	ds_read_b128 v[12:15], v118
	ds_read_b128 v[16:19], v118 offset:1024
	ds_read_b128 v[20:23], v118 offset:2048
	ds_read_b128 v[24:27], v118 offset:3072
	ds_read_b128 v[214:217], v119
	ds_read_b128 v[218:221], v119 offset:1024
	ds_read_b128 v[222:225], v119 offset:2048
	ds_read_b128 v[226:229], v119 offset:3072
	s_mov_b64 s[10:11], 0x84100
	s_mov_b32 m0, s31
	v_lshl_add_u64 v[92:93], v[208:209], 0, s[10:11]
	s_mov_b64 s[10:11], 0xc6100
	ds_read_b128 v[28:31], v178 offset:32768
	ds_read_b128 v[32:35], v178 offset:33792
	ds_read_b128 v[64:67], v178 offset:34816
	ds_read_b128 v[230:233], v178 offset:35840
	ds_read_b128 v[234:237], v178 offset:36864
	ds_read_b128 v[238:241], v178 offset:37888
	ds_read_b128 v[242:245], v178 offset:38912
	ds_read_b128 v[246:249], v178 offset:39936
	global_load_lds_dwordx4 v[92:93], off
	v_lshl_add_u64 v[92:93], v[208:209], 0, s[10:11]
	s_mov_b32 m0, s34
	s_nop 0
	global_load_lds_dwordx4 v[92:93], off
	s_waitcnt vmcnt(8)
	s_waitcnt lgkmcnt(0)
	s_barrier
	s_waitcnt lgkmcnt(0)
	v_mfma_f32_16x16x32_bf16 v[68:71], v[12:15], v[28:31], v[68:71]
	v_mfma_f32_16x16x32_bf16 v[140:143], v[16:19], v[32:35], v[68:71]
	v_mfma_f32_16x16x32_bf16 v[68:71], v[20:23], v[28:31], v[72:75]
	v_mfma_f32_16x16x32_bf16 v[136:139], v[24:27], v[32:35], v[68:71]
	v_mfma_f32_16x16x32_bf16 v[68:71], v[12:15], v[64:67], v[76:79]
	v_mfma_f32_16x16x32_bf16 v[112:115], v[16:19], v[230:233], v[68:71]
	v_mfma_f32_16x16x32_bf16 v[68:71], v[20:23], v[64:67], v[80:83]
	v_mfma_f32_16x16x32_bf16 v[108:111], v[24:27], v[230:233], v[68:71]
	v_mfma_f32_16x16x32_bf16 v[68:71], v[12:15], v[234:237], v[84:87]
	v_mfma_f32_16x16x32_bf16 v[96:99], v[16:19], v[238:241], v[68:71]
	v_mfma_f32_16x16x32_bf16 v[68:71], v[20:23], v[234:237], v[88:91]
	v_mfma_f32_16x16x32_bf16 v[92:95], v[24:27], v[238:241], v[68:71]
	v_mfma_f32_16x16x32_bf16 v[68:71], v[12:15], v[242:245], v[100:103]
	v_mfma_f32_16x16x32_bf16 v[80:83], v[16:19], v[246:249], v[68:71]
	v_mfma_f32_16x16x32_bf16 v[68:71], v[20:23], v[242:245], v[104:107]
	v_mfma_f32_16x16x32_bf16 v[76:79], v[24:27], v[246:249], v[68:71]
	v_mfma_f32_16x16x32_bf16 v[68:71], v[214:217], v[28:31], v[120:123]
	v_mfma_f32_16x16x32_bf16 v[28:31], v[222:225], v[28:31], v[36:39]
	v_mfma_f32_16x16x32_bf16 v[124:127], v[226:229], v[32:35], v[28:31]
	v_mfma_f32_16x16x32_bf16 v[28:31], v[214:217], v[64:67], v[40:43]
	v_mfma_f32_16x16x32_bf16 v[104:107], v[218:221], v[230:233], v[28:31]
	v_mfma_f32_16x16x32_bf16 v[28:31], v[222:225], v[64:67], v[44:47]
	v_mfma_f32_16x16x32_bf16 v[100:103], v[226:229], v[230:233], v[28:31]
	v_mfma_f32_16x16x32_bf16 v[28:31], v[214:217], v[234:237], v[48:51]
	v_mfma_f32_16x16x32_bf16 v[88:91], v[218:221], v[238:241], v[28:31]
	v_mfma_f32_16x16x32_bf16 v[28:31], v[222:225], v[234:237], v[52:55]
	v_mfma_f32_16x16x32_bf16 v[84:87], v[226:229], v[238:241], v[28:31]
	v_mfma_f32_16x16x32_bf16 v[28:31], v[214:217], v[242:245], v[56:59]
	v_mfma_f32_16x16x32_bf16 v[72:75], v[218:221], v[246:249], v[28:31]
	v_mfma_f32_16x16x32_bf16 v[28:31], v[222:225], v[242:245], v[60:63]
	v_mfma_f32_16x16x32_bf16 v[128:131], v[218:221], v[32:35], v[68:71]
	v_mfma_f32_16x16x32_bf16 v[68:71], v[226:229], v[246:249], v[28:31]
	s_barrier
; #define PG8_MMA(ai, bj, At, Bt) do { __builtin_amdgcn_s_setprio(1); _Pragma("unroll") for (int m = 0; m < 4; ++m) _Pragma("unroll") for (int n = 0; n < 2; ++n) _Pragma("unroll") for (int k = 0; k < 2; ++k) \
;         acc[ai][bj][m][n] = __builtin_amdgcn_mfma_f32_16x16x32_bf16(Bt[n][k], At[m][k], acc[ai][bj][m][n], 0, 0, 0); __builtin_amdgcn_s_setprio(0); } while (0)
; #define PG8_WAIT_V(n) asm volatile("s_waitcnt vmcnt(" #n ")" ::: "memory")
; #define PG8_TRIP_HEAD(T) const int t = (T); const bool last = (t == nt - 2); \
;             const char* a1 = cA + (size_t)(t + 1) * kstep; \
;             const char* a2 = last ? nA : cA + (size_t)(t + 2) * kstep; const char* b2 = last ? nB : cB + (size_t)(t + 2) * kstep; \
;             const char* a3 = a2 + kstep; const char* b3 = b2 + kstep; \
;             if (last && has_next) S.a_ready(nxt);
; template <class Epi, class Sched, bool ALIGN_EPI = false, bool SP2 = false>
; __device__ __forceinline__ void gemm_phase(PG8_LAS unsigned char* lds, const Gemm g, const Sched& S, const Epi& E) {
;     ...
;         if constexpr (SP2) {
;             { PG8_TRIP_HEAD(0) PG8_TRIP_SP2(asm volatile("s_waitcnt vmcnt(%0)" :: "n"(8 + Epi::NST) : "memory"), PG8_MMAZ) }
;             for (int tt = 2; tt < nt; tt += 2) { PG8_TRIP_HEAD(tt) PG8_TRIP_SP2(PG8_WAIT_V(8), PG8_MMA) }
	s_mov_b64 s[10:11], 0x180
	s_add_i32 s43, s43, s28
	s_nop 1
	v_lshl_add_u64 v[28:29], v[250:251], 0, s[10:11]
	s_mov_b32 m0, s43
	s_mov_b64 s[46:47], 0x40180
	s_add_i32 s44, s43, 0x2000
	ds_read_b128 v[36:39], v178 offset:49152
	ds_read_b128 v[40:43], v178 offset:50176
	ds_read_b128 v[120:123], v178 offset:51200
	ds_read_b128 v[230:233], v178 offset:52224
	ds_read_b128 v[234:237], v178 offset:53248
	ds_read_b128 v[238:241], v178 offset:54272
	ds_read_b128 v[242:245], v178 offset:55296
	ds_read_b128 v[246:249], v178 offset:56320
	global_load_lds_dwordx4 v[28:29], off
	v_lshl_add_u64 v[28:29], v[250:251], 0, s[46:47]
	s_mov_b32 m0, s44
	s_mov_b64 s[46:47], 0x80180
	s_add_i32 s45, s45, s28
	global_load_lds_dwordx4 v[28:29], off
	v_lshl_add_u64 v[28:29], v[250:251], 0, s[46:47]
	s_mov_b32 m0, s45
	s_mov_b64 s[46:47], 0xc0180
	global_load_lds_dwordx4 v[28:29], off
	v_lshl_add_u64 v[28:29], v[250:251], 0, s[46:47]
	s_add_i32 s46, s45, 0x2000
	s_mov_b32 m0, s46
	s_nop 0
	global_load_lds_dwordx4 v[28:29], off
	v_lshl_add_u64 v[28:29], v[208:209], 0, s[10:11]
	s_mov_b32 m0, s36
	s_mov_b64 s[10:11], 0x42180
	global_load_lds_dwordx4 v[28:29], off
	v_lshl_add_u64 v[28:29], v[208:209], 0, s[10:11]
	s_mov_b32 m0, s37
	s_nop 0
	global_load_lds_dwordx4 v[28:29], off
	s_waitcnt vmcnt(8)
	s_waitcnt lgkmcnt(0)
	s_barrier
	s_waitcnt lgkmcnt(0)
	v_mfma_f32_16x16x32_bf16 v[28:31], v[12:15], v[36:39], v[144:147]
	v_mfma_f32_16x16x32_bf16 v[56:59], v[16:19], v[40:43], v[28:31]
	v_mfma_f32_16x16x32_bf16 v[28:31], v[20:23], v[36:39], v[148:151]
	v_mfma_f32_16x16x32_bf16 v[52:55], v[24:27], v[40:43], v[28:31]
	v_mfma_f32_16x16x32_bf16 v[28:31], v[12:15], v[120:123], v[152:155]
	v_mfma_f32_16x16x32_bf16 v[48:51], v[16:19], v[230:233], v[28:31]
	v_mfma_f32_16x16x32_bf16 v[28:31], v[20:23], v[120:123], v[156:159]
	v_mfma_f32_16x16x32_bf16 v[44:47], v[24:27], v[230:233], v[28:31]
	v_mfma_f32_16x16x32_bf16 v[28:31], v[12:15], v[234:237], v[166:169]
	v_mfma_f32_16x16x32_bf16 v[4:7], v[12:15], v[242:245], v[4:7]
	v_mfma_f32_16x16x32_bf16 v[32:35], v[16:19], v[238:241], v[28:31]
	v_mfma_f32_16x16x32_bf16 v[28:31], v[20:23], v[234:237], v[170:173]
	v_mfma_f32_16x16x32_bf16 v[16:19], v[16:19], v[246:249], v[4:7]
	v_mfma_f32_16x16x32_bf16 v[4:7], v[20:23], v[242:245], v[8:11]
	v_mfma_f32_16x16x32_bf16 v[28:31], v[24:27], v[238:241], v[28:31]
	v_mfma_f32_16x16x32_bf16 v[12:15], v[24:27], v[246:249], v[4:7]
	v_mfma_f32_16x16x32_bf16 v[4:7], v[214:217], v[36:39], v[180:183]
	v_mfma_f32_16x16x32_bf16 v[64:67], v[218:221], v[40:43], v[4:7]
	v_mfma_f32_16x16x32_bf16 v[4:7], v[222:225], v[36:39], v[184:187]
	v_mfma_f32_16x16x32_bf16 v[60:63], v[226:229], v[40:43], v[4:7]
	v_mfma_f32_16x16x32_bf16 v[4:7], v[214:217], v[120:123], v[188:191]
	v_mfma_f32_16x16x32_bf16 v[40:43], v[218:221], v[230:233], v[4:7]
	v_mfma_f32_16x16x32_bf16 v[4:7], v[222:225], v[120:123], v[192:195]
	v_mfma_f32_16x16x32_bf16 v[36:39], v[226:229], v[230:233], v[4:7]
	v_mfma_f32_16x16x32_bf16 v[4:7], v[214:217], v[234:237], v[196:199]
	v_mfma_f32_16x16x32_bf16 v[24:27], v[218:221], v[238:241], v[4:7]
	v_mfma_f32_16x16x32_bf16 v[4:7], v[222:225], v[234:237], v[200:203]
	v_mfma_f32_16x16x32_bf16 v[20:23], v[226:229], v[238:241], v[4:7]
	v_mfma_f32_16x16x32_bf16 v[4:7], v[214:217], v[242:245], v[204:207]
	v_mfma_f32_16x16x32_bf16 v[8:11], v[218:221], v[246:249], v[4:7]
	v_mfma_f32_16x16x32_bf16 v[4:7], v[222:225], v[242:245], v[132:135]
	v_mfma_f32_16x16x32_bf16 v[4:7], v[226:229], v[246:249], v[4:7]
	s_barrier
	s_add_u32 s10, s26, 0x84180
	s_addc_u32 s11, s27, 0
	s_add_u32 s24, s24, 0x200
	s_addc_u32 s25, s25, 0
	s_mov_b32 s26, 0
	s_mov_b64 s[52:53], 0x80000
	s_mov_b64 s[54:55], 0x80080
	s_mov_b64 s[56:57], 0xc0000
	s_mov_b64 s[60:61], 0xc0080
	s_mov_b64 s[62:63], 0xc6000
.LBB0_700:
	ds_read_b128 v[120:123], v116
	ds_read_b128 v[132:135], v116 offset:1024
	ds_read_b128 v[144:147], v116 offset:2048
	ds_read_b128 v[148:151], v116 offset:3072
	ds_read_b128 v[152:155], v117
	ds_read_b128 v[156:159], v117 offset:1024
	ds_read_b128 v[166:169], v117 offset:2048
	ds_read_b128 v[170:173], v117 offset:3072
	s_add_u32 s27, s10, 0xfff7c080
	s_addc_u32 s47, s11, -1
	s_cmp_eq_u32 s26, 28
	s_cselect_b32 s49, s21, s47
	s_cselect_b32 s48, s20, s27
	s_cselect_b32 s51, s3, s25
	s_cselect_b32 s50, s4, s24
	s_mov_b32 m0, s5
	v_lshl_add_u64 v[208:209], s[10:11], 0, v[164:165]
	ds_read_b128 v[180:183], v178
	ds_read_b128 v[184:187], v178 offset:1024
	ds_read_b128 v[188:191], v178 offset:2048
	ds_read_b128 v[192:195], v178 offset:3072
	ds_read_b128 v[196:199], v178 offset:4096
	ds_read_b128 v[200:203], v178 offset:5120
	ds_read_b128 v[204:207], v178 offset:6144
	ds_read_b128 v[214:217], v178 offset:7168
	global_load_lds_dwordx4 v[208:209], off
	v_lshl_add_u64 v[208:209], v[208:209], 0, s[96:97]
	s_mov_b32 m0, s19
	s_nop 0
	global_load_lds_dwordx4 v[208:209], off
	s_waitcnt vmcnt(8)
	s_waitcnt lgkmcnt(0)
	s_barrier
; #define PG8_MMA(ai, bj, At, Bt) do { __builtin_amdgcn_s_setprio(1); _Pragma("unroll") for (int m = 0; m < 4; ++m) _Pragma("unroll") for (int n = 0; n < 2; ++n) _Pragma("unroll") for (int k = 0; k < 2; ++k) \
;         acc[ai][bj][m][n] = __builtin_amdgcn_mfma_f32_16x16x32_bf16(Bt[n][k], At[m][k], acc[ai][bj][m][n], 0, 0, 0); __builtin_amdgcn_s_setprio(0); } while (0)
; #define PG8_WAIT_V(n) asm volatile("s_waitcnt vmcnt(" #n ")" ::: "memory")
; #define PG8_TRIP_HEAD(T) const int t = (T); const bool last = (t == nt - 2); \
;             const char* a1 = cA + (size_t)(t + 1) * kstep; \
;             const char* a2 = last ? nA : cA + (size_t)(t + 2) * kstep; const char* b2 = last ? nB : cB + (size_t)(t + 2) * kstep; \
;             const char* a3 = a2 + kstep; const char* b3 = b2 + kstep; \
;             if (last && has_next) S.a_ready(nxt);
; template <class Epi, class Sched, bool ALIGN_EPI = false, bool SP2 = false>
; __device__ __forceinline__ void gemm_phase(PG8_LAS unsigned char* lds, const Gemm g, const Sched& S, const Epi& E) {
;     ...
;         if constexpr (SP2) {
;             { PG8_TRIP_HEAD(0) PG8_TRIP_SP2(asm volatile("s_waitcnt vmcnt(%0)" :: "n"(8 + Epi::NST) : "memory"), PG8_MMAZ) }
;             for (int tt = 2; tt < nt; tt += 2) { PG8_TRIP_HEAD(tt) PG8_TRIP_SP2(PG8_WAIT_V(8), PG8_MMA) }
	s_waitcnt lgkmcnt(0)
	v_mfma_f32_16x16x32_bf16 v[140:143], v[120:123], v[180:183], v[140:143]
	v_mfma_f32_16x16x32_bf16 v[136:139], v[144:147], v[180:183], v[136:139]
	v_mfma_f32_16x16x32_bf16 v[112:115], v[120:123], v[188:191], v[112:115]
	v_mfma_f32_16x16x32_bf16 v[108:111], v[144:147], v[188:191], v[108:111]
	v_mfma_f32_16x16x32_bf16 v[96:99], v[120:123], v[196:199], v[96:99]
	v_mfma_f32_16x16x32_bf16 v[92:95], v[144:147], v[196:199], v[92:95]
	v_mfma_f32_16x16x32_bf16 v[80:83], v[120:123], v[204:207], v[80:83]
	v_mfma_f32_16x16x32_bf16 v[76:79], v[144:147], v[204:207], v[76:79]
	v_mfma_f32_16x16x32_bf16 v[140:143], v[132:135], v[184:187], v[140:143]
	v_mfma_f32_16x16x32_bf16 v[136:139], v[148:151], v[184:187], v[136:139]
	v_mfma_f32_16x16x32_bf16 v[112:115], v[132:135], v[192:195], v[112:115]
	v_mfma_f32_16x16x32_bf16 v[108:111], v[148:151], v[192:195], v[108:111]
	v_mfma_f32_16x16x32_bf16 v[96:99], v[132:135], v[200:203], v[96:99]
	v_mfma_f32_16x16x32_bf16 v[92:95], v[148:151], v[200:203], v[92:95]
	v_mfma_f32_16x16x32_bf16 v[80:83], v[132:135], v[214:217], v[80:83]
	v_mfma_f32_16x16x32_bf16 v[76:79], v[148:151], v[214:217], v[76:79]
	v_mfma_f32_16x16x32_bf16 v[128:131], v[152:155], v[180:183], v[128:131]
	v_mfma_f32_16x16x32_bf16 v[124:127], v[166:169], v[180:183], v[124:127]
	v_mfma_f32_16x16x32_bf16 v[104:107], v[152:155], v[188:191], v[104:107]
	v_mfma_f32_16x16x32_bf16 v[100:103], v[166:169], v[188:191], v[100:103]
	v_mfma_f32_16x16x32_bf16 v[88:91], v[152:155], v[196:199], v[88:91]
	v_mfma_f32_16x16x32_bf16 v[84:87], v[166:169], v[196:199], v[84:87]
	v_mfma_f32_16x16x32_bf16 v[72:75], v[152:155], v[204:207], v[72:75]
	v_mfma_f32_16x16x32_bf16 v[68:71], v[166:169], v[204:207], v[68:71]
	v_mfma_f32_16x16x32_bf16 v[128:131], v[156:159], v[184:187], v[128:131]
	v_mfma_f32_16x16x32_bf16 v[124:127], v[170:173], v[184:187], v[124:127]
	v_mfma_f32_16x16x32_bf16 v[104:107], v[156:159], v[192:195], v[104:107]
	v_mfma_f32_16x16x32_bf16 v[100:103], v[170:173], v[192:195], v[100:103]
	v_mfma_f32_16x16x32_bf16 v[88:91], v[156:159], v[200:203], v[88:91]
	v_mfma_f32_16x16x32_bf16 v[84:87], v[170:173], v[200:203], v[84:87]
	v_mfma_f32_16x16x32_bf16 v[72:75], v[156:159], v[214:217], v[72:75]
	v_mfma_f32_16x16x32_bf16 v[68:71], v[170:173], v[214:217], v[68:71]
	s_barrier
	s_mov_b32 m0, s33
	v_lshl_add_u64 v[208:209], s[50:51], 0, v[160:161]
	ds_read_b128 v[180:183], v178 offset:16384
	ds_read_b128 v[184:187], v178 offset:17408
	ds_read_b128 v[188:191], v178 offset:18432
	ds_read_b128 v[192:195], v178 offset:19456
	ds_read_b128 v[196:199], v178 offset:20480
	ds_read_b128 v[200:203], v178 offset:21504
	ds_read_b128 v[204:207], v178 offset:22528
	ds_read_b128 v[214:217], v178 offset:23552
	global_load_lds_dwordx4 v[208:209], off
	v_lshl_add_u64 v[218:219], v[208:209], 0, s[90:91]
	s_mov_b32 m0, s40
	s_nop 0
	global_load_lds_dwordx4 v[218:219], off
	v_lshl_add_u64 v[218:219], v[208:209], 0, s[52:53]
	s_mov_b32 m0, s41
	s_nop 0
	global_load_lds_dwordx4 v[218:219], off
	v_lshl_add_u64 v[218:219], v[208:209], 0, s[56:57]
	s_mov_b32 m0, s42
	s_nop 0
	global_load_lds_dwordx4 v[218:219], off
	v_lshl_add_u64 v[218:219], s[48:49], 0, v[162:163]
	s_mov_b32 m0, s29
	v_lshl_add_u64 v[220:221], v[218:219], 0, s[96:97]
	global_load_lds_dwordx4 v[218:219], off
	s_mov_b32 m0, s30
	s_nop 0
	global_load_lds_dwordx4 v[220:221], off
	s_waitcnt vmcnt(8)
	s_waitcnt lgkmcnt(0)
	s_barrier
	s_waitcnt lgkmcnt(0)
	v_mfma_f32_16x16x32_bf16 v[56:59], v[120:123], v[180:183], v[56:59]
	v_mfma_f32_16x16x32_bf16 v[52:55], v[144:147], v[180:183], v[52:55]
	v_mfma_f32_16x16x32_bf16 v[48:51], v[120:123], v[188:191], v[48:51]
	v_mfma_f32_16x16x32_bf16 v[44:47], v[144:147], v[188:191], v[44:47]
	v_mfma_f32_16x16x32_bf16 v[32:35], v[120:123], v[196:199], v[32:35]
	v_mfma_f32_16x16x32_bf16 v[28:31], v[144:147], v[196:199], v[28:31]
	v_mfma_f32_16x16x32_bf16 v[16:19], v[120:123], v[204:207], v[16:19]
	v_mfma_f32_16x16x32_bf16 v[12:15], v[144:147], v[204:207], v[12:15]
	v_mfma_f32_16x16x32_bf16 v[56:59], v[132:135], v[184:187], v[56:59]
	v_mfma_f32_16x16x32_bf16 v[52:55], v[148:151], v[184:187], v[52:55]
	v_mfma_f32_16x16x32_bf16 v[48:51], v[132:135], v[192:195], v[48:51]
	v_mfma_f32_16x16x32_bf16 v[44:47], v[148:151], v[192:195], v[44:47]
	v_mfma_f32_16x16x32_bf16 v[32:35], v[132:135], v[200:203], v[32:35]
	v_mfma_f32_16x16x32_bf16 v[28:31], v[148:151], v[200:203], v[28:31]
	v_mfma_f32_16x16x32_bf16 v[16:19], v[132:135], v[214:217], v[16:19]
	v_mfma_f32_16x16x32_bf16 v[12:15], v[148:151], v[214:217], v[12:15]
	v_mfma_f32_16x16x32_bf16 v[64:67], v[152:155], v[180:183], v[64:67]
	v_mfma_f32_16x16x32_bf16 v[60:63], v[166:169], v[180:183], v[60:63]
	v_mfma_f32_16x16x32_bf16 v[40:43], v[152:155], v[188:191], v[40:43]
	v_mfma_f32_16x16x32_bf16 v[36:39], v[166:169], v[188:191], v[36:39]
	v_mfma_f32_16x16x32_bf16 v[24:27], v[152:155], v[196:199], v[24:27]
	v_mfma_f32_16x16x32_bf16 v[20:23], v[166:169], v[196:199], v[20:23]
	v_mfma_f32_16x16x32_bf16 v[8:11], v[152:155], v[204:207], v[8:11]
	v_mfma_f32_16x16x32_bf16 v[4:7], v[166:169], v[204:207], v[4:7]
	v_mfma_f32_16x16x32_bf16 v[64:67], v[156:159], v[184:187], v[64:67]
	v_mfma_f32_16x16x32_bf16 v[60:63], v[170:173], v[184:187], v[60:63]
	v_mfma_f32_16x16x32_bf16 v[40:43], v[156:159], v[192:195], v[40:43]
	v_mfma_f32_16x16x32_bf16 v[36:39], v[170:173], v[192:195], v[36:39]
	v_mfma_f32_16x16x32_bf16 v[24:27], v[156:159], v[200:203], v[24:27]
	v_mfma_f32_16x16x32_bf16 v[20:23], v[170:173], v[200:203], v[20:23]
	v_mfma_f32_16x16x32_bf16 v[8:11], v[156:159], v[214:217], v[8:11]
	v_mfma_f32_16x16x32_bf16 v[4:7], v[170:173], v[214:217], v[4:7]
	s_barrier
; #define PG8_MMA(ai, bj, At, Bt) do { __builtin_amdgcn_s_setprio(1); _Pragma("unroll") for (int m = 0; m < 4; ++m) _Pragma("unroll") for (int n = 0; n < 2; ++n) _Pragma("unroll") for (int k = 0; k < 2; ++k) \
;         acc[ai][bj][m][n] = __builtin_amdgcn_mfma_f32_16x16x32_bf16(Bt[n][k], At[m][k], acc[ai][bj][m][n], 0, 0, 0); __builtin_amdgcn_s_setprio(0); } while (0)
; #define PG8_WAIT_V(n) asm volatile("s_waitcnt vmcnt(" #n ")" ::: "memory")
; #define PG8_BAR __builtin_amdgcn_s_barrier()
; #define PG8_TRIP_HEAD(T) const int t = (T); const bool last = (t == nt - 2); \
;             const char* a1 = cA + (size_t)(t + 1) * kstep; \
;             const char* a2 = last ? nA : cA + (size_t)(t + 2) * kstep; const char* b2 = last ? nB : cB + (size_t)(t + 2) * kstep; \
;             const char* a3 = a2 + kstep; const char* b3 = b2 + kstep; \
;             if (last && has_next) S.a_ready(nxt);
; template <class Epi, class Sched, bool ALIGN_EPI = false, bool SP2 = false>
; __device__ __forceinline__ void gemm_phase(PG8_LAS unsigned char* lds, const Gemm g, const Sched& S, const Epi& E) {
;     ...
;         if constexpr (SP2) {
;             { PG8_TRIP_HEAD(0) PG8_TRIP_SP2(asm volatile("s_waitcnt vmcnt(%0)" :: "n"(8 + Epi::NST) : "memory"), PG8_MMAZ) }
;             for (int tt = 2; tt < nt; tt += 2) { PG8_TRIP_HEAD(tt) PG8_TRIP_SP2(PG8_WAIT_V(8), PG8_MMA) }
;     ...
;         if constexpr (ALIGN_EPI) { if (wr == 0) PG8_BAR; }
	ds_read_b128 v[120:123], v118
	ds_read_b128 v[132:135], v118 offset:1024
	ds_read_b128 v[144:147], v118 offset:2048
	ds_read_b128 v[148:151], v118 offset:3072
	ds_read_b128 v[152:155], v119
	ds_read_b128 v[156:159], v119 offset:1024
	ds_read_b128 v[166:169], v119 offset:2048
	ds_read_b128 v[170:173], v119 offset:3072
	s_mov_b32 m0, s31
	v_lshl_add_u64 v[220:221], v[218:219], 0, s[82:83]
	ds_read_b128 v[180:183], v178 offset:32768
	ds_read_b128 v[184:187], v178 offset:33792
	ds_read_b128 v[188:191], v178 offset:34816
	ds_read_b128 v[192:195], v178 offset:35840
	ds_read_b128 v[196:199], v178 offset:36864
	ds_read_b128 v[200:203], v178 offset:37888
	ds_read_b128 v[204:207], v178 offset:38912
	ds_read_b128 v[214:217], v178 offset:39936
	global_load_lds_dwordx4 v[220:221], off
	v_lshl_add_u64 v[220:221], v[218:219], 0, s[62:63]
	s_mov_b32 m0, s34
	s_nop 0
	global_load_lds_dwordx4 v[220:221], off
	s_waitcnt vmcnt(8)
	s_waitcnt lgkmcnt(0)
	s_barrier
	s_waitcnt lgkmcnt(0)
	v_mfma_f32_16x16x32_bf16 v[140:143], v[120:123], v[180:183], v[140:143]
	v_mfma_f32_16x16x32_bf16 v[136:139], v[144:147], v[180:183], v[136:139]
	v_mfma_f32_16x16x32_bf16 v[112:115], v[120:123], v[188:191], v[112:115]
	v_mfma_f32_16x16x32_bf16 v[108:111], v[144:147], v[188:191], v[108:111]
	v_mfma_f32_16x16x32_bf16 v[96:99], v[120:123], v[196:199], v[96:99]
	v_mfma_f32_16x16x32_bf16 v[92:95], v[144:147], v[196:199], v[92:95]
	v_mfma_f32_16x16x32_bf16 v[80:83], v[120:123], v[204:207], v[80:83]
	v_mfma_f32_16x16x32_bf16 v[76:79], v[144:147], v[204:207], v[76:79]
	v_mfma_f32_16x16x32_bf16 v[140:143], v[132:135], v[184:187], v[140:143]
	v_mfma_f32_16x16x32_bf16 v[136:139], v[148:151], v[184:187], v[136:139]
	v_mfma_f32_16x16x32_bf16 v[112:115], v[132:135], v[192:195], v[112:115]
	v_mfma_f32_16x16x32_bf16 v[108:111], v[148:151], v[192:195], v[108:111]
	v_mfma_f32_16x16x32_bf16 v[96:99], v[132:135], v[200:203], v[96:99]
	v_mfma_f32_16x16x32_bf16 v[92:95], v[148:151], v[200:203], v[92:95]
	v_mfma_f32_16x16x32_bf16 v[80:83], v[132:135], v[214:217], v[80:83]
	v_mfma_f32_16x16x32_bf16 v[76:79], v[148:151], v[214:217], v[76:79]
	v_mfma_f32_16x16x32_bf16 v[128:131], v[152:155], v[180:183], v[128:131]
	v_mfma_f32_16x16x32_bf16 v[124:127], v[166:169], v[180:183], v[124:127]
	v_mfma_f32_16x16x32_bf16 v[104:107], v[152:155], v[188:191], v[104:107]
	v_mfma_f32_16x16x32_bf16 v[100:103], v[166:169], v[188:191], v[100:103]
	v_mfma_f32_16x16x32_bf16 v[88:91], v[152:155], v[196:199], v[88:91]
	v_mfma_f32_16x16x32_bf16 v[84:87], v[166:169], v[196:199], v[84:87]
	v_mfma_f32_16x16x32_bf16 v[72:75], v[152:155], v[204:207], v[72:75]
	v_mfma_f32_16x16x32_bf16 v[68:71], v[166:169], v[204:207], v[68:71]
	v_mfma_f32_16x16x32_bf16 v[128:131], v[156:159], v[184:187], v[128:131]
	v_mfma_f32_16x16x32_bf16 v[124:127], v[170:173], v[184:187], v[124:127]
	v_mfma_f32_16x16x32_bf16 v[104:107], v[156:159], v[192:195], v[104:107]
	v_mfma_f32_16x16x32_bf16 v[100:103], v[170:173], v[192:195], v[100:103]
	v_mfma_f32_16x16x32_bf16 v[88:91], v[156:159], v[200:203], v[88:91]
	v_mfma_f32_16x16x32_bf16 v[84:87], v[170:173], v[200:203], v[84:87]
	v_mfma_f32_16x16x32_bf16 v[72:75], v[156:159], v[214:217], v[72:75]
	v_mfma_f32_16x16x32_bf16 v[68:71], v[170:173], v[214:217], v[68:71]
	s_barrier
	s_mov_b32 m0, s43
	v_lshl_add_u64 v[220:221], v[208:209], 0, s[78:79]
	ds_read_b128 v[180:183], v178 offset:49152
	ds_read_b128 v[184:187], v178 offset:50176
	ds_read_b128 v[188:191], v178 offset:51200
	ds_read_b128 v[192:195], v178 offset:52224
	ds_read_b128 v[196:199], v178 offset:53248
	ds_read_b128 v[200:203], v178 offset:54272
	ds_read_b128 v[204:207], v178 offset:55296
	ds_read_b128 v[214:217], v178 offset:56320
	global_load_lds_dwordx4 v[220:221], off
	v_lshl_add_u64 v[220:221], v[208:209], 0, s[84:85]
	s_mov_b32 m0, s44
	s_nop 0
	global_load_lds_dwordx4 v[220:221], off
	v_lshl_add_u64 v[220:221], v[208:209], 0, s[54:55]
	s_mov_b32 m0, s45
	v_lshl_add_u64 v[208:209], v[208:209], 0, s[60:61]
	global_load_lds_dwordx4 v[220:221], off
	s_mov_b32 m0, s46
	s_nop 0
	global_load_lds_dwordx4 v[208:209], off
	v_lshl_add_u64 v[208:209], v[218:219], 0, s[78:79]
	s_mov_b32 m0, s36
	s_nop 0
	global_load_lds_dwordx4 v[208:209], off
	v_lshl_add_u64 v[208:209], v[218:219], 0, s[92:93]
	s_mov_b32 m0, s37
	s_nop 0
	global_load_lds_dwordx4 v[208:209], off
	s_waitcnt vmcnt(8)
	s_waitcnt lgkmcnt(0)
	s_barrier
	s_waitcnt lgkmcnt(0)
	v_mfma_f32_16x16x32_bf16 v[56:59], v[120:123], v[180:183], v[56:59]
	v_mfma_f32_16x16x32_bf16 v[52:55], v[144:147], v[180:183], v[52:55]
	v_mfma_f32_16x16x32_bf16 v[48:51], v[120:123], v[188:191], v[48:51]
	v_mfma_f32_16x16x32_bf16 v[44:47], v[144:147], v[188:191], v[44:47]
	v_mfma_f32_16x16x32_bf16 v[32:35], v[120:123], v[196:199], v[32:35]
	v_mfma_f32_16x16x32_bf16 v[28:31], v[144:147], v[196:199], v[28:31]
	v_mfma_f32_16x16x32_bf16 v[16:19], v[120:123], v[204:207], v[16:19]
	v_mfma_f32_16x16x32_bf16 v[12:15], v[144:147], v[204:207], v[12:15]
	v_mfma_f32_16x16x32_bf16 v[56:59], v[132:135], v[184:187], v[56:59]
	v_mfma_f32_16x16x32_bf16 v[52:55], v[148:151], v[184:187], v[52:55]
	v_mfma_f32_16x16x32_bf16 v[48:51], v[132:135], v[192:195], v[48:51]
	v_mfma_f32_16x16x32_bf16 v[44:47], v[148:151], v[192:195], v[44:47]
	v_mfma_f32_16x16x32_bf16 v[32:35], v[132:135], v[200:203], v[32:35]
	v_mfma_f32_16x16x32_bf16 v[28:31], v[148:151], v[200:203], v[28:31]
	v_mfma_f32_16x16x32_bf16 v[16:19], v[132:135], v[214:217], v[16:19]
	v_mfma_f32_16x16x32_bf16 v[12:15], v[148:151], v[214:217], v[12:15]
	v_mfma_f32_16x16x32_bf16 v[64:67], v[152:155], v[180:183], v[64:67]
	v_mfma_f32_16x16x32_bf16 v[60:63], v[166:169], v[180:183], v[60:63]
	v_mfma_f32_16x16x32_bf16 v[40:43], v[152:155], v[188:191], v[40:43]
	v_mfma_f32_16x16x32_bf16 v[36:39], v[166:169], v[188:191], v[36:39]
	v_mfma_f32_16x16x32_bf16 v[24:27], v[152:155], v[196:199], v[24:27]
	v_mfma_f32_16x16x32_bf16 v[20:23], v[166:169], v[196:199], v[20:23]
	v_mfma_f32_16x16x32_bf16 v[8:11], v[152:155], v[204:207], v[8:11]
	v_mfma_f32_16x16x32_bf16 v[4:7], v[166:169], v[204:207], v[4:7]
	v_mfma_f32_16x16x32_bf16 v[64:67], v[156:159], v[184:187], v[64:67]
	v_mfma_f32_16x16x32_bf16 v[60:63], v[170:173], v[184:187], v[60:63]
	v_mfma_f32_16x16x32_bf16 v[40:43], v[156:159], v[192:195], v[40:43]
	v_mfma_f32_16x16x32_bf16 v[36:39], v[170:173], v[192:195], v[36:39]
	v_mfma_f32_16x16x32_bf16 v[24:27], v[156:159], v[200:203], v[24:27]
	v_mfma_f32_16x16x32_bf16 v[20:23], v[170:173], v[200:203], v[20:23]
	v_mfma_f32_16x16x32_bf16 v[8:11], v[156:159], v[214:217], v[8:11]
	v_mfma_f32_16x16x32_bf16 v[4:7], v[170:173], v[214:217], v[4:7]
	s_barrier
	s_add_i32 s26, s26, 2
	s_add_u32 s10, s10, 0x100
	s_addc_u32 s11, s11, 0
	s_add_u32 s24, s24, 0x100
	s_addc_u32 s25, s25, 0
	s_cmp_gt_u32 s26, 29
	s_cbranch_scc0 .LBB0_700
	s_and_b64 vcc, exec, s[16:17]
	s_cbranch_vccz .LBB0_703
	s_barrier

; #define PG8_WAIT_V(n) asm volatile("s_waitcnt vmcnt(" #n ")" ::: "memory")
; #define PG8_BAR __builtin_amdgcn_s_barrier()
; __device__ __forceinline__ unsigned xb_xcc_id() { return (unsigned)__builtin_amdgcn_s_getreg((3 << 11) | 20) & 0xFu; }
; template <class Epi, class Sched, bool ALIGN_EPI = false, bool SP2 = false>
; __device__ __forceinline__ void gemm_phase(PG8_LAS unsigned char* lds, const Gemm g, const Sched& S, const Epi& E) {
;     ...
;     PG8_WAIT_V(0);
;     if constexpr (!ALIGN_EPI) { if (wr == 0) PG8_BAR; }
;     PG8_BAR;
; __device__ __forceinline__ void xcd_barrier(const XcdBarrier& b) {
;     asm volatile("s_waitcnt vmcnt(0)" ::: "memory");
;     __syncthreads();
;     if (threadIdx.x == 0) {
;         unsigned* bar = b.bar; const unsigned bx_ = xb_xcc_id();
.LBB0_723:
	s_setprio 0
	s_waitcnt vmcnt(0)
	s_barrier
	s_mov_b64 s[6:7], exec
	v_readlane_b32 s2, v252, 15
	v_readlane_b32 s3, v252, 16
	s_and_b64 s[2:3], s[6:7], s[2:3]
	s_mov_b64 exec, s[2:3]
	s_cbranch_execnz .LBB0_724
	s_getpc_b64 s[98:99]
